# v6 plus hand-written norm1 phases (all three modes)
# speedup vs baseline: 1.0468x; 1.0038x over previous
.LBB0_2828:
	s_andn2_b64 vcc, exec, s[0:1]
	s_xor_b64 s[0:1], s[36:37], -1
	v_writelane_b32 v255, s0, 23
	s_nop 1
	v_writelane_b32 v255, s1, 24
	s_cbranch_vccnz .LBB0_2918
	v_readlane_b32 s2, v255, 23
	v_readlane_b32 s3, v255, 24
	s_mov_b64 s[0:1], -1
	s_and_b64 vcc, exec, s[2:3]
	s_cbranch_vccz .LBB0_2858
	v_readlane_b32 s4, v251, 59
	v_readlane_b32 s5, v251, 60
	v_readlane_b32 s8, v255, 20
	v_readlane_b32 s10, v251, 61
	v_readfirstlane_b32 s0, v0
	v_readlane_b32 s56, v251, 53
	v_readlane_b32 s57, v251, 54
	s_nop 3
	s_lshr_b32 s0, s0, 6
	s_add_i32 s10, s10, s0
	s_lshl_b32 s1, s8, 13
	s_add_u32 s56, s56, s1
	s_addc_u32 s57, s57, 0
	s_add_u32 s58, s56, 0x1000
	s_addc_u32 s59, s57, 0
	s_add_u32 s50, s4, 0x3cc90000
	s_addc_u32 s51, s5, 0
	s_mul_i32 s1, s8, 0x6c000
	s_add_i32 s1, s1, 0x10000
	s_add_u32 s52, s4, s1
	s_addc_u32 s53, s5, 0
	s_add_i32 s1, s8, -1
	s_mul_i32 s1, s1, 0x6c000
	s_add_i32 s1, s1, 0x10000
	s_add_u32 s54, s4, s1
	s_addc_u32 s55, s5, 0
	s_add_u32 s48, s4, 0x33c90000
	s_addc_u32 s49, s5, 0
	s_add_u32 s62, s4, 0x4f0000
	s_addc_u32 s63, s5, 0
	s_add_u32 s64, s4, 0x57c90000
	s_addc_u32 s65, s5, 0
	v_and_b32_e32 v238, 63, v0
	v_lshlrev_b32_e32 v1, 4, v238
	v_lshlrev_b32_e32 v2, 3, v238
	v_lshlrev_b32_e32 v246, 2, v238
	s_add_i32 s11, s10, 0x0
	s_lshr_b32 s0, s11, 8
	s_mul_i32 s0, s0, 57
	s_lshr_b32 s44, s0, 9
	s_mul_i32 s1, s44, 0x900
	s_sub_i32 s43, s11, s1
	s_lshl_b32 s1, s11, 6
	s_add_u32 s78, s62, s1
	s_addc_u32 s79, s63, 0
	global_load_dword v234, v246, s[78:79]
	s_lshl_b32 s1, s11, 13
	s_add_u32 s12, s48, s1
	s_addc_u32 s13, s49, 0
	s_add_u32 s14, s12, 0x1000
	s_addc_u32 s15, s13, 0
	global_load_dwordx4 v[4:7], v1, s[12:13]
	global_load_dwordx4 v[8:11], v1, s[12:13] offset:1024
	global_load_dwordx4 v[12:15], v1, s[12:13] offset:2048
	global_load_dwordx4 v[16:19], v1, s[12:13] offset:3072
	global_load_dwordx4 v[20:23], v1, s[14:15]
	global_load_dwordx4 v[24:27], v1, s[14:15] offset:1024
	global_load_dwordx4 v[28:31], v1, s[14:15] offset:2048
	global_load_dwordx4 v[32:35], v1, s[14:15] offset:3072
	s_add_i32 s11, s10, 0x0
	s_lshr_b32 s0, s11, 8
	s_mul_i32 s0, s0, 57
	s_lshr_b32 s44, s0, 9
	s_mul_i32 s1, s44, 0x900
	s_sub_i32 s43, s11, s1
	s_lshl_b32 s1, s11, 13
	s_add_u32 s16, s48, s1
	s_addc_u32 s17, s49, 0
	s_add_u32 s18, s16, 0x1000
	s_addc_u32 s19, s17, 0
	s_lshl_b32 s1, s11, 12
	s_add_u32 s22, s50, s1
	s_addc_u32 s23, s51, 0
	s_cmpk_lt_u32 s43, 0x100
	s_cselect_b32 s0, 8, s44
	s_mul_i32 s1, s0, 0xc000
	s_add_u32 s28, s52, s1
	s_addc_u32 s29, s53, 0
	s_add_u32 s30, s28, 0x1000
	s_addc_u32 s31, s29, 0
	s_add_u32 s72, s54, s1
	s_addc_u32 s73, s55, 0
	s_add_u32 s72, s72, 0xa000
	s_addc_u32 s73, s73, 0
	s_add_u32 s74, s72, 0x1000
	s_addc_u32 s75, s73, 0
	global_load_dwordx4 v[68:71], v1, s[72:73]
	global_load_dwordx4 v[100:103], v1, s[56:57]
	global_load_dwordx4 v[72:75], v1, s[72:73] offset:1024
	global_load_dwordx4 v[104:107], v1, s[56:57] offset:1024
	global_load_dwordx4 v[76:79], v1, s[72:73] offset:2048
	global_load_dwordx4 v[108:111], v1, s[56:57] offset:2048
	global_load_dwordx4 v[80:83], v1, s[72:73] offset:3072
	global_load_dwordx4 v[112:115], v1, s[56:57] offset:3072
	global_load_dwordx4 v[84:87], v1, s[74:75]
	global_load_dwordx4 v[116:119], v1, s[58:59]
	global_load_dwordx4 v[88:91], v1, s[74:75] offset:1024
	global_load_dwordx4 v[120:123], v1, s[58:59] offset:1024
	global_load_dwordx4 v[92:95], v1, s[74:75] offset:2048
	global_load_dwordx4 v[124:127], v1, s[58:59] offset:2048
	global_load_dwordx4 v[96:99], v1, s[74:75] offset:3072
	global_load_dwordx4 v[128:131], v1, s[58:59] offset:3072
	s_add_u32 s84, s28, 0x2000
	s_addc_u32 s85, s29, 0
	s_add_u32 s86, s28, 0x3000
	s_addc_u32 s87, s29, 0
	global_load_dwordx4 v[164:167], v1, s[28:29]
	global_load_dwordx4 v[132:135], v1, s[84:85]
	global_load_dwordx4 v[168:171], v1, s[28:29] offset:1024
	global_load_dwordx4 v[136:139], v1, s[84:85] offset:1024
	global_load_dwordx4 v[172:175], v1, s[28:29] offset:2048
	global_load_dwordx4 v[140:143], v1, s[84:85] offset:2048
	global_load_dwordx4 v[176:179], v1, s[28:29] offset:3072
	global_load_dwordx4 v[144:147], v1, s[84:85] offset:3072
	global_load_dwordx4 v[180:183], v1, s[30:31]
	global_load_dwordx4 v[148:151], v1, s[86:87]
	global_load_dwordx4 v[184:187], v1, s[30:31] offset:1024
	global_load_dwordx4 v[152:155], v1, s[86:87] offset:1024
	global_load_dwordx4 v[188:191], v1, s[30:31] offset:2048
	global_load_dwordx4 v[156:159], v1, s[86:87] offset:2048
	global_load_dwordx4 v[192:195], v1, s[30:31] offset:3072
	global_load_dwordx4 v[160:163], v1, s[86:87] offset:3072
	s_waitcnt vmcnt(40)
	v_cmp_le_i32_e64 s[0:1], 0, v234
	s_nop 1
	s_and_b32 s45, s0, 0xffff
	s_mov_b32 s47, 0
	s_mov_b32 s61, 0
	s_cmp_eq_u32 s45, 0
	s_cbranch_scc1 .Ln1_y0_0
	s_mov_b32 s47, 1
	s_ff1_i32_b32 s0, s45
	s_add_i32 s1, s45, -1
	s_and_b32 s45, s45, s1
	s_nop 0
	v_readlane_b32 s0, v234, s0
	s_nop 3
	s_lshl_b32 s0, s0, 12
	s_add_u32 s76, s64, s0
	s_addc_u32 s77, s65, 0
	global_load_dwordx2 v[196:197], v2, s[76:77]
	global_load_dwordx2 v[198:199], v2, s[76:77] offset:512
	global_load_dwordx2 v[200:201], v2, s[76:77] offset:1024
	global_load_dwordx2 v[202:203], v2, s[76:77] offset:1536
	global_load_dwordx2 v[204:205], v2, s[76:77] offset:2048
	global_load_dwordx2 v[206:207], v2, s[76:77] offset:2560
	global_load_dwordx2 v[208:209], v2, s[76:77] offset:3072
	global_load_dwordx2 v[210:211], v2, s[76:77] offset:3584
	s_cmp_eq_u32 s45, 0
	s_cbranch_scc1 .Ln1_y0_0
	s_mov_b32 s61, 1
	s_ff1_i32_b32 s0, s45
	s_add_i32 s1, s45, -1
	s_and_b32 s45, s45, s1
	s_nop 0
	v_readlane_b32 s0, v234, s0
	s_nop 3
	s_lshl_b32 s0, s0, 12
	s_add_u32 s76, s64, s0
	s_addc_u32 s77, s65, 0
	global_load_dwordx2 v[212:213], v2, s[76:77]
	global_load_dwordx2 v[214:215], v2, s[76:77] offset:512
	global_load_dwordx2 v[216:217], v2, s[76:77] offset:1024
	global_load_dwordx2 v[218:219], v2, s[76:77] offset:1536
	global_load_dwordx2 v[226:227], v2, s[76:77] offset:2048
	global_load_dwordx2 v[228:229], v2, s[76:77] offset:2560
	global_load_dwordx2 v[230:231], v2, s[76:77] offset:3072
	global_load_dwordx2 v[232:233], v2, s[76:77] offset:3584
.Ln1_y0_0:
	s_add_i32 s11, s10, 0x800
	s_lshr_b32 s0, s11, 8
	s_mul_i32 s0, s0, 57
	s_lshr_b32 s44, s0, 9
	s_mul_i32 s1, s44, 0x900
	s_sub_i32 s43, s11, s1
	s_lshl_b32 s1, s11, 6
	s_add_u32 s78, s62, s1
	s_addc_u32 s79, s63, 0
	global_load_dword v235, v246, s[78:79]
	s_lshl_b32 s1, s11, 13
	s_add_u32 s12, s48, s1
	s_addc_u32 s13, s49, 0
	s_add_u32 s14, s12, 0x1000
	s_addc_u32 s15, s13, 0
	global_load_dwordx4 v[36:39], v1, s[12:13]
	global_load_dwordx4 v[40:43], v1, s[12:13] offset:1024
	global_load_dwordx4 v[44:47], v1, s[12:13] offset:2048
	global_load_dwordx4 v[48:51], v1, s[12:13] offset:3072
	global_load_dwordx4 v[52:55], v1, s[14:15]
	global_load_dwordx4 v[56:59], v1, s[14:15] offset:1024
	global_load_dwordx4 v[60:63], v1, s[14:15] offset:2048
	global_load_dwordx4 v[64:67], v1, s[14:15] offset:3072
	s_waitcnt vmcnt(9)
	s_cmp_eq_u32 s47, 0
	s_cbranch_scc1 .Ln1_a1_0
	v_lshlrev_b32_e32 v238, 16, v196
	v_and_b32_e32 v239, 0xffff0000, v196
	v_fmac_f32_e32 v4, v68, v238
	v_fmac_f32_e32 v5, v69, v239
	v_lshlrev_b32_e32 v238, 16, v197
	v_and_b32_e32 v239, 0xffff0000, v197
	v_fmac_f32_e32 v6, v70, v238
	v_fmac_f32_e32 v7, v71, v239
	v_lshlrev_b32_e32 v238, 16, v198
	v_and_b32_e32 v239, 0xffff0000, v198
	v_fmac_f32_e32 v8, v72, v238
	v_fmac_f32_e32 v9, v73, v239
	v_lshlrev_b32_e32 v238, 16, v199
	v_and_b32_e32 v239, 0xffff0000, v199
	v_fmac_f32_e32 v10, v74, v238
	v_fmac_f32_e32 v11, v75, v239
	v_lshlrev_b32_e32 v238, 16, v200
	v_and_b32_e32 v239, 0xffff0000, v200
	v_fmac_f32_e32 v12, v76, v238
	v_fmac_f32_e32 v13, v77, v239
	v_lshlrev_b32_e32 v238, 16, v201
	v_and_b32_e32 v239, 0xffff0000, v201
	v_fmac_f32_e32 v14, v78, v238
	v_fmac_f32_e32 v15, v79, v239
	v_lshlrev_b32_e32 v238, 16, v202
	v_and_b32_e32 v239, 0xffff0000, v202
	v_fmac_f32_e32 v16, v80, v238
	v_fmac_f32_e32 v17, v81, v239
	v_lshlrev_b32_e32 v238, 16, v203
	v_and_b32_e32 v239, 0xffff0000, v203
	v_fmac_f32_e32 v18, v82, v238
	v_fmac_f32_e32 v19, v83, v239
	v_lshlrev_b32_e32 v238, 16, v204
	v_and_b32_e32 v239, 0xffff0000, v204
	v_fmac_f32_e32 v20, v84, v238
	v_fmac_f32_e32 v21, v85, v239
	v_lshlrev_b32_e32 v238, 16, v205
	v_and_b32_e32 v239, 0xffff0000, v205
	v_fmac_f32_e32 v22, v86, v238
	v_fmac_f32_e32 v23, v87, v239
	v_lshlrev_b32_e32 v238, 16, v206
	v_and_b32_e32 v239, 0xffff0000, v206
	v_fmac_f32_e32 v24, v88, v238
	v_fmac_f32_e32 v25, v89, v239
	v_lshlrev_b32_e32 v238, 16, v207
	v_and_b32_e32 v239, 0xffff0000, v207
	v_fmac_f32_e32 v26, v90, v238
	v_fmac_f32_e32 v27, v91, v239
	v_lshlrev_b32_e32 v238, 16, v208
	v_and_b32_e32 v239, 0xffff0000, v208
	v_fmac_f32_e32 v28, v92, v238
	v_fmac_f32_e32 v29, v93, v239
	v_lshlrev_b32_e32 v238, 16, v209
	v_and_b32_e32 v239, 0xffff0000, v209
	v_fmac_f32_e32 v30, v94, v238
	v_fmac_f32_e32 v31, v95, v239
	v_lshlrev_b32_e32 v238, 16, v210
	v_and_b32_e32 v239, 0xffff0000, v210
	v_fmac_f32_e32 v32, v96, v238
	v_fmac_f32_e32 v33, v97, v239
	v_lshlrev_b32_e32 v238, 16, v211
	v_and_b32_e32 v239, 0xffff0000, v211
	v_fmac_f32_e32 v34, v98, v238
	v_fmac_f32_e32 v35, v99, v239
.Ln1_a1_0:
	s_cmp_eq_u32 s61, 0
	s_cbranch_scc1 .Ln1_a2_0
	v_lshlrev_b32_e32 v238, 16, v212
	v_and_b32_e32 v239, 0xffff0000, v212
	v_fmac_f32_e32 v4, v68, v238
	v_fmac_f32_e32 v5, v69, v239
	v_lshlrev_b32_e32 v238, 16, v213
	v_and_b32_e32 v239, 0xffff0000, v213
	v_fmac_f32_e32 v6, v70, v238
	v_fmac_f32_e32 v7, v71, v239
	v_lshlrev_b32_e32 v238, 16, v214
	v_and_b32_e32 v239, 0xffff0000, v214
	v_fmac_f32_e32 v8, v72, v238
	v_fmac_f32_e32 v9, v73, v239
	v_lshlrev_b32_e32 v238, 16, v215
	v_and_b32_e32 v239, 0xffff0000, v215
	v_fmac_f32_e32 v10, v74, v238
	v_fmac_f32_e32 v11, v75, v239
	v_lshlrev_b32_e32 v238, 16, v216
	v_and_b32_e32 v239, 0xffff0000, v216
	v_fmac_f32_e32 v12, v76, v238
	v_fmac_f32_e32 v13, v77, v239
	v_lshlrev_b32_e32 v238, 16, v217
	v_and_b32_e32 v239, 0xffff0000, v217
	v_fmac_f32_e32 v14, v78, v238
	v_fmac_f32_e32 v15, v79, v239
	v_lshlrev_b32_e32 v238, 16, v218
	v_and_b32_e32 v239, 0xffff0000, v218
	v_fmac_f32_e32 v16, v80, v238
	v_fmac_f32_e32 v17, v81, v239
	v_lshlrev_b32_e32 v238, 16, v219
	v_and_b32_e32 v239, 0xffff0000, v219
	v_fmac_f32_e32 v18, v82, v238
	v_fmac_f32_e32 v19, v83, v239
	v_lshlrev_b32_e32 v238, 16, v226
	v_and_b32_e32 v239, 0xffff0000, v226
	v_fmac_f32_e32 v20, v84, v238
	v_fmac_f32_e32 v21, v85, v239
	v_lshlrev_b32_e32 v238, 16, v227
	v_and_b32_e32 v239, 0xffff0000, v227
	v_fmac_f32_e32 v22, v86, v238
	v_fmac_f32_e32 v23, v87, v239
	v_lshlrev_b32_e32 v238, 16, v228
	v_and_b32_e32 v239, 0xffff0000, v228
	v_fmac_f32_e32 v24, v88, v238
	v_fmac_f32_e32 v25, v89, v239
	v_lshlrev_b32_e32 v238, 16, v229
	v_and_b32_e32 v239, 0xffff0000, v229
	v_fmac_f32_e32 v26, v90, v238
	v_fmac_f32_e32 v27, v91, v239
	v_lshlrev_b32_e32 v238, 16, v230
	v_and_b32_e32 v239, 0xffff0000, v230
	v_fmac_f32_e32 v28, v92, v238
	v_fmac_f32_e32 v29, v93, v239
	v_lshlrev_b32_e32 v238, 16, v231
	v_and_b32_e32 v239, 0xffff0000, v231
	v_fmac_f32_e32 v30, v94, v238
	v_fmac_f32_e32 v31, v95, v239
	v_lshlrev_b32_e32 v238, 16, v232
	v_and_b32_e32 v239, 0xffff0000, v232
	v_fmac_f32_e32 v32, v96, v238
	v_fmac_f32_e32 v33, v97, v239
	v_lshlrev_b32_e32 v238, 16, v233
	v_and_b32_e32 v239, 0xffff0000, v233
	v_fmac_f32_e32 v34, v98, v238
	v_fmac_f32_e32 v35, v99, v239
.Ln1_a2_0:
.Ln1_more_0:
	s_cmp_eq_u32 s45, 0
	s_cbranch_scc1 .Ln1_gd_0
	s_ff1_i32_b32 s0, s45
	s_add_i32 s1, s45, -1
	s_and_b32 s45, s45, s1
	s_nop 0
	v_readlane_b32 s0, v234, s0
	s_nop 3
	s_lshl_b32 s0, s0, 12
	s_add_u32 s76, s64, s0
	s_addc_u32 s77, s65, 0
	global_load_dwordx2 v[196:197], v2, s[76:77]
	global_load_dwordx2 v[198:199], v2, s[76:77] offset:512
	global_load_dwordx2 v[200:201], v2, s[76:77] offset:1024
	global_load_dwordx2 v[202:203], v2, s[76:77] offset:1536
	global_load_dwordx2 v[204:205], v2, s[76:77] offset:2048
	global_load_dwordx2 v[206:207], v2, s[76:77] offset:2560
	global_load_dwordx2 v[208:209], v2, s[76:77] offset:3072
	global_load_dwordx2 v[210:211], v2, s[76:77] offset:3584
	s_waitcnt vmcnt(0)
	v_lshlrev_b32_e32 v238, 16, v196
	v_and_b32_e32 v239, 0xffff0000, v196
	v_fmac_f32_e32 v4, v68, v238
	v_fmac_f32_e32 v5, v69, v239
	v_lshlrev_b32_e32 v238, 16, v197
	v_and_b32_e32 v239, 0xffff0000, v197
	v_fmac_f32_e32 v6, v70, v238
	v_fmac_f32_e32 v7, v71, v239
	v_lshlrev_b32_e32 v238, 16, v198
	v_and_b32_e32 v239, 0xffff0000, v198
	v_fmac_f32_e32 v8, v72, v238
	v_fmac_f32_e32 v9, v73, v239
	v_lshlrev_b32_e32 v238, 16, v199
	v_and_b32_e32 v239, 0xffff0000, v199
	v_fmac_f32_e32 v10, v74, v238
	v_fmac_f32_e32 v11, v75, v239
	v_lshlrev_b32_e32 v238, 16, v200
	v_and_b32_e32 v239, 0xffff0000, v200
	v_fmac_f32_e32 v12, v76, v238
	v_fmac_f32_e32 v13, v77, v239
	v_lshlrev_b32_e32 v238, 16, v201
	v_and_b32_e32 v239, 0xffff0000, v201
	v_fmac_f32_e32 v14, v78, v238
	v_fmac_f32_e32 v15, v79, v239
	v_lshlrev_b32_e32 v238, 16, v202
	v_and_b32_e32 v239, 0xffff0000, v202
	v_fmac_f32_e32 v16, v80, v238
	v_fmac_f32_e32 v17, v81, v239
	v_lshlrev_b32_e32 v238, 16, v203
	v_and_b32_e32 v239, 0xffff0000, v203
	v_fmac_f32_e32 v18, v82, v238
	v_fmac_f32_e32 v19, v83, v239
	v_lshlrev_b32_e32 v238, 16, v204
	v_and_b32_e32 v239, 0xffff0000, v204
	v_fmac_f32_e32 v20, v84, v238
	v_fmac_f32_e32 v21, v85, v239
	v_lshlrev_b32_e32 v238, 16, v205
	v_and_b32_e32 v239, 0xffff0000, v205
	v_fmac_f32_e32 v22, v86, v238
	v_fmac_f32_e32 v23, v87, v239
	v_lshlrev_b32_e32 v238, 16, v206
	v_and_b32_e32 v239, 0xffff0000, v206
	v_fmac_f32_e32 v24, v88, v238
	v_fmac_f32_e32 v25, v89, v239
	v_lshlrev_b32_e32 v238, 16, v207
	v_and_b32_e32 v239, 0xffff0000, v207
	v_fmac_f32_e32 v26, v90, v238
	v_fmac_f32_e32 v27, v91, v239
	v_lshlrev_b32_e32 v238, 16, v208
	v_and_b32_e32 v239, 0xffff0000, v208
	v_fmac_f32_e32 v28, v92, v238
	v_fmac_f32_e32 v29, v93, v239
	v_lshlrev_b32_e32 v238, 16, v209
	v_and_b32_e32 v239, 0xffff0000, v209
	v_fmac_f32_e32 v30, v94, v238
	v_fmac_f32_e32 v31, v95, v239
	v_lshlrev_b32_e32 v238, 16, v210
	v_and_b32_e32 v239, 0xffff0000, v210
	v_fmac_f32_e32 v32, v96, v238
	v_fmac_f32_e32 v33, v97, v239
	v_lshlrev_b32_e32 v238, 16, v211
	v_and_b32_e32 v239, 0xffff0000, v211
	v_fmac_f32_e32 v34, v98, v238
	v_fmac_f32_e32 v35, v99, v239
	s_branch .Ln1_more_0
.Ln1_gd_0:
	global_store_dwordx4 v1, v[4:7], s[16:17]
	global_store_dwordx4 v1, v[8:11], s[16:17] offset:1024
	global_store_dwordx4 v1, v[12:15], s[16:17] offset:2048
	global_store_dwordx4 v1, v[16:19], s[16:17] offset:3072
	global_store_dwordx4 v1, v[20:23], s[18:19]
	global_store_dwordx4 v1, v[24:27], s[18:19] offset:1024
	global_store_dwordx4 v1, v[28:31], s[18:19] offset:2048
	global_store_dwordx4 v1, v[32:35], s[18:19] offset:3072
	v_mul_f32_e32 v236, v4, v4
	v_fmac_f32_e32 v236, v5, v5
	v_fmac_f32_e32 v236, v6, v6
	v_fmac_f32_e32 v236, v7, v7
	v_fmac_f32_e32 v236, v8, v8
	v_fmac_f32_e32 v236, v9, v9
	v_fmac_f32_e32 v236, v10, v10
	v_fmac_f32_e32 v236, v11, v11
	v_fmac_f32_e32 v236, v12, v12
	v_fmac_f32_e32 v236, v13, v13
	v_fmac_f32_e32 v236, v14, v14
	v_fmac_f32_e32 v236, v15, v15
	v_fmac_f32_e32 v236, v16, v16
	v_fmac_f32_e32 v236, v17, v17
	v_fmac_f32_e32 v236, v18, v18
	v_fmac_f32_e32 v236, v19, v19
	v_fmac_f32_e32 v236, v20, v20
	v_fmac_f32_e32 v236, v21, v21
	v_fmac_f32_e32 v236, v22, v22
	v_fmac_f32_e32 v236, v23, v23
	v_fmac_f32_e32 v236, v24, v24
	v_fmac_f32_e32 v236, v25, v25
	v_fmac_f32_e32 v236, v26, v26
	v_fmac_f32_e32 v236, v27, v27
	v_fmac_f32_e32 v236, v28, v28
	v_fmac_f32_e32 v236, v29, v29
	v_fmac_f32_e32 v236, v30, v30
	v_fmac_f32_e32 v236, v31, v31
	v_fmac_f32_e32 v236, v32, v32
	v_fmac_f32_e32 v236, v33, v33
	v_fmac_f32_e32 v236, v34, v34
	v_fmac_f32_e32 v236, v35, v35
	v_fma_f32 v100, v100, v132, v100
	v_fma_f32 v101, v101, v133, v101
	v_fma_f32 v102, v102, v134, v102
	v_fma_f32 v103, v103, v135, v103
	v_fma_f32 v104, v104, v136, v104
	v_fma_f32 v105, v105, v137, v105
	v_fma_f32 v106, v106, v138, v106
	v_fma_f32 v107, v107, v139, v107
	v_fma_f32 v108, v108, v140, v108
	v_fma_f32 v109, v109, v141, v109
	v_fma_f32 v110, v110, v142, v110
	v_fma_f32 v111, v111, v143, v111
	v_fma_f32 v112, v112, v144, v112
	v_fma_f32 v113, v113, v145, v113
	v_fma_f32 v114, v114, v146, v114
	v_fma_f32 v115, v115, v147, v115
	v_fma_f32 v116, v116, v148, v116
	v_fma_f32 v117, v117, v149, v117
	v_fma_f32 v118, v118, v150, v118
	v_fma_f32 v119, v119, v151, v119
	v_fma_f32 v120, v120, v152, v120
	v_fma_f32 v121, v121, v153, v121
	v_fma_f32 v122, v122, v154, v122
	v_fma_f32 v123, v123, v155, v123
	v_fma_f32 v124, v124, v156, v124
	v_fma_f32 v125, v125, v157, v125
	v_fma_f32 v126, v126, v158, v126
	v_fma_f32 v127, v127, v159, v127
	v_fma_f32 v128, v128, v160, v128
	v_fma_f32 v129, v129, v161, v129
	v_fma_f32 v130, v130, v162, v130
	v_fma_f32 v131, v131, v163, v131
	s_nop 1
	v_add_f32_dpp v236, v236, v236 quad_perm:[1,0,3,2] row_mask:0xf bank_mask:0xf
	s_nop 1
	v_add_f32_dpp v236, v236, v236 quad_perm:[2,3,0,1] row_mask:0xf bank_mask:0xf
	s_nop 1
	v_add_f32_dpp v236, v236, v236 row_half_mirror row_mask:0xf bank_mask:0xf
	s_nop 1
	v_add_f32_dpp v236, v236, v236 row_mirror row_mask:0xf bank_mask:0xf
	s_nop 1
	v_readlane_b32 s0, v236, 0
	v_readlane_b32 s1, v236, 16
	v_readlane_b32 s2, v236, 32
	v_readlane_b32 s3, v236, 48
	s_nop 3
	v_mov_b32_e32 v237, s0
	v_add_f32_e32 v237, s1, v237
	v_add_f32_e32 v237, s2, v237
	v_add_f32_e32 v237, s3, v237
	v_mul_f32_e32 v237, 0x3a000000, v237
	v_add_f32_e32 v237, 0x358637bd, v237
	v_rsq_f32_e32 v237, v237
	s_nop 0
	v_mul_f32_e32 v100, v100, v237
	v_mul_f32_e32 v101, v101, v237
	v_mul_f32_e32 v102, v102, v237
	v_mul_f32_e32 v103, v103, v237
	v_mul_f32_e32 v104, v104, v237
	v_mul_f32_e32 v105, v105, v237
	v_mul_f32_e32 v106, v106, v237
	v_mul_f32_e32 v107, v107, v237
	v_mul_f32_e32 v108, v108, v237
	v_mul_f32_e32 v109, v109, v237
	v_mul_f32_e32 v110, v110, v237
	v_mul_f32_e32 v111, v111, v237
	v_mul_f32_e32 v112, v112, v237
	v_mul_f32_e32 v113, v113, v237
	v_mul_f32_e32 v114, v114, v237
	v_mul_f32_e32 v115, v115, v237
	v_mul_f32_e32 v116, v116, v237
	v_mul_f32_e32 v117, v117, v237
	v_mul_f32_e32 v118, v118, v237
	v_mul_f32_e32 v119, v119, v237
	v_mul_f32_e32 v120, v120, v237
	v_mul_f32_e32 v121, v121, v237
	v_mul_f32_e32 v122, v122, v237
	v_mul_f32_e32 v123, v123, v237
	v_mul_f32_e32 v124, v124, v237
	v_mul_f32_e32 v125, v125, v237
	v_mul_f32_e32 v126, v126, v237
	v_mul_f32_e32 v127, v127, v237
	v_mul_f32_e32 v128, v128, v237
	v_mul_f32_e32 v129, v129, v237
	v_mul_f32_e32 v130, v130, v237
	v_mul_f32_e32 v131, v131, v237
	v_fma_f32 v4, v4, v100, v164
	v_fma_f32 v5, v5, v101, v165
	v_fma_f32 v6, v6, v102, v166
	v_fma_f32 v7, v7, v103, v167
	v_cvt_pk_bf16_f32 v238, v4, v5
	v_cvt_pk_bf16_f32 v239, v6, v7
	global_store_dwordx2 v2, v[238:239], s[22:23]
	v_fma_f32 v8, v8, v104, v168
	v_fma_f32 v9, v9, v105, v169
	v_fma_f32 v10, v10, v106, v170
	v_fma_f32 v11, v11, v107, v171
	v_cvt_pk_bf16_f32 v240, v8, v9
	v_cvt_pk_bf16_f32 v241, v10, v11
	global_store_dwordx2 v2, v[240:241], s[22:23] offset:512
	v_fma_f32 v12, v12, v108, v172
	v_fma_f32 v13, v13, v109, v173
	v_fma_f32 v14, v14, v110, v174
	v_fma_f32 v15, v15, v111, v175
	v_cvt_pk_bf16_f32 v238, v12, v13
	v_cvt_pk_bf16_f32 v239, v14, v15
	global_store_dwordx2 v2, v[238:239], s[22:23] offset:1024
	v_fma_f32 v16, v16, v112, v176
	v_fma_f32 v17, v17, v113, v177
	v_fma_f32 v18, v18, v114, v178
	v_fma_f32 v19, v19, v115, v179
	v_cvt_pk_bf16_f32 v240, v16, v17
	v_cvt_pk_bf16_f32 v241, v18, v19
	global_store_dwordx2 v2, v[240:241], s[22:23] offset:1536
	v_fma_f32 v20, v20, v116, v180
	v_fma_f32 v21, v21, v117, v181
	v_fma_f32 v22, v22, v118, v182
	v_fma_f32 v23, v23, v119, v183
	v_cvt_pk_bf16_f32 v238, v20, v21
	v_cvt_pk_bf16_f32 v239, v22, v23
	global_store_dwordx2 v2, v[238:239], s[22:23] offset:2048
	v_fma_f32 v24, v24, v120, v184
	v_fma_f32 v25, v25, v121, v185
	v_fma_f32 v26, v26, v122, v186
	v_fma_f32 v27, v27, v123, v187
	v_cvt_pk_bf16_f32 v240, v24, v25
	v_cvt_pk_bf16_f32 v241, v26, v27
	global_store_dwordx2 v2, v[240:241], s[22:23] offset:2560
	v_fma_f32 v28, v28, v124, v188
	v_fma_f32 v29, v29, v125, v189
	v_fma_f32 v30, v30, v126, v190
	v_fma_f32 v31, v31, v127, v191
	v_cvt_pk_bf16_f32 v238, v28, v29
	v_cvt_pk_bf16_f32 v239, v30, v31
	global_store_dwordx2 v2, v[238:239], s[22:23] offset:3072
	v_fma_f32 v32, v32, v128, v192
	v_fma_f32 v33, v33, v129, v193
	v_fma_f32 v34, v34, v130, v194
	v_fma_f32 v35, v35, v131, v195
	v_cvt_pk_bf16_f32 v240, v32, v33
	v_cvt_pk_bf16_f32 v241, v34, v35
	global_store_dwordx2 v2, v[240:241], s[22:23] offset:3584
	s_add_i32 s11, s10, 0x800
	s_lshr_b32 s0, s11, 8
	s_mul_i32 s0, s0, 57
	s_lshr_b32 s44, s0, 9
	s_mul_i32 s1, s44, 0x900
	s_sub_i32 s43, s11, s1
	s_lshl_b32 s1, s11, 13
	s_add_u32 s16, s48, s1
	s_addc_u32 s17, s49, 0
	s_add_u32 s18, s16, 0x1000
	s_addc_u32 s19, s17, 0
	s_lshl_b32 s1, s11, 12
	s_add_u32 s22, s50, s1
	s_addc_u32 s23, s51, 0
	s_cmpk_lt_u32 s43, 0x100
	s_cselect_b32 s0, 8, s44
	s_mul_i32 s1, s0, 0xc000
	s_add_u32 s28, s52, s1
	s_addc_u32 s29, s53, 0
	s_add_u32 s30, s28, 0x1000
	s_addc_u32 s31, s29, 0
	s_add_u32 s72, s54, s1
	s_addc_u32 s73, s55, 0
	s_add_u32 s72, s72, 0xa000
	s_addc_u32 s73, s73, 0
	s_add_u32 s74, s72, 0x1000
	s_addc_u32 s75, s73, 0
	global_load_dwordx4 v[68:71], v1, s[72:73]
	global_load_dwordx4 v[100:103], v1, s[56:57]
	global_load_dwordx4 v[72:75], v1, s[72:73] offset:1024
	global_load_dwordx4 v[104:107], v1, s[56:57] offset:1024
	global_load_dwordx4 v[76:79], v1, s[72:73] offset:2048
	global_load_dwordx4 v[108:111], v1, s[56:57] offset:2048
	global_load_dwordx4 v[80:83], v1, s[72:73] offset:3072
	global_load_dwordx4 v[112:115], v1, s[56:57] offset:3072
	global_load_dwordx4 v[84:87], v1, s[74:75]
	global_load_dwordx4 v[116:119], v1, s[58:59]
	global_load_dwordx4 v[88:91], v1, s[74:75] offset:1024
	global_load_dwordx4 v[120:123], v1, s[58:59] offset:1024
	global_load_dwordx4 v[92:95], v1, s[74:75] offset:2048
	global_load_dwordx4 v[124:127], v1, s[58:59] offset:2048
	global_load_dwordx4 v[96:99], v1, s[74:75] offset:3072
	global_load_dwordx4 v[128:131], v1, s[58:59] offset:3072
	s_add_u32 s84, s28, 0x2000
	s_addc_u32 s85, s29, 0
	s_add_u32 s86, s28, 0x3000
	s_addc_u32 s87, s29, 0
	global_load_dwordx4 v[164:167], v1, s[28:29]
	global_load_dwordx4 v[132:135], v1, s[84:85]
	global_load_dwordx4 v[168:171], v1, s[28:29] offset:1024
	global_load_dwordx4 v[136:139], v1, s[84:85] offset:1024
	global_load_dwordx4 v[172:175], v1, s[28:29] offset:2048
	global_load_dwordx4 v[140:143], v1, s[84:85] offset:2048
	global_load_dwordx4 v[176:179], v1, s[28:29] offset:3072
	global_load_dwordx4 v[144:147], v1, s[84:85] offset:3072
	global_load_dwordx4 v[180:183], v1, s[30:31]
	global_load_dwordx4 v[148:151], v1, s[86:87]
	global_load_dwordx4 v[184:187], v1, s[30:31] offset:1024
	global_load_dwordx4 v[152:155], v1, s[86:87] offset:1024
	global_load_dwordx4 v[188:191], v1, s[30:31] offset:2048
	global_load_dwordx4 v[156:159], v1, s[86:87] offset:2048
	global_load_dwordx4 v[192:195], v1, s[30:31] offset:3072
	global_load_dwordx4 v[160:163], v1, s[86:87] offset:3072
	s_waitcnt vmcnt(56)
	v_cmp_le_i32_e64 s[0:1], 0, v235
	s_nop 1
	s_and_b32 s45, s0, 0xffff
	s_mov_b32 s47, 0
	s_mov_b32 s61, 0
	s_cmp_eq_u32 s45, 0
	s_cbranch_scc1 .Ln1_y0_1
	s_mov_b32 s47, 1
	s_ff1_i32_b32 s0, s45
	s_add_i32 s1, s45, -1
	s_and_b32 s45, s45, s1
	s_nop 0
	v_readlane_b32 s0, v235, s0
	s_nop 3
	s_lshl_b32 s0, s0, 12
	s_add_u32 s76, s64, s0
	s_addc_u32 s77, s65, 0
	global_load_dwordx2 v[196:197], v2, s[76:77]
	global_load_dwordx2 v[198:199], v2, s[76:77] offset:512
	global_load_dwordx2 v[200:201], v2, s[76:77] offset:1024
	global_load_dwordx2 v[202:203], v2, s[76:77] offset:1536
	global_load_dwordx2 v[204:205], v2, s[76:77] offset:2048
	global_load_dwordx2 v[206:207], v2, s[76:77] offset:2560
	global_load_dwordx2 v[208:209], v2, s[76:77] offset:3072
	global_load_dwordx2 v[210:211], v2, s[76:77] offset:3584
	s_cmp_eq_u32 s45, 0
	s_cbranch_scc1 .Ln1_y0_1
	s_mov_b32 s61, 1
	s_ff1_i32_b32 s0, s45
	s_add_i32 s1, s45, -1
	s_and_b32 s45, s45, s1
	s_nop 0
	v_readlane_b32 s0, v235, s0
	s_nop 3
	s_lshl_b32 s0, s0, 12
	s_add_u32 s76, s64, s0
	s_addc_u32 s77, s65, 0
	global_load_dwordx2 v[212:213], v2, s[76:77]
	global_load_dwordx2 v[214:215], v2, s[76:77] offset:512
	global_load_dwordx2 v[216:217], v2, s[76:77] offset:1024
	global_load_dwordx2 v[218:219], v2, s[76:77] offset:1536
	global_load_dwordx2 v[226:227], v2, s[76:77] offset:2048
	global_load_dwordx2 v[228:229], v2, s[76:77] offset:2560
	global_load_dwordx2 v[230:231], v2, s[76:77] offset:3072
	global_load_dwordx2 v[232:233], v2, s[76:77] offset:3584
.Ln1_y0_1:
	s_add_i32 s11, s10, 0x1000
	s_lshr_b32 s0, s11, 8
	s_mul_i32 s0, s0, 57
	s_lshr_b32 s44, s0, 9
	s_mul_i32 s1, s44, 0x900
	s_sub_i32 s43, s11, s1
	s_lshl_b32 s1, s11, 6
	s_add_u32 s78, s62, s1
	s_addc_u32 s79, s63, 0
	global_load_dword v234, v246, s[78:79]
	s_lshl_b32 s1, s11, 13
	s_add_u32 s12, s48, s1
	s_addc_u32 s13, s49, 0
	s_add_u32 s14, s12, 0x1000
	s_addc_u32 s15, s13, 0
	global_load_dwordx4 v[4:7], v1, s[12:13]
	global_load_dwordx4 v[8:11], v1, s[12:13] offset:1024
	global_load_dwordx4 v[12:15], v1, s[12:13] offset:2048
	global_load_dwordx4 v[16:19], v1, s[12:13] offset:3072
	global_load_dwordx4 v[20:23], v1, s[14:15]
	global_load_dwordx4 v[24:27], v1, s[14:15] offset:1024
	global_load_dwordx4 v[28:31], v1, s[14:15] offset:2048
	global_load_dwordx4 v[32:35], v1, s[14:15] offset:3072
	s_waitcnt vmcnt(9)
	s_cmp_eq_u32 s47, 0
	s_cbranch_scc1 .Ln1_a1_1
	v_lshlrev_b32_e32 v238, 16, v196
	v_and_b32_e32 v239, 0xffff0000, v196
	v_fmac_f32_e32 v36, v68, v238
	v_fmac_f32_e32 v37, v69, v239
	v_lshlrev_b32_e32 v238, 16, v197
	v_and_b32_e32 v239, 0xffff0000, v197
	v_fmac_f32_e32 v38, v70, v238
	v_fmac_f32_e32 v39, v71, v239
	v_lshlrev_b32_e32 v238, 16, v198
	v_and_b32_e32 v239, 0xffff0000, v198
	v_fmac_f32_e32 v40, v72, v238
	v_fmac_f32_e32 v41, v73, v239
	v_lshlrev_b32_e32 v238, 16, v199
	v_and_b32_e32 v239, 0xffff0000, v199
	v_fmac_f32_e32 v42, v74, v238
	v_fmac_f32_e32 v43, v75, v239
	v_lshlrev_b32_e32 v238, 16, v200
	v_and_b32_e32 v239, 0xffff0000, v200
	v_fmac_f32_e32 v44, v76, v238
	v_fmac_f32_e32 v45, v77, v239
	v_lshlrev_b32_e32 v238, 16, v201
	v_and_b32_e32 v239, 0xffff0000, v201
	v_fmac_f32_e32 v46, v78, v238
	v_fmac_f32_e32 v47, v79, v239
	v_lshlrev_b32_e32 v238, 16, v202
	v_and_b32_e32 v239, 0xffff0000, v202
	v_fmac_f32_e32 v48, v80, v238
	v_fmac_f32_e32 v49, v81, v239
	v_lshlrev_b32_e32 v238, 16, v203
	v_and_b32_e32 v239, 0xffff0000, v203
	v_fmac_f32_e32 v50, v82, v238
	v_fmac_f32_e32 v51, v83, v239
	v_lshlrev_b32_e32 v238, 16, v204
	v_and_b32_e32 v239, 0xffff0000, v204
	v_fmac_f32_e32 v52, v84, v238
	v_fmac_f32_e32 v53, v85, v239
	v_lshlrev_b32_e32 v238, 16, v205
	v_and_b32_e32 v239, 0xffff0000, v205
	v_fmac_f32_e32 v54, v86, v238
	v_fmac_f32_e32 v55, v87, v239
	v_lshlrev_b32_e32 v238, 16, v206
	v_and_b32_e32 v239, 0xffff0000, v206
	v_fmac_f32_e32 v56, v88, v238
	v_fmac_f32_e32 v57, v89, v239
	v_lshlrev_b32_e32 v238, 16, v207
	v_and_b32_e32 v239, 0xffff0000, v207
	v_fmac_f32_e32 v58, v90, v238
	v_fmac_f32_e32 v59, v91, v239
	v_lshlrev_b32_e32 v238, 16, v208
	v_and_b32_e32 v239, 0xffff0000, v208
	v_fmac_f32_e32 v60, v92, v238
	v_fmac_f32_e32 v61, v93, v239
	v_lshlrev_b32_e32 v238, 16, v209
	v_and_b32_e32 v239, 0xffff0000, v209
	v_fmac_f32_e32 v62, v94, v238
	v_fmac_f32_e32 v63, v95, v239
	v_lshlrev_b32_e32 v238, 16, v210
	v_and_b32_e32 v239, 0xffff0000, v210
	v_fmac_f32_e32 v64, v96, v238
	v_fmac_f32_e32 v65, v97, v239
	v_lshlrev_b32_e32 v238, 16, v211
	v_and_b32_e32 v239, 0xffff0000, v211
	v_fmac_f32_e32 v66, v98, v238
	v_fmac_f32_e32 v67, v99, v239
.Ln1_a1_1:
	s_cmp_eq_u32 s61, 0
	s_cbranch_scc1 .Ln1_a2_1
	v_lshlrev_b32_e32 v238, 16, v212
	v_and_b32_e32 v239, 0xffff0000, v212
	v_fmac_f32_e32 v36, v68, v238
	v_fmac_f32_e32 v37, v69, v239
	v_lshlrev_b32_e32 v238, 16, v213
	v_and_b32_e32 v239, 0xffff0000, v213
	v_fmac_f32_e32 v38, v70, v238
	v_fmac_f32_e32 v39, v71, v239
	v_lshlrev_b32_e32 v238, 16, v214
	v_and_b32_e32 v239, 0xffff0000, v214
	v_fmac_f32_e32 v40, v72, v238
	v_fmac_f32_e32 v41, v73, v239
	v_lshlrev_b32_e32 v238, 16, v215
	v_and_b32_e32 v239, 0xffff0000, v215
	v_fmac_f32_e32 v42, v74, v238
	v_fmac_f32_e32 v43, v75, v239
	v_lshlrev_b32_e32 v238, 16, v216
	v_and_b32_e32 v239, 0xffff0000, v216
	v_fmac_f32_e32 v44, v76, v238
	v_fmac_f32_e32 v45, v77, v239
	v_lshlrev_b32_e32 v238, 16, v217
	v_and_b32_e32 v239, 0xffff0000, v217
	v_fmac_f32_e32 v46, v78, v238
	v_fmac_f32_e32 v47, v79, v239
	v_lshlrev_b32_e32 v238, 16, v218
	v_and_b32_e32 v239, 0xffff0000, v218
	v_fmac_f32_e32 v48, v80, v238
	v_fmac_f32_e32 v49, v81, v239
	v_lshlrev_b32_e32 v238, 16, v219
	v_and_b32_e32 v239, 0xffff0000, v219
	v_fmac_f32_e32 v50, v82, v238
	v_fmac_f32_e32 v51, v83, v239
	v_lshlrev_b32_e32 v238, 16, v226
	v_and_b32_e32 v239, 0xffff0000, v226
	v_fmac_f32_e32 v52, v84, v238
	v_fmac_f32_e32 v53, v85, v239
	v_lshlrev_b32_e32 v238, 16, v227
	v_and_b32_e32 v239, 0xffff0000, v227
	v_fmac_f32_e32 v54, v86, v238
	v_fmac_f32_e32 v55, v87, v239
	v_lshlrev_b32_e32 v238, 16, v228
	v_and_b32_e32 v239, 0xffff0000, v228
	v_fmac_f32_e32 v56, v88, v238
	v_fmac_f32_e32 v57, v89, v239
	v_lshlrev_b32_e32 v238, 16, v229
	v_and_b32_e32 v239, 0xffff0000, v229
	v_fmac_f32_e32 v58, v90, v238
	v_fmac_f32_e32 v59, v91, v239
	v_lshlrev_b32_e32 v238, 16, v230
	v_and_b32_e32 v239, 0xffff0000, v230
	v_fmac_f32_e32 v60, v92, v238
	v_fmac_f32_e32 v61, v93, v239
	v_lshlrev_b32_e32 v238, 16, v231
	v_and_b32_e32 v239, 0xffff0000, v231
	v_fmac_f32_e32 v62, v94, v238
	v_fmac_f32_e32 v63, v95, v239
	v_lshlrev_b32_e32 v238, 16, v232
	v_and_b32_e32 v239, 0xffff0000, v232
	v_fmac_f32_e32 v64, v96, v238
	v_fmac_f32_e32 v65, v97, v239
	v_lshlrev_b32_e32 v238, 16, v233
	v_and_b32_e32 v239, 0xffff0000, v233
	v_fmac_f32_e32 v66, v98, v238
	v_fmac_f32_e32 v67, v99, v239
.Ln1_a2_1:
.Ln1_more_1:
	s_cmp_eq_u32 s45, 0
	s_cbranch_scc1 .Ln1_gd_1
	s_ff1_i32_b32 s0, s45
	s_add_i32 s1, s45, -1
	s_and_b32 s45, s45, s1
	s_nop 0
	v_readlane_b32 s0, v235, s0
	s_nop 3
	s_lshl_b32 s0, s0, 12
	s_add_u32 s76, s64, s0
	s_addc_u32 s77, s65, 0
	global_load_dwordx2 v[196:197], v2, s[76:77]
	global_load_dwordx2 v[198:199], v2, s[76:77] offset:512
	global_load_dwordx2 v[200:201], v2, s[76:77] offset:1024
	global_load_dwordx2 v[202:203], v2, s[76:77] offset:1536
	global_load_dwordx2 v[204:205], v2, s[76:77] offset:2048
	global_load_dwordx2 v[206:207], v2, s[76:77] offset:2560
	global_load_dwordx2 v[208:209], v2, s[76:77] offset:3072
	global_load_dwordx2 v[210:211], v2, s[76:77] offset:3584
	s_waitcnt vmcnt(0)
	v_lshlrev_b32_e32 v238, 16, v196
	v_and_b32_e32 v239, 0xffff0000, v196
	v_fmac_f32_e32 v36, v68, v238
	v_fmac_f32_e32 v37, v69, v239
	v_lshlrev_b32_e32 v238, 16, v197
	v_and_b32_e32 v239, 0xffff0000, v197
	v_fmac_f32_e32 v38, v70, v238
	v_fmac_f32_e32 v39, v71, v239
	v_lshlrev_b32_e32 v238, 16, v198
	v_and_b32_e32 v239, 0xffff0000, v198
	v_fmac_f32_e32 v40, v72, v238
	v_fmac_f32_e32 v41, v73, v239
	v_lshlrev_b32_e32 v238, 16, v199
	v_and_b32_e32 v239, 0xffff0000, v199
	v_fmac_f32_e32 v42, v74, v238
	v_fmac_f32_e32 v43, v75, v239
	v_lshlrev_b32_e32 v238, 16, v200
	v_and_b32_e32 v239, 0xffff0000, v200
	v_fmac_f32_e32 v44, v76, v238
	v_fmac_f32_e32 v45, v77, v239
	v_lshlrev_b32_e32 v238, 16, v201
	v_and_b32_e32 v239, 0xffff0000, v201
	v_fmac_f32_e32 v46, v78, v238
	v_fmac_f32_e32 v47, v79, v239
	v_lshlrev_b32_e32 v238, 16, v202
	v_and_b32_e32 v239, 0xffff0000, v202
	v_fmac_f32_e32 v48, v80, v238
	v_fmac_f32_e32 v49, v81, v239
	v_lshlrev_b32_e32 v238, 16, v203
	v_and_b32_e32 v239, 0xffff0000, v203
	v_fmac_f32_e32 v50, v82, v238
	v_fmac_f32_e32 v51, v83, v239
	v_lshlrev_b32_e32 v238, 16, v204
	v_and_b32_e32 v239, 0xffff0000, v204
	v_fmac_f32_e32 v52, v84, v238
	v_fmac_f32_e32 v53, v85, v239
	v_lshlrev_b32_e32 v238, 16, v205
	v_and_b32_e32 v239, 0xffff0000, v205
	v_fmac_f32_e32 v54, v86, v238
	v_fmac_f32_e32 v55, v87, v239
	v_lshlrev_b32_e32 v238, 16, v206
	v_and_b32_e32 v239, 0xffff0000, v206
	v_fmac_f32_e32 v56, v88, v238
	v_fmac_f32_e32 v57, v89, v239
	v_lshlrev_b32_e32 v238, 16, v207
	v_and_b32_e32 v239, 0xffff0000, v207
	v_fmac_f32_e32 v58, v90, v238
	v_fmac_f32_e32 v59, v91, v239
	v_lshlrev_b32_e32 v238, 16, v208
	v_and_b32_e32 v239, 0xffff0000, v208
	v_fmac_f32_e32 v60, v92, v238
	v_fmac_f32_e32 v61, v93, v239
	v_lshlrev_b32_e32 v238, 16, v209
	v_and_b32_e32 v239, 0xffff0000, v209
	v_fmac_f32_e32 v62, v94, v238
	v_fmac_f32_e32 v63, v95, v239
	v_lshlrev_b32_e32 v238, 16, v210
	v_and_b32_e32 v239, 0xffff0000, v210
	v_fmac_f32_e32 v64, v96, v238
	v_fmac_f32_e32 v65, v97, v239
	v_lshlrev_b32_e32 v238, 16, v211
	v_and_b32_e32 v239, 0xffff0000, v211
	v_fmac_f32_e32 v66, v98, v238
	v_fmac_f32_e32 v67, v99, v239
	s_branch .Ln1_more_1
.Ln1_gd_1:
	global_store_dwordx4 v1, v[36:39], s[16:17]
	global_store_dwordx4 v1, v[40:43], s[16:17] offset:1024
	global_store_dwordx4 v1, v[44:47], s[16:17] offset:2048
	global_store_dwordx4 v1, v[48:51], s[16:17] offset:3072
	global_store_dwordx4 v1, v[52:55], s[18:19]
	global_store_dwordx4 v1, v[56:59], s[18:19] offset:1024
	global_store_dwordx4 v1, v[60:63], s[18:19] offset:2048
	global_store_dwordx4 v1, v[64:67], s[18:19] offset:3072
	v_mul_f32_e32 v236, v36, v36
	v_fmac_f32_e32 v236, v37, v37
	v_fmac_f32_e32 v236, v38, v38
	v_fmac_f32_e32 v236, v39, v39
	v_fmac_f32_e32 v236, v40, v40
	v_fmac_f32_e32 v236, v41, v41
	v_fmac_f32_e32 v236, v42, v42
	v_fmac_f32_e32 v236, v43, v43
	v_fmac_f32_e32 v236, v44, v44
	v_fmac_f32_e32 v236, v45, v45
	v_fmac_f32_e32 v236, v46, v46
	v_fmac_f32_e32 v236, v47, v47
	v_fmac_f32_e32 v236, v48, v48
	v_fmac_f32_e32 v236, v49, v49
	v_fmac_f32_e32 v236, v50, v50
	v_fmac_f32_e32 v236, v51, v51
	v_fmac_f32_e32 v236, v52, v52
	v_fmac_f32_e32 v236, v53, v53
	v_fmac_f32_e32 v236, v54, v54
	v_fmac_f32_e32 v236, v55, v55
	v_fmac_f32_e32 v236, v56, v56
	v_fmac_f32_e32 v236, v57, v57
	v_fmac_f32_e32 v236, v58, v58
	v_fmac_f32_e32 v236, v59, v59
	v_fmac_f32_e32 v236, v60, v60
	v_fmac_f32_e32 v236, v61, v61
	v_fmac_f32_e32 v236, v62, v62
	v_fmac_f32_e32 v236, v63, v63
	v_fmac_f32_e32 v236, v64, v64
	v_fmac_f32_e32 v236, v65, v65
	v_fmac_f32_e32 v236, v66, v66
	v_fmac_f32_e32 v236, v67, v67
	v_fma_f32 v100, v100, v132, v100
	v_fma_f32 v101, v101, v133, v101
	v_fma_f32 v102, v102, v134, v102
	v_fma_f32 v103, v103, v135, v103
	v_fma_f32 v104, v104, v136, v104
	v_fma_f32 v105, v105, v137, v105
	v_fma_f32 v106, v106, v138, v106
	v_fma_f32 v107, v107, v139, v107
	v_fma_f32 v108, v108, v140, v108
	v_fma_f32 v109, v109, v141, v109
	v_fma_f32 v110, v110, v142, v110
	v_fma_f32 v111, v111, v143, v111
	v_fma_f32 v112, v112, v144, v112
	v_fma_f32 v113, v113, v145, v113
	v_fma_f32 v114, v114, v146, v114
	v_fma_f32 v115, v115, v147, v115
	v_fma_f32 v116, v116, v148, v116
	v_fma_f32 v117, v117, v149, v117
	v_fma_f32 v118, v118, v150, v118
	v_fma_f32 v119, v119, v151, v119
	v_fma_f32 v120, v120, v152, v120
	v_fma_f32 v121, v121, v153, v121
	v_fma_f32 v122, v122, v154, v122
	v_fma_f32 v123, v123, v155, v123
	v_fma_f32 v124, v124, v156, v124
	v_fma_f32 v125, v125, v157, v125
	v_fma_f32 v126, v126, v158, v126
	v_fma_f32 v127, v127, v159, v127
	v_fma_f32 v128, v128, v160, v128
	v_fma_f32 v129, v129, v161, v129
	v_fma_f32 v130, v130, v162, v130
	v_fma_f32 v131, v131, v163, v131
	s_nop 1
	v_add_f32_dpp v236, v236, v236 quad_perm:[1,0,3,2] row_mask:0xf bank_mask:0xf
	s_nop 1
	v_add_f32_dpp v236, v236, v236 quad_perm:[2,3,0,1] row_mask:0xf bank_mask:0xf
	s_nop 1
	v_add_f32_dpp v236, v236, v236 row_half_mirror row_mask:0xf bank_mask:0xf
	s_nop 1
	v_add_f32_dpp v236, v236, v236 row_mirror row_mask:0xf bank_mask:0xf
	s_nop 1
	v_readlane_b32 s0, v236, 0
	v_readlane_b32 s1, v236, 16
	v_readlane_b32 s2, v236, 32
	v_readlane_b32 s3, v236, 48
	s_nop 3
	v_mov_b32_e32 v237, s0
	v_add_f32_e32 v237, s1, v237
	v_add_f32_e32 v237, s2, v237
	v_add_f32_e32 v237, s3, v237
	v_mul_f32_e32 v237, 0x3a000000, v237
	v_add_f32_e32 v237, 0x358637bd, v237
	v_rsq_f32_e32 v237, v237
	s_nop 0
	v_mul_f32_e32 v100, v100, v237
	v_mul_f32_e32 v101, v101, v237
	v_mul_f32_e32 v102, v102, v237
	v_mul_f32_e32 v103, v103, v237
	v_mul_f32_e32 v104, v104, v237
	v_mul_f32_e32 v105, v105, v237
	v_mul_f32_e32 v106, v106, v237
	v_mul_f32_e32 v107, v107, v237
	v_mul_f32_e32 v108, v108, v237
	v_mul_f32_e32 v109, v109, v237
	v_mul_f32_e32 v110, v110, v237
	v_mul_f32_e32 v111, v111, v237
	v_mul_f32_e32 v112, v112, v237
	v_mul_f32_e32 v113, v113, v237
	v_mul_f32_e32 v114, v114, v237
	v_mul_f32_e32 v115, v115, v237
	v_mul_f32_e32 v116, v116, v237
	v_mul_f32_e32 v117, v117, v237
	v_mul_f32_e32 v118, v118, v237
	v_mul_f32_e32 v119, v119, v237
	v_mul_f32_e32 v120, v120, v237
	v_mul_f32_e32 v121, v121, v237
	v_mul_f32_e32 v122, v122, v237
	v_mul_f32_e32 v123, v123, v237
	v_mul_f32_e32 v124, v124, v237
	v_mul_f32_e32 v125, v125, v237
	v_mul_f32_e32 v126, v126, v237
	v_mul_f32_e32 v127, v127, v237
	v_mul_f32_e32 v128, v128, v237
	v_mul_f32_e32 v129, v129, v237
	v_mul_f32_e32 v130, v130, v237
	v_mul_f32_e32 v131, v131, v237
	v_fma_f32 v36, v36, v100, v164
	v_fma_f32 v37, v37, v101, v165
	v_fma_f32 v38, v38, v102, v166
	v_fma_f32 v39, v39, v103, v167
	v_cvt_pk_bf16_f32 v238, v36, v37
	v_cvt_pk_bf16_f32 v239, v38, v39
	global_store_dwordx2 v2, v[238:239], s[22:23]
	v_fma_f32 v40, v40, v104, v168
	v_fma_f32 v41, v41, v105, v169
	v_fma_f32 v42, v42, v106, v170
	v_fma_f32 v43, v43, v107, v171
	v_cvt_pk_bf16_f32 v240, v40, v41
	v_cvt_pk_bf16_f32 v241, v42, v43
	global_store_dwordx2 v2, v[240:241], s[22:23] offset:512
	v_fma_f32 v44, v44, v108, v172
	v_fma_f32 v45, v45, v109, v173
	v_fma_f32 v46, v46, v110, v174
	v_fma_f32 v47, v47, v111, v175
	v_cvt_pk_bf16_f32 v238, v44, v45
	v_cvt_pk_bf16_f32 v239, v46, v47
	global_store_dwordx2 v2, v[238:239], s[22:23] offset:1024
	v_fma_f32 v48, v48, v112, v176
	v_fma_f32 v49, v49, v113, v177
	v_fma_f32 v50, v50, v114, v178
	v_fma_f32 v51, v51, v115, v179
	v_cvt_pk_bf16_f32 v240, v48, v49
	v_cvt_pk_bf16_f32 v241, v50, v51
	global_store_dwordx2 v2, v[240:241], s[22:23] offset:1536
	v_fma_f32 v52, v52, v116, v180
	v_fma_f32 v53, v53, v117, v181
	v_fma_f32 v54, v54, v118, v182
	v_fma_f32 v55, v55, v119, v183
	v_cvt_pk_bf16_f32 v238, v52, v53
	v_cvt_pk_bf16_f32 v239, v54, v55
	global_store_dwordx2 v2, v[238:239], s[22:23] offset:2048
	v_fma_f32 v56, v56, v120, v184
	v_fma_f32 v57, v57, v121, v185
	v_fma_f32 v58, v58, v122, v186
	v_fma_f32 v59, v59, v123, v187
	v_cvt_pk_bf16_f32 v240, v56, v57
	v_cvt_pk_bf16_f32 v241, v58, v59
	global_store_dwordx2 v2, v[240:241], s[22:23] offset:2560
	v_fma_f32 v60, v60, v124, v188
	v_fma_f32 v61, v61, v125, v189
	v_fma_f32 v62, v62, v126, v190
	v_fma_f32 v63, v63, v127, v191
	v_cvt_pk_bf16_f32 v238, v60, v61
	v_cvt_pk_bf16_f32 v239, v62, v63
	global_store_dwordx2 v2, v[238:239], s[22:23] offset:3072
	v_fma_f32 v64, v64, v128, v192
	v_fma_f32 v65, v65, v129, v193
	v_fma_f32 v66, v66, v130, v194
	v_fma_f32 v67, v67, v131, v195
	v_cvt_pk_bf16_f32 v240, v64, v65
	v_cvt_pk_bf16_f32 v241, v66, v67
	global_store_dwordx2 v2, v[240:241], s[22:23] offset:3584
	s_add_i32 s11, s10, 0x1000
	s_lshr_b32 s0, s11, 8
	s_mul_i32 s0, s0, 57
	s_lshr_b32 s44, s0, 9
	s_mul_i32 s1, s44, 0x900
	s_sub_i32 s43, s11, s1
	s_lshl_b32 s1, s11, 13
	s_add_u32 s16, s48, s1
	s_addc_u32 s17, s49, 0
	s_add_u32 s18, s16, 0x1000
	s_addc_u32 s19, s17, 0
	s_lshl_b32 s1, s11, 12
	s_add_u32 s22, s50, s1
	s_addc_u32 s23, s51, 0
	s_cmpk_lt_u32 s43, 0x100
	s_cselect_b32 s0, 8, s44
	s_mul_i32 s1, s0, 0xc000
	s_add_u32 s28, s52, s1
	s_addc_u32 s29, s53, 0
	s_add_u32 s30, s28, 0x1000
	s_addc_u32 s31, s29, 0
	s_add_u32 s72, s54, s1
	s_addc_u32 s73, s55, 0
	s_add_u32 s72, s72, 0xa000
	s_addc_u32 s73, s73, 0
	s_add_u32 s74, s72, 0x1000
	s_addc_u32 s75, s73, 0
	global_load_dwordx4 v[68:71], v1, s[72:73]
	global_load_dwordx4 v[100:103], v1, s[56:57]
	global_load_dwordx4 v[72:75], v1, s[72:73] offset:1024
	global_load_dwordx4 v[104:107], v1, s[56:57] offset:1024
	global_load_dwordx4 v[76:79], v1, s[72:73] offset:2048
	global_load_dwordx4 v[108:111], v1, s[56:57] offset:2048
	global_load_dwordx4 v[80:83], v1, s[72:73] offset:3072
	global_load_dwordx4 v[112:115], v1, s[56:57] offset:3072
	global_load_dwordx4 v[84:87], v1, s[74:75]
	global_load_dwordx4 v[116:119], v1, s[58:59]
	global_load_dwordx4 v[88:91], v1, s[74:75] offset:1024
	global_load_dwordx4 v[120:123], v1, s[58:59] offset:1024
	global_load_dwordx4 v[92:95], v1, s[74:75] offset:2048
	global_load_dwordx4 v[124:127], v1, s[58:59] offset:2048
	global_load_dwordx4 v[96:99], v1, s[74:75] offset:3072
	global_load_dwordx4 v[128:131], v1, s[58:59] offset:3072
	s_add_u32 s84, s28, 0x2000
	s_addc_u32 s85, s29, 0
	s_add_u32 s86, s28, 0x3000
	s_addc_u32 s87, s29, 0
	global_load_dwordx4 v[164:167], v1, s[28:29]
	global_load_dwordx4 v[132:135], v1, s[84:85]
	global_load_dwordx4 v[168:171], v1, s[28:29] offset:1024
	global_load_dwordx4 v[136:139], v1, s[84:85] offset:1024
	global_load_dwordx4 v[172:175], v1, s[28:29] offset:2048
	global_load_dwordx4 v[140:143], v1, s[84:85] offset:2048
	global_load_dwordx4 v[176:179], v1, s[28:29] offset:3072
	global_load_dwordx4 v[144:147], v1, s[84:85] offset:3072
	global_load_dwordx4 v[180:183], v1, s[30:31]
	global_load_dwordx4 v[148:151], v1, s[86:87]
	global_load_dwordx4 v[184:187], v1, s[30:31] offset:1024
	global_load_dwordx4 v[152:155], v1, s[86:87] offset:1024
	global_load_dwordx4 v[188:191], v1, s[30:31] offset:2048
	global_load_dwordx4 v[156:159], v1, s[86:87] offset:2048
	global_load_dwordx4 v[192:195], v1, s[30:31] offset:3072
	global_load_dwordx4 v[160:163], v1, s[86:87] offset:3072
	s_waitcnt vmcnt(56)
	v_cmp_le_i32_e64 s[0:1], 0, v234
	s_nop 1
	s_and_b32 s45, s0, 0xffff
	s_mov_b32 s47, 0
	s_mov_b32 s61, 0
	s_cmp_eq_u32 s45, 0
	s_cbranch_scc1 .Ln1_y0_2
	s_mov_b32 s47, 1
	s_ff1_i32_b32 s0, s45
	s_add_i32 s1, s45, -1
	s_and_b32 s45, s45, s1
	s_nop 0
	v_readlane_b32 s0, v234, s0
	s_nop 3
	s_lshl_b32 s0, s0, 12
	s_add_u32 s76, s64, s0
	s_addc_u32 s77, s65, 0
	global_load_dwordx2 v[196:197], v2, s[76:77]
	global_load_dwordx2 v[198:199], v2, s[76:77] offset:512
	global_load_dwordx2 v[200:201], v2, s[76:77] offset:1024
	global_load_dwordx2 v[202:203], v2, s[76:77] offset:1536
	global_load_dwordx2 v[204:205], v2, s[76:77] offset:2048
	global_load_dwordx2 v[206:207], v2, s[76:77] offset:2560
	global_load_dwordx2 v[208:209], v2, s[76:77] offset:3072
	global_load_dwordx2 v[210:211], v2, s[76:77] offset:3584
	s_cmp_eq_u32 s45, 0
	s_cbranch_scc1 .Ln1_y0_2
	s_mov_b32 s61, 1
	s_ff1_i32_b32 s0, s45
	s_add_i32 s1, s45, -1
	s_and_b32 s45, s45, s1
	s_nop 0
	v_readlane_b32 s0, v234, s0
	s_nop 3
	s_lshl_b32 s0, s0, 12
	s_add_u32 s76, s64, s0
	s_addc_u32 s77, s65, 0
	global_load_dwordx2 v[212:213], v2, s[76:77]
	global_load_dwordx2 v[214:215], v2, s[76:77] offset:512
	global_load_dwordx2 v[216:217], v2, s[76:77] offset:1024
	global_load_dwordx2 v[218:219], v2, s[76:77] offset:1536
	global_load_dwordx2 v[226:227], v2, s[76:77] offset:2048
	global_load_dwordx2 v[228:229], v2, s[76:77] offset:2560
	global_load_dwordx2 v[230:231], v2, s[76:77] offset:3072
	global_load_dwordx2 v[232:233], v2, s[76:77] offset:3584
.Ln1_y0_2:
	s_add_i32 s11, s10, 0x1800
	s_lshr_b32 s0, s11, 8
	s_mul_i32 s0, s0, 57
	s_lshr_b32 s44, s0, 9
	s_mul_i32 s1, s44, 0x900
	s_sub_i32 s43, s11, s1
	s_lshl_b32 s1, s11, 6
	s_add_u32 s78, s62, s1
	s_addc_u32 s79, s63, 0
	global_load_dword v235, v246, s[78:79]
	s_lshl_b32 s1, s11, 13
	s_add_u32 s12, s48, s1
	s_addc_u32 s13, s49, 0
	s_add_u32 s14, s12, 0x1000
	s_addc_u32 s15, s13, 0
	global_load_dwordx4 v[36:39], v1, s[12:13]
	global_load_dwordx4 v[40:43], v1, s[12:13] offset:1024
	global_load_dwordx4 v[44:47], v1, s[12:13] offset:2048
	global_load_dwordx4 v[48:51], v1, s[12:13] offset:3072
	global_load_dwordx4 v[52:55], v1, s[14:15]
	global_load_dwordx4 v[56:59], v1, s[14:15] offset:1024
	global_load_dwordx4 v[60:63], v1, s[14:15] offset:2048
	global_load_dwordx4 v[64:67], v1, s[14:15] offset:3072
	s_waitcnt vmcnt(9)
	s_cmp_eq_u32 s47, 0
	s_cbranch_scc1 .Ln1_a1_2
	v_lshlrev_b32_e32 v238, 16, v196
	v_and_b32_e32 v239, 0xffff0000, v196
	v_fmac_f32_e32 v4, v68, v238
	v_fmac_f32_e32 v5, v69, v239
	v_lshlrev_b32_e32 v238, 16, v197
	v_and_b32_e32 v239, 0xffff0000, v197
	v_fmac_f32_e32 v6, v70, v238
	v_fmac_f32_e32 v7, v71, v239
	v_lshlrev_b32_e32 v238, 16, v198
	v_and_b32_e32 v239, 0xffff0000, v198
	v_fmac_f32_e32 v8, v72, v238
	v_fmac_f32_e32 v9, v73, v239
	v_lshlrev_b32_e32 v238, 16, v199
	v_and_b32_e32 v239, 0xffff0000, v199
	v_fmac_f32_e32 v10, v74, v238
	v_fmac_f32_e32 v11, v75, v239
	v_lshlrev_b32_e32 v238, 16, v200
	v_and_b32_e32 v239, 0xffff0000, v200
	v_fmac_f32_e32 v12, v76, v238
	v_fmac_f32_e32 v13, v77, v239
	v_lshlrev_b32_e32 v238, 16, v201
	v_and_b32_e32 v239, 0xffff0000, v201
	v_fmac_f32_e32 v14, v78, v238
	v_fmac_f32_e32 v15, v79, v239
	v_lshlrev_b32_e32 v238, 16, v202
	v_and_b32_e32 v239, 0xffff0000, v202
	v_fmac_f32_e32 v16, v80, v238
	v_fmac_f32_e32 v17, v81, v239
	v_lshlrev_b32_e32 v238, 16, v203
	v_and_b32_e32 v239, 0xffff0000, v203
	v_fmac_f32_e32 v18, v82, v238
	v_fmac_f32_e32 v19, v83, v239
	v_lshlrev_b32_e32 v238, 16, v204
	v_and_b32_e32 v239, 0xffff0000, v204
	v_fmac_f32_e32 v20, v84, v238
	v_fmac_f32_e32 v21, v85, v239
	v_lshlrev_b32_e32 v238, 16, v205
	v_and_b32_e32 v239, 0xffff0000, v205
	v_fmac_f32_e32 v22, v86, v238
	v_fmac_f32_e32 v23, v87, v239
	v_lshlrev_b32_e32 v238, 16, v206
	v_and_b32_e32 v239, 0xffff0000, v206
	v_fmac_f32_e32 v24, v88, v238
	v_fmac_f32_e32 v25, v89, v239
	v_lshlrev_b32_e32 v238, 16, v207
	v_and_b32_e32 v239, 0xffff0000, v207
	v_fmac_f32_e32 v26, v90, v238
	v_fmac_f32_e32 v27, v91, v239
	v_lshlrev_b32_e32 v238, 16, v208
	v_and_b32_e32 v239, 0xffff0000, v208
	v_fmac_f32_e32 v28, v92, v238
	v_fmac_f32_e32 v29, v93, v239
	v_lshlrev_b32_e32 v238, 16, v209
	v_and_b32_e32 v239, 0xffff0000, v209
	v_fmac_f32_e32 v30, v94, v238
	v_fmac_f32_e32 v31, v95, v239
	v_lshlrev_b32_e32 v238, 16, v210
	v_and_b32_e32 v239, 0xffff0000, v210
	v_fmac_f32_e32 v32, v96, v238
	v_fmac_f32_e32 v33, v97, v239
	v_lshlrev_b32_e32 v238, 16, v211
	v_and_b32_e32 v239, 0xffff0000, v211
	v_fmac_f32_e32 v34, v98, v238
	v_fmac_f32_e32 v35, v99, v239

.Ln1_gd_2:
	global_store_dwordx4 v1, v[4:7], s[16:17]
	global_store_dwordx4 v1, v[8:11], s[16:17] offset:1024
	global_store_dwordx4 v1, v[12:15], s[16:17] offset:2048
	global_store_dwordx4 v1, v[16:19], s[16:17] offset:3072
	global_store_dwordx4 v1, v[20:23], s[18:19]
	global_store_dwordx4 v1, v[24:27], s[18:19] offset:1024
	global_store_dwordx4 v1, v[28:31], s[18:19] offset:2048
	global_store_dwordx4 v1, v[32:35], s[18:19] offset:3072
	v_mul_f32_e32 v236, v4, v4
	v_fmac_f32_e32 v236, v5, v5
	v_fmac_f32_e32 v236, v6, v6
	v_fmac_f32_e32 v236, v7, v7
	v_fmac_f32_e32 v236, v8, v8
	v_fmac_f32_e32 v236, v9, v9
	v_fmac_f32_e32 v236, v10, v10
	v_fmac_f32_e32 v236, v11, v11
	v_fmac_f32_e32 v236, v12, v12
	v_fmac_f32_e32 v236, v13, v13
	v_fmac_f32_e32 v236, v14, v14
	v_fmac_f32_e32 v236, v15, v15
	v_fmac_f32_e32 v236, v16, v16
	v_fmac_f32_e32 v236, v17, v17
	v_fmac_f32_e32 v236, v18, v18
	v_fmac_f32_e32 v236, v19, v19
	v_fmac_f32_e32 v236, v20, v20
	v_fmac_f32_e32 v236, v21, v21
	v_fmac_f32_e32 v236, v22, v22
	v_fmac_f32_e32 v236, v23, v23
	v_fmac_f32_e32 v236, v24, v24
	v_fmac_f32_e32 v236, v25, v25
	v_fmac_f32_e32 v236, v26, v26
	v_fmac_f32_e32 v236, v27, v27
	v_fmac_f32_e32 v236, v28, v28
	v_fmac_f32_e32 v236, v29, v29
	v_fmac_f32_e32 v236, v30, v30
	v_fmac_f32_e32 v236, v31, v31
	v_fmac_f32_e32 v236, v32, v32
	v_fmac_f32_e32 v236, v33, v33
	v_fmac_f32_e32 v236, v34, v34
	v_fmac_f32_e32 v236, v35, v35
	v_fma_f32 v100, v100, v132, v100
	v_fma_f32 v101, v101, v133, v101
	v_fma_f32 v102, v102, v134, v102
	v_fma_f32 v103, v103, v135, v103
	v_fma_f32 v104, v104, v136, v104
	v_fma_f32 v105, v105, v137, v105
	v_fma_f32 v106, v106, v138, v106
	v_fma_f32 v107, v107, v139, v107
	v_fma_f32 v108, v108, v140, v108
	v_fma_f32 v109, v109, v141, v109
	v_fma_f32 v110, v110, v142, v110
	v_fma_f32 v111, v111, v143, v111
	v_fma_f32 v112, v112, v144, v112
	v_fma_f32 v113, v113, v145, v113
	v_fma_f32 v114, v114, v146, v114
	v_fma_f32 v115, v115, v147, v115
	v_fma_f32 v116, v116, v148, v116
	v_fma_f32 v117, v117, v149, v117
	v_fma_f32 v118, v118, v150, v118
	v_fma_f32 v119, v119, v151, v119
	v_fma_f32 v120, v120, v152, v120
	v_fma_f32 v121, v121, v153, v121
	v_fma_f32 v122, v122, v154, v122
	v_fma_f32 v123, v123, v155, v123
	v_fma_f32 v124, v124, v156, v124
	v_fma_f32 v125, v125, v157, v125
	v_fma_f32 v126, v126, v158, v126
	v_fma_f32 v127, v127, v159, v127
	v_fma_f32 v128, v128, v160, v128
	v_fma_f32 v129, v129, v161, v129
	v_fma_f32 v130, v130, v162, v130
	v_fma_f32 v131, v131, v163, v131
	s_nop 1
	v_add_f32_dpp v236, v236, v236 quad_perm:[1,0,3,2] row_mask:0xf bank_mask:0xf
	s_nop 1
	v_add_f32_dpp v236, v236, v236 quad_perm:[2,3,0,1] row_mask:0xf bank_mask:0xf
	s_nop 1
	v_add_f32_dpp v236, v236, v236 row_half_mirror row_mask:0xf bank_mask:0xf
	s_nop 1
	v_add_f32_dpp v236, v236, v236 row_mirror row_mask:0xf bank_mask:0xf
	s_nop 1
	v_readlane_b32 s0, v236, 0
	v_readlane_b32 s1, v236, 16
	v_readlane_b32 s2, v236, 32
	v_readlane_b32 s3, v236, 48
	s_nop 3
	v_mov_b32_e32 v237, s0
	v_add_f32_e32 v237, s1, v237
	v_add_f32_e32 v237, s2, v237
	v_add_f32_e32 v237, s3, v237
	v_mul_f32_e32 v237, 0x3a000000, v237
	v_add_f32_e32 v237, 0x358637bd, v237
	v_rsq_f32_e32 v237, v237
	s_nop 0
	v_mul_f32_e32 v100, v100, v237
	v_mul_f32_e32 v101, v101, v237
	v_mul_f32_e32 v102, v102, v237
	v_mul_f32_e32 v103, v103, v237
	v_mul_f32_e32 v104, v104, v237
	v_mul_f32_e32 v105, v105, v237
	v_mul_f32_e32 v106, v106, v237
	v_mul_f32_e32 v107, v107, v237
	v_mul_f32_e32 v108, v108, v237
	v_mul_f32_e32 v109, v109, v237
	v_mul_f32_e32 v110, v110, v237
	v_mul_f32_e32 v111, v111, v237
	v_mul_f32_e32 v112, v112, v237
	v_mul_f32_e32 v113, v113, v237
	v_mul_f32_e32 v114, v114, v237
	v_mul_f32_e32 v115, v115, v237
	v_mul_f32_e32 v116, v116, v237
	v_mul_f32_e32 v117, v117, v237
	v_mul_f32_e32 v118, v118, v237
	v_mul_f32_e32 v119, v119, v237
	v_mul_f32_e32 v120, v120, v237
	v_mul_f32_e32 v121, v121, v237
	v_mul_f32_e32 v122, v122, v237
	v_mul_f32_e32 v123, v123, v237
	v_mul_f32_e32 v124, v124, v237
	v_mul_f32_e32 v125, v125, v237
	v_mul_f32_e32 v126, v126, v237
	v_mul_f32_e32 v127, v127, v237
	v_mul_f32_e32 v128, v128, v237
	v_mul_f32_e32 v129, v129, v237
	v_mul_f32_e32 v130, v130, v237
	v_mul_f32_e32 v131, v131, v237
	v_fma_f32 v4, v4, v100, v164
	v_fma_f32 v5, v5, v101, v165
	v_fma_f32 v6, v6, v102, v166
	v_fma_f32 v7, v7, v103, v167
	v_cvt_pk_bf16_f32 v238, v4, v5
	v_cvt_pk_bf16_f32 v239, v6, v7
	global_store_dwordx2 v2, v[238:239], s[22:23]
	v_fma_f32 v8, v8, v104, v168
	v_fma_f32 v9, v9, v105, v169
	v_fma_f32 v10, v10, v106, v170
	v_fma_f32 v11, v11, v107, v171
	v_cvt_pk_bf16_f32 v240, v8, v9
	v_cvt_pk_bf16_f32 v241, v10, v11
	global_store_dwordx2 v2, v[240:241], s[22:23] offset:512
	v_fma_f32 v12, v12, v108, v172
	v_fma_f32 v13, v13, v109, v173
	v_fma_f32 v14, v14, v110, v174
	v_fma_f32 v15, v15, v111, v175
	v_cvt_pk_bf16_f32 v238, v12, v13
	v_cvt_pk_bf16_f32 v239, v14, v15
	global_store_dwordx2 v2, v[238:239], s[22:23] offset:1024
	v_fma_f32 v16, v16, v112, v176
	v_fma_f32 v17, v17, v113, v177
	v_fma_f32 v18, v18, v114, v178
	v_fma_f32 v19, v19, v115, v179
	v_cvt_pk_bf16_f32 v240, v16, v17
	v_cvt_pk_bf16_f32 v241, v18, v19
	global_store_dwordx2 v2, v[240:241], s[22:23] offset:1536
	v_fma_f32 v20, v20, v116, v180
	v_fma_f32 v21, v21, v117, v181
	v_fma_f32 v22, v22, v118, v182
	v_fma_f32 v23, v23, v119, v183
	v_cvt_pk_bf16_f32 v238, v20, v21
	v_cvt_pk_bf16_f32 v239, v22, v23
	global_store_dwordx2 v2, v[238:239], s[22:23] offset:2048
	v_fma_f32 v24, v24, v120, v184
	v_fma_f32 v25, v25, v121, v185
	v_fma_f32 v26, v26, v122, v186
	v_fma_f32 v27, v27, v123, v187
	v_cvt_pk_bf16_f32 v240, v24, v25
	v_cvt_pk_bf16_f32 v241, v26, v27
	global_store_dwordx2 v2, v[240:241], s[22:23] offset:2560
	v_fma_f32 v28, v28, v124, v188
	v_fma_f32 v29, v29, v125, v189
	v_fma_f32 v30, v30, v126, v190
	v_fma_f32 v31, v31, v127, v191
	v_cvt_pk_bf16_f32 v238, v28, v29
	v_cvt_pk_bf16_f32 v239, v30, v31
	global_store_dwordx2 v2, v[238:239], s[22:23] offset:3072
	v_fma_f32 v32, v32, v128, v192
	v_fma_f32 v33, v33, v129, v193
	v_fma_f32 v34, v34, v130, v194
	v_fma_f32 v35, v35, v131, v195
	v_cvt_pk_bf16_f32 v240, v32, v33
	v_cvt_pk_bf16_f32 v241, v34, v35
	global_store_dwordx2 v2, v[240:241], s[22:23] offset:3584
	s_add_i32 s11, s10, 0x1800
	s_lshr_b32 s0, s11, 8
	s_mul_i32 s0, s0, 57
	s_lshr_b32 s44, s0, 9
	s_mul_i32 s1, s44, 0x900
	s_sub_i32 s43, s11, s1
	s_lshl_b32 s1, s11, 13
	s_add_u32 s16, s48, s1
	s_addc_u32 s17, s49, 0
	s_add_u32 s18, s16, 0x1000
	s_addc_u32 s19, s17, 0
	s_lshl_b32 s1, s11, 12
	s_add_u32 s22, s50, s1
	s_addc_u32 s23, s51, 0
	s_cmpk_lt_u32 s43, 0x100
	s_cselect_b32 s0, 8, s44
	s_mul_i32 s1, s0, 0xc000
	s_add_u32 s28, s52, s1
	s_addc_u32 s29, s53, 0
	s_add_u32 s30, s28, 0x1000
	s_addc_u32 s31, s29, 0
	s_add_u32 s72, s54, s1
	s_addc_u32 s73, s55, 0
	s_add_u32 s72, s72, 0xa000
	s_addc_u32 s73, s73, 0
	s_add_u32 s74, s72, 0x1000
	s_addc_u32 s75, s73, 0
	global_load_dwordx4 v[68:71], v1, s[72:73]
	global_load_dwordx4 v[100:103], v1, s[56:57]
	global_load_dwordx4 v[72:75], v1, s[72:73] offset:1024
	global_load_dwordx4 v[104:107], v1, s[56:57] offset:1024
	global_load_dwordx4 v[76:79], v1, s[72:73] offset:2048
	global_load_dwordx4 v[108:111], v1, s[56:57] offset:2048
	global_load_dwordx4 v[80:83], v1, s[72:73] offset:3072
	global_load_dwordx4 v[112:115], v1, s[56:57] offset:3072
	global_load_dwordx4 v[84:87], v1, s[74:75]
	global_load_dwordx4 v[116:119], v1, s[58:59]
	global_load_dwordx4 v[88:91], v1, s[74:75] offset:1024
	global_load_dwordx4 v[120:123], v1, s[58:59] offset:1024
	global_load_dwordx4 v[92:95], v1, s[74:75] offset:2048
	global_load_dwordx4 v[124:127], v1, s[58:59] offset:2048
	global_load_dwordx4 v[96:99], v1, s[74:75] offset:3072
	global_load_dwordx4 v[128:131], v1, s[58:59] offset:3072
	s_add_u32 s84, s28, 0x2000
	s_addc_u32 s85, s29, 0
	s_add_u32 s86, s28, 0x3000
	s_addc_u32 s87, s29, 0
	global_load_dwordx4 v[164:167], v1, s[28:29]
	global_load_dwordx4 v[132:135], v1, s[84:85]
	global_load_dwordx4 v[168:171], v1, s[28:29] offset:1024
	global_load_dwordx4 v[136:139], v1, s[84:85] offset:1024
	global_load_dwordx4 v[172:175], v1, s[28:29] offset:2048
	global_load_dwordx4 v[140:143], v1, s[84:85] offset:2048
	global_load_dwordx4 v[176:179], v1, s[28:29] offset:3072
	global_load_dwordx4 v[144:147], v1, s[84:85] offset:3072
	global_load_dwordx4 v[180:183], v1, s[30:31]
	global_load_dwordx4 v[148:151], v1, s[86:87]
	global_load_dwordx4 v[184:187], v1, s[30:31] offset:1024
	global_load_dwordx4 v[152:155], v1, s[86:87] offset:1024
	global_load_dwordx4 v[188:191], v1, s[30:31] offset:2048
	global_load_dwordx4 v[156:159], v1, s[86:87] offset:2048
	global_load_dwordx4 v[192:195], v1, s[30:31] offset:3072
	global_load_dwordx4 v[160:163], v1, s[86:87] offset:3072
	s_waitcnt vmcnt(56)
	v_cmp_le_i32_e64 s[0:1], 0, v235
	s_nop 1
	s_and_b32 s45, s0, 0xffff
	s_mov_b32 s47, 0
	s_mov_b32 s61, 0
	s_cmp_eq_u32 s45, 0
	s_cbranch_scc1 .Ln1_y0_3
	s_mov_b32 s47, 1
	s_ff1_i32_b32 s0, s45
	s_add_i32 s1, s45, -1
	s_and_b32 s45, s45, s1
	s_nop 0
	v_readlane_b32 s0, v235, s0
	s_nop 3
	s_lshl_b32 s0, s0, 12
	s_add_u32 s76, s64, s0
	s_addc_u32 s77, s65, 0
	global_load_dwordx2 v[196:197], v2, s[76:77]
	global_load_dwordx2 v[198:199], v2, s[76:77] offset:512
	global_load_dwordx2 v[200:201], v2, s[76:77] offset:1024
	global_load_dwordx2 v[202:203], v2, s[76:77] offset:1536
	global_load_dwordx2 v[204:205], v2, s[76:77] offset:2048
	global_load_dwordx2 v[206:207], v2, s[76:77] offset:2560
	global_load_dwordx2 v[208:209], v2, s[76:77] offset:3072
	global_load_dwordx2 v[210:211], v2, s[76:77] offset:3584
	s_cmp_eq_u32 s45, 0
	s_cbranch_scc1 .Ln1_y0_3
	s_mov_b32 s61, 1
	s_ff1_i32_b32 s0, s45
	s_add_i32 s1, s45, -1
	s_and_b32 s45, s45, s1
	s_nop 0
	v_readlane_b32 s0, v235, s0
	s_nop 3
	s_lshl_b32 s0, s0, 12
	s_add_u32 s76, s64, s0
	s_addc_u32 s77, s65, 0
	global_load_dwordx2 v[212:213], v2, s[76:77]
	global_load_dwordx2 v[214:215], v2, s[76:77] offset:512
	global_load_dwordx2 v[216:217], v2, s[76:77] offset:1024
	global_load_dwordx2 v[218:219], v2, s[76:77] offset:1536
	global_load_dwordx2 v[226:227], v2, s[76:77] offset:2048
	global_load_dwordx2 v[228:229], v2, s[76:77] offset:2560
	global_load_dwordx2 v[230:231], v2, s[76:77] offset:3072
	global_load_dwordx2 v[232:233], v2, s[76:77] offset:3584
.Ln1_y0_3:
	s_add_i32 s11, s10, 0x2000
	s_lshr_b32 s0, s11, 8
	s_mul_i32 s0, s0, 57
	s_lshr_b32 s44, s0, 9
	s_mul_i32 s1, s44, 0x900
	s_sub_i32 s43, s11, s1
	s_lshl_b32 s1, s11, 6
	s_add_u32 s78, s62, s1
	s_addc_u32 s79, s63, 0
	global_load_dword v234, v246, s[78:79]
	s_lshl_b32 s1, s11, 13
	s_add_u32 s12, s48, s1
	s_addc_u32 s13, s49, 0
	s_add_u32 s14, s12, 0x1000
	s_addc_u32 s15, s13, 0
	global_load_dwordx4 v[4:7], v1, s[12:13]
	global_load_dwordx4 v[8:11], v1, s[12:13] offset:1024
	global_load_dwordx4 v[12:15], v1, s[12:13] offset:2048
	global_load_dwordx4 v[16:19], v1, s[12:13] offset:3072
	global_load_dwordx4 v[20:23], v1, s[14:15]
	global_load_dwordx4 v[24:27], v1, s[14:15] offset:1024
	global_load_dwordx4 v[28:31], v1, s[14:15] offset:2048
	global_load_dwordx4 v[32:35], v1, s[14:15] offset:3072
	s_waitcnt vmcnt(9)
	s_cmp_eq_u32 s47, 0
	s_cbranch_scc1 .Ln1_a1_3
	v_lshlrev_b32_e32 v238, 16, v196
	v_and_b32_e32 v239, 0xffff0000, v196
	v_fmac_f32_e32 v36, v68, v238
	v_fmac_f32_e32 v37, v69, v239
	v_lshlrev_b32_e32 v238, 16, v197
	v_and_b32_e32 v239, 0xffff0000, v197
	v_fmac_f32_e32 v38, v70, v238
	v_fmac_f32_e32 v39, v71, v239
	v_lshlrev_b32_e32 v238, 16, v198
	v_and_b32_e32 v239, 0xffff0000, v198
	v_fmac_f32_e32 v40, v72, v238
	v_fmac_f32_e32 v41, v73, v239
	v_lshlrev_b32_e32 v238, 16, v199
	v_and_b32_e32 v239, 0xffff0000, v199
	v_fmac_f32_e32 v42, v74, v238
	v_fmac_f32_e32 v43, v75, v239
	v_lshlrev_b32_e32 v238, 16, v200
	v_and_b32_e32 v239, 0xffff0000, v200
	v_fmac_f32_e32 v44, v76, v238
	v_fmac_f32_e32 v45, v77, v239
	v_lshlrev_b32_e32 v238, 16, v201
	v_and_b32_e32 v239, 0xffff0000, v201
	v_fmac_f32_e32 v46, v78, v238
	v_fmac_f32_e32 v47, v79, v239
	v_lshlrev_b32_e32 v238, 16, v202
	v_and_b32_e32 v239, 0xffff0000, v202
	v_fmac_f32_e32 v48, v80, v238
	v_fmac_f32_e32 v49, v81, v239
	v_lshlrev_b32_e32 v238, 16, v203
	v_and_b32_e32 v239, 0xffff0000, v203
	v_fmac_f32_e32 v50, v82, v238
	v_fmac_f32_e32 v51, v83, v239
	v_lshlrev_b32_e32 v238, 16, v204
	v_and_b32_e32 v239, 0xffff0000, v204
	v_fmac_f32_e32 v52, v84, v238
	v_fmac_f32_e32 v53, v85, v239
	v_lshlrev_b32_e32 v238, 16, v205
	v_and_b32_e32 v239, 0xffff0000, v205
	v_fmac_f32_e32 v54, v86, v238
	v_fmac_f32_e32 v55, v87, v239
	v_lshlrev_b32_e32 v238, 16, v206
	v_and_b32_e32 v239, 0xffff0000, v206
	v_fmac_f32_e32 v56, v88, v238
	v_fmac_f32_e32 v57, v89, v239
	v_lshlrev_b32_e32 v238, 16, v207
	v_and_b32_e32 v239, 0xffff0000, v207
	v_fmac_f32_e32 v58, v90, v238
	v_fmac_f32_e32 v59, v91, v239
	v_lshlrev_b32_e32 v238, 16, v208
	v_and_b32_e32 v239, 0xffff0000, v208
	v_fmac_f32_e32 v60, v92, v238
	v_fmac_f32_e32 v61, v93, v239
	v_lshlrev_b32_e32 v238, 16, v209
	v_and_b32_e32 v239, 0xffff0000, v209
	v_fmac_f32_e32 v62, v94, v238
	v_fmac_f32_e32 v63, v95, v239
	v_lshlrev_b32_e32 v238, 16, v210
	v_and_b32_e32 v239, 0xffff0000, v210
	v_fmac_f32_e32 v64, v96, v238
	v_fmac_f32_e32 v65, v97, v239
	v_lshlrev_b32_e32 v238, 16, v211
	v_and_b32_e32 v239, 0xffff0000, v211
	v_fmac_f32_e32 v66, v98, v238
	v_fmac_f32_e32 v67, v99, v239

.Ln1_gd_3:
	global_store_dwordx4 v1, v[36:39], s[16:17]
	global_store_dwordx4 v1, v[40:43], s[16:17] offset:1024
	global_store_dwordx4 v1, v[44:47], s[16:17] offset:2048
	global_store_dwordx4 v1, v[48:51], s[16:17] offset:3072
	global_store_dwordx4 v1, v[52:55], s[18:19]
	global_store_dwordx4 v1, v[56:59], s[18:19] offset:1024
	global_store_dwordx4 v1, v[60:63], s[18:19] offset:2048
	global_store_dwordx4 v1, v[64:67], s[18:19] offset:3072
	v_mul_f32_e32 v236, v36, v36
	v_fmac_f32_e32 v236, v37, v37
	v_fmac_f32_e32 v236, v38, v38
	v_fmac_f32_e32 v236, v39, v39
	v_fmac_f32_e32 v236, v40, v40
	v_fmac_f32_e32 v236, v41, v41
	v_fmac_f32_e32 v236, v42, v42
	v_fmac_f32_e32 v236, v43, v43
	v_fmac_f32_e32 v236, v44, v44
	v_fmac_f32_e32 v236, v45, v45
	v_fmac_f32_e32 v236, v46, v46
	v_fmac_f32_e32 v236, v47, v47
	v_fmac_f32_e32 v236, v48, v48
	v_fmac_f32_e32 v236, v49, v49
	v_fmac_f32_e32 v236, v50, v50
	v_fmac_f32_e32 v236, v51, v51
	v_fmac_f32_e32 v236, v52, v52
	v_fmac_f32_e32 v236, v53, v53
	v_fmac_f32_e32 v236, v54, v54
	v_fmac_f32_e32 v236, v55, v55
	v_fmac_f32_e32 v236, v56, v56
	v_fmac_f32_e32 v236, v57, v57
	v_fmac_f32_e32 v236, v58, v58
	v_fmac_f32_e32 v236, v59, v59
	v_fmac_f32_e32 v236, v60, v60
	v_fmac_f32_e32 v236, v61, v61
	v_fmac_f32_e32 v236, v62, v62
	v_fmac_f32_e32 v236, v63, v63
	v_fmac_f32_e32 v236, v64, v64
	v_fmac_f32_e32 v236, v65, v65
	v_fmac_f32_e32 v236, v66, v66
	v_fmac_f32_e32 v236, v67, v67
	v_fma_f32 v100, v100, v132, v100
	v_fma_f32 v101, v101, v133, v101
	v_fma_f32 v102, v102, v134, v102
	v_fma_f32 v103, v103, v135, v103
	v_fma_f32 v104, v104, v136, v104
	v_fma_f32 v105, v105, v137, v105
	v_fma_f32 v106, v106, v138, v106
	v_fma_f32 v107, v107, v139, v107
	v_fma_f32 v108, v108, v140, v108
	v_fma_f32 v109, v109, v141, v109
	v_fma_f32 v110, v110, v142, v110
	v_fma_f32 v111, v111, v143, v111
	v_fma_f32 v112, v112, v144, v112
	v_fma_f32 v113, v113, v145, v113
	v_fma_f32 v114, v114, v146, v114
	v_fma_f32 v115, v115, v147, v115
	v_fma_f32 v116, v116, v148, v116
	v_fma_f32 v117, v117, v149, v117
	v_fma_f32 v118, v118, v150, v118
	v_fma_f32 v119, v119, v151, v119
	v_fma_f32 v120, v120, v152, v120
	v_fma_f32 v121, v121, v153, v121
	v_fma_f32 v122, v122, v154, v122
	v_fma_f32 v123, v123, v155, v123
	v_fma_f32 v124, v124, v156, v124
	v_fma_f32 v125, v125, v157, v125
	v_fma_f32 v126, v126, v158, v126
	v_fma_f32 v127, v127, v159, v127
	v_fma_f32 v128, v128, v160, v128
	v_fma_f32 v129, v129, v161, v129
	v_fma_f32 v130, v130, v162, v130
	v_fma_f32 v131, v131, v163, v131
	s_nop 1
	v_add_f32_dpp v236, v236, v236 quad_perm:[1,0,3,2] row_mask:0xf bank_mask:0xf
	s_nop 1
	v_add_f32_dpp v236, v236, v236 quad_perm:[2,3,0,1] row_mask:0xf bank_mask:0xf
	s_nop 1
	v_add_f32_dpp v236, v236, v236 row_half_mirror row_mask:0xf bank_mask:0xf
	s_nop 1
	v_add_f32_dpp v236, v236, v236 row_mirror row_mask:0xf bank_mask:0xf
	s_nop 1
	v_readlane_b32 s0, v236, 0
	v_readlane_b32 s1, v236, 16
	v_readlane_b32 s2, v236, 32
	v_readlane_b32 s3, v236, 48
	s_nop 3
	v_mov_b32_e32 v237, s0
	v_add_f32_e32 v237, s1, v237
	v_add_f32_e32 v237, s2, v237
	v_add_f32_e32 v237, s3, v237
	v_mul_f32_e32 v237, 0x3a000000, v237
	v_add_f32_e32 v237, 0x358637bd, v237
	v_rsq_f32_e32 v237, v237
	s_nop 0
	v_mul_f32_e32 v100, v100, v237
	v_mul_f32_e32 v101, v101, v237
	v_mul_f32_e32 v102, v102, v237
	v_mul_f32_e32 v103, v103, v237
	v_mul_f32_e32 v104, v104, v237
	v_mul_f32_e32 v105, v105, v237
	v_mul_f32_e32 v106, v106, v237
	v_mul_f32_e32 v107, v107, v237
	v_mul_f32_e32 v108, v108, v237
	v_mul_f32_e32 v109, v109, v237
	v_mul_f32_e32 v110, v110, v237
	v_mul_f32_e32 v111, v111, v237
	v_mul_f32_e32 v112, v112, v237
	v_mul_f32_e32 v113, v113, v237
	v_mul_f32_e32 v114, v114, v237
	v_mul_f32_e32 v115, v115, v237
	v_mul_f32_e32 v116, v116, v237
	v_mul_f32_e32 v117, v117, v237
	v_mul_f32_e32 v118, v118, v237
	v_mul_f32_e32 v119, v119, v237
	v_mul_f32_e32 v120, v120, v237
	v_mul_f32_e32 v121, v121, v237
	v_mul_f32_e32 v122, v122, v237
	v_mul_f32_e32 v123, v123, v237
	v_mul_f32_e32 v124, v124, v237
	v_mul_f32_e32 v125, v125, v237
	v_mul_f32_e32 v126, v126, v237
	v_mul_f32_e32 v127, v127, v237
	v_mul_f32_e32 v128, v128, v237
	v_mul_f32_e32 v129, v129, v237
	v_mul_f32_e32 v130, v130, v237
	v_mul_f32_e32 v131, v131, v237
	v_fma_f32 v36, v36, v100, v164
	v_fma_f32 v37, v37, v101, v165
	v_fma_f32 v38, v38, v102, v166
	v_fma_f32 v39, v39, v103, v167
	v_cvt_pk_bf16_f32 v238, v36, v37
	v_cvt_pk_bf16_f32 v239, v38, v39
	global_store_dwordx2 v2, v[238:239], s[22:23]
	v_fma_f32 v40, v40, v104, v168
	v_fma_f32 v41, v41, v105, v169
	v_fma_f32 v42, v42, v106, v170
	v_fma_f32 v43, v43, v107, v171
	v_cvt_pk_bf16_f32 v240, v40, v41
	v_cvt_pk_bf16_f32 v241, v42, v43
	global_store_dwordx2 v2, v[240:241], s[22:23] offset:512
	v_fma_f32 v44, v44, v108, v172
	v_fma_f32 v45, v45, v109, v173
	v_fma_f32 v46, v46, v110, v174
	v_fma_f32 v47, v47, v111, v175
	v_cvt_pk_bf16_f32 v238, v44, v45
	v_cvt_pk_bf16_f32 v239, v46, v47
	global_store_dwordx2 v2, v[238:239], s[22:23] offset:1024
	v_fma_f32 v48, v48, v112, v176
	v_fma_f32 v49, v49, v113, v177
	v_fma_f32 v50, v50, v114, v178
	v_fma_f32 v51, v51, v115, v179
	v_cvt_pk_bf16_f32 v240, v48, v49
	v_cvt_pk_bf16_f32 v241, v50, v51
	global_store_dwordx2 v2, v[240:241], s[22:23] offset:1536
	v_fma_f32 v52, v52, v116, v180
	v_fma_f32 v53, v53, v117, v181
	v_fma_f32 v54, v54, v118, v182
	v_fma_f32 v55, v55, v119, v183
	v_cvt_pk_bf16_f32 v238, v52, v53
	v_cvt_pk_bf16_f32 v239, v54, v55
	global_store_dwordx2 v2, v[238:239], s[22:23] offset:2048
	v_fma_f32 v56, v56, v120, v184
	v_fma_f32 v57, v57, v121, v185
	v_fma_f32 v58, v58, v122, v186
	v_fma_f32 v59, v59, v123, v187
	v_cvt_pk_bf16_f32 v240, v56, v57
	v_cvt_pk_bf16_f32 v241, v58, v59
	global_store_dwordx2 v2, v[240:241], s[22:23] offset:2560
	v_fma_f32 v60, v60, v124, v188
	v_fma_f32 v61, v61, v125, v189
	v_fma_f32 v62, v62, v126, v190
	v_fma_f32 v63, v63, v127, v191
	v_cvt_pk_bf16_f32 v238, v60, v61
	v_cvt_pk_bf16_f32 v239, v62, v63
	global_store_dwordx2 v2, v[238:239], s[22:23] offset:3072
	v_fma_f32 v64, v64, v128, v192
	v_fma_f32 v65, v65, v129, v193
	v_fma_f32 v66, v66, v130, v194
	v_fma_f32 v67, v67, v131, v195
	v_cvt_pk_bf16_f32 v240, v64, v65
	v_cvt_pk_bf16_f32 v241, v66, v67
	global_store_dwordx2 v2, v[240:241], s[22:23] offset:3584
	s_add_i32 s11, s10, 0x2000
	s_lshr_b32 s0, s11, 8
	s_mul_i32 s0, s0, 57
	s_lshr_b32 s44, s0, 9
	s_mul_i32 s1, s44, 0x900
	s_sub_i32 s43, s11, s1
	s_lshl_b32 s1, s11, 13
	s_add_u32 s16, s48, s1
	s_addc_u32 s17, s49, 0
	s_add_u32 s18, s16, 0x1000
	s_addc_u32 s19, s17, 0
	s_lshl_b32 s1, s11, 12
	s_add_u32 s22, s50, s1
	s_addc_u32 s23, s51, 0
	s_cmpk_lt_u32 s43, 0x100
	s_cselect_b32 s0, 8, s44
	s_mul_i32 s1, s0, 0xc000
	s_add_u32 s28, s52, s1
	s_addc_u32 s29, s53, 0
	s_add_u32 s30, s28, 0x1000
	s_addc_u32 s31, s29, 0
	s_add_u32 s72, s54, s1
	s_addc_u32 s73, s55, 0
	s_add_u32 s72, s72, 0xa000
	s_addc_u32 s73, s73, 0
	s_add_u32 s74, s72, 0x1000
	s_addc_u32 s75, s73, 0
	global_load_dwordx4 v[68:71], v1, s[72:73]
	global_load_dwordx4 v[100:103], v1, s[56:57]
	global_load_dwordx4 v[72:75], v1, s[72:73] offset:1024
	global_load_dwordx4 v[104:107], v1, s[56:57] offset:1024
	global_load_dwordx4 v[76:79], v1, s[72:73] offset:2048
	global_load_dwordx4 v[108:111], v1, s[56:57] offset:2048
	global_load_dwordx4 v[80:83], v1, s[72:73] offset:3072
	global_load_dwordx4 v[112:115], v1, s[56:57] offset:3072
	global_load_dwordx4 v[84:87], v1, s[74:75]
	global_load_dwordx4 v[116:119], v1, s[58:59]
	global_load_dwordx4 v[88:91], v1, s[74:75] offset:1024
	global_load_dwordx4 v[120:123], v1, s[58:59] offset:1024
	global_load_dwordx4 v[92:95], v1, s[74:75] offset:2048
	global_load_dwordx4 v[124:127], v1, s[58:59] offset:2048
	global_load_dwordx4 v[96:99], v1, s[74:75] offset:3072
	global_load_dwordx4 v[128:131], v1, s[58:59] offset:3072
	s_add_u32 s84, s28, 0x2000
	s_addc_u32 s85, s29, 0
	s_add_u32 s86, s28, 0x3000
	s_addc_u32 s87, s29, 0
	global_load_dwordx4 v[164:167], v1, s[28:29]
	global_load_dwordx4 v[132:135], v1, s[84:85]
	global_load_dwordx4 v[168:171], v1, s[28:29] offset:1024
	global_load_dwordx4 v[136:139], v1, s[84:85] offset:1024
	global_load_dwordx4 v[172:175], v1, s[28:29] offset:2048
	global_load_dwordx4 v[140:143], v1, s[84:85] offset:2048
	global_load_dwordx4 v[176:179], v1, s[28:29] offset:3072
	global_load_dwordx4 v[144:147], v1, s[84:85] offset:3072
	global_load_dwordx4 v[180:183], v1, s[30:31]
	global_load_dwordx4 v[148:151], v1, s[86:87]
	global_load_dwordx4 v[184:187], v1, s[30:31] offset:1024
	global_load_dwordx4 v[152:155], v1, s[86:87] offset:1024
	global_load_dwordx4 v[188:191], v1, s[30:31] offset:2048
	global_load_dwordx4 v[156:159], v1, s[86:87] offset:2048
	global_load_dwordx4 v[192:195], v1, s[30:31] offset:3072
	global_load_dwordx4 v[160:163], v1, s[86:87] offset:3072
	s_waitcnt vmcnt(56)
	v_cmp_le_i32_e64 s[0:1], 0, v234
	s_nop 1
	s_and_b32 s45, s0, 0xffff
	s_mov_b32 s47, 0
	s_mov_b32 s61, 0
	s_cmp_eq_u32 s45, 0
	s_cbranch_scc1 .Ln1_y0_4
	s_mov_b32 s47, 1
	s_ff1_i32_b32 s0, s45
	s_add_i32 s1, s45, -1
	s_and_b32 s45, s45, s1
	s_nop 0
	v_readlane_b32 s0, v234, s0
	s_nop 3
	s_lshl_b32 s0, s0, 12
	s_add_u32 s76, s64, s0
	s_addc_u32 s77, s65, 0
	global_load_dwordx2 v[196:197], v2, s[76:77]
	global_load_dwordx2 v[198:199], v2, s[76:77] offset:512
	global_load_dwordx2 v[200:201], v2, s[76:77] offset:1024
	global_load_dwordx2 v[202:203], v2, s[76:77] offset:1536
	global_load_dwordx2 v[204:205], v2, s[76:77] offset:2048
	global_load_dwordx2 v[206:207], v2, s[76:77] offset:2560
	global_load_dwordx2 v[208:209], v2, s[76:77] offset:3072
	global_load_dwordx2 v[210:211], v2, s[76:77] offset:3584
	s_cmp_eq_u32 s45, 0
	s_cbranch_scc1 .Ln1_y0_4
	s_mov_b32 s61, 1
	s_ff1_i32_b32 s0, s45
	s_add_i32 s1, s45, -1
	s_and_b32 s45, s45, s1
	s_nop 0
	v_readlane_b32 s0, v234, s0
	s_nop 3
	s_lshl_b32 s0, s0, 12
	s_add_u32 s76, s64, s0
	s_addc_u32 s77, s65, 0
	global_load_dwordx2 v[212:213], v2, s[76:77]
	global_load_dwordx2 v[214:215], v2, s[76:77] offset:512
	global_load_dwordx2 v[216:217], v2, s[76:77] offset:1024
	global_load_dwordx2 v[218:219], v2, s[76:77] offset:1536
	global_load_dwordx2 v[226:227], v2, s[76:77] offset:2048
	global_load_dwordx2 v[228:229], v2, s[76:77] offset:2560
	global_load_dwordx2 v[230:231], v2, s[76:77] offset:3072
	global_load_dwordx2 v[232:233], v2, s[76:77] offset:3584
.Ln1_y0_4:
	s_add_i32 s11, s10, 0x2800
	s_lshr_b32 s0, s11, 8
	s_mul_i32 s0, s0, 57
	s_lshr_b32 s44, s0, 9
	s_mul_i32 s1, s44, 0x900
	s_sub_i32 s43, s11, s1
	s_lshl_b32 s1, s11, 6
	s_add_u32 s78, s62, s1
	s_addc_u32 s79, s63, 0
	global_load_dword v235, v246, s[78:79]
	s_lshl_b32 s1, s11, 13
	s_add_u32 s12, s48, s1
	s_addc_u32 s13, s49, 0
	s_add_u32 s14, s12, 0x1000
	s_addc_u32 s15, s13, 0
	global_load_dwordx4 v[36:39], v1, s[12:13]
	global_load_dwordx4 v[40:43], v1, s[12:13] offset:1024
	global_load_dwordx4 v[44:47], v1, s[12:13] offset:2048
	global_load_dwordx4 v[48:51], v1, s[12:13] offset:3072
	global_load_dwordx4 v[52:55], v1, s[14:15]
	global_load_dwordx4 v[56:59], v1, s[14:15] offset:1024
	global_load_dwordx4 v[60:63], v1, s[14:15] offset:2048
	global_load_dwordx4 v[64:67], v1, s[14:15] offset:3072
	s_waitcnt vmcnt(9)
	s_cmp_eq_u32 s47, 0
	s_cbranch_scc1 .Ln1_a1_4
	v_lshlrev_b32_e32 v238, 16, v196
	v_and_b32_e32 v239, 0xffff0000, v196
	v_fmac_f32_e32 v4, v68, v238
	v_fmac_f32_e32 v5, v69, v239
	v_lshlrev_b32_e32 v238, 16, v197
	v_and_b32_e32 v239, 0xffff0000, v197
	v_fmac_f32_e32 v6, v70, v238
	v_fmac_f32_e32 v7, v71, v239
	v_lshlrev_b32_e32 v238, 16, v198
	v_and_b32_e32 v239, 0xffff0000, v198
	v_fmac_f32_e32 v8, v72, v238
	v_fmac_f32_e32 v9, v73, v239
	v_lshlrev_b32_e32 v238, 16, v199
	v_and_b32_e32 v239, 0xffff0000, v199
	v_fmac_f32_e32 v10, v74, v238
	v_fmac_f32_e32 v11, v75, v239
	v_lshlrev_b32_e32 v238, 16, v200
	v_and_b32_e32 v239, 0xffff0000, v200
	v_fmac_f32_e32 v12, v76, v238
	v_fmac_f32_e32 v13, v77, v239
	v_lshlrev_b32_e32 v238, 16, v201
	v_and_b32_e32 v239, 0xffff0000, v201
	v_fmac_f32_e32 v14, v78, v238
	v_fmac_f32_e32 v15, v79, v239
	v_lshlrev_b32_e32 v238, 16, v202
	v_and_b32_e32 v239, 0xffff0000, v202
	v_fmac_f32_e32 v16, v80, v238
	v_fmac_f32_e32 v17, v81, v239
	v_lshlrev_b32_e32 v238, 16, v203
	v_and_b32_e32 v239, 0xffff0000, v203
	v_fmac_f32_e32 v18, v82, v238
	v_fmac_f32_e32 v19, v83, v239
	v_lshlrev_b32_e32 v238, 16, v204
	v_and_b32_e32 v239, 0xffff0000, v204
	v_fmac_f32_e32 v20, v84, v238
	v_fmac_f32_e32 v21, v85, v239
	v_lshlrev_b32_e32 v238, 16, v205
	v_and_b32_e32 v239, 0xffff0000, v205
	v_fmac_f32_e32 v22, v86, v238
	v_fmac_f32_e32 v23, v87, v239
	v_lshlrev_b32_e32 v238, 16, v206
	v_and_b32_e32 v239, 0xffff0000, v206
	v_fmac_f32_e32 v24, v88, v238
	v_fmac_f32_e32 v25, v89, v239
	v_lshlrev_b32_e32 v238, 16, v207
	v_and_b32_e32 v239, 0xffff0000, v207
	v_fmac_f32_e32 v26, v90, v238
	v_fmac_f32_e32 v27, v91, v239
	v_lshlrev_b32_e32 v238, 16, v208
	v_and_b32_e32 v239, 0xffff0000, v208
	v_fmac_f32_e32 v28, v92, v238
	v_fmac_f32_e32 v29, v93, v239
	v_lshlrev_b32_e32 v238, 16, v209
	v_and_b32_e32 v239, 0xffff0000, v209
	v_fmac_f32_e32 v30, v94, v238
	v_fmac_f32_e32 v31, v95, v239
	v_lshlrev_b32_e32 v238, 16, v210
	v_and_b32_e32 v239, 0xffff0000, v210
	v_fmac_f32_e32 v32, v96, v238
	v_fmac_f32_e32 v33, v97, v239
	v_lshlrev_b32_e32 v238, 16, v211
	v_and_b32_e32 v239, 0xffff0000, v211
	v_fmac_f32_e32 v34, v98, v238
	v_fmac_f32_e32 v35, v99, v239

.Ln1_gd_4:
	global_store_dwordx4 v1, v[4:7], s[16:17]
	global_store_dwordx4 v1, v[8:11], s[16:17] offset:1024
	global_store_dwordx4 v1, v[12:15], s[16:17] offset:2048
	global_store_dwordx4 v1, v[16:19], s[16:17] offset:3072
	global_store_dwordx4 v1, v[20:23], s[18:19]
	global_store_dwordx4 v1, v[24:27], s[18:19] offset:1024
	global_store_dwordx4 v1, v[28:31], s[18:19] offset:2048
	global_store_dwordx4 v1, v[32:35], s[18:19] offset:3072
	v_mul_f32_e32 v236, v4, v4
	v_fmac_f32_e32 v236, v5, v5
	v_fmac_f32_e32 v236, v6, v6
	v_fmac_f32_e32 v236, v7, v7
	v_fmac_f32_e32 v236, v8, v8
	v_fmac_f32_e32 v236, v9, v9
	v_fmac_f32_e32 v236, v10, v10
	v_fmac_f32_e32 v236, v11, v11
	v_fmac_f32_e32 v236, v12, v12
	v_fmac_f32_e32 v236, v13, v13
	v_fmac_f32_e32 v236, v14, v14
	v_fmac_f32_e32 v236, v15, v15
	v_fmac_f32_e32 v236, v16, v16
	v_fmac_f32_e32 v236, v17, v17
	v_fmac_f32_e32 v236, v18, v18
	v_fmac_f32_e32 v236, v19, v19
	v_fmac_f32_e32 v236, v20, v20
	v_fmac_f32_e32 v236, v21, v21
	v_fmac_f32_e32 v236, v22, v22
	v_fmac_f32_e32 v236, v23, v23
	v_fmac_f32_e32 v236, v24, v24
	v_fmac_f32_e32 v236, v25, v25
	v_fmac_f32_e32 v236, v26, v26
	v_fmac_f32_e32 v236, v27, v27
	v_fmac_f32_e32 v236, v28, v28
	v_fmac_f32_e32 v236, v29, v29
	v_fmac_f32_e32 v236, v30, v30
	v_fmac_f32_e32 v236, v31, v31
	v_fmac_f32_e32 v236, v32, v32
	v_fmac_f32_e32 v236, v33, v33
	v_fmac_f32_e32 v236, v34, v34
	v_fmac_f32_e32 v236, v35, v35
	v_fma_f32 v100, v100, v132, v100
	v_fma_f32 v101, v101, v133, v101
	v_fma_f32 v102, v102, v134, v102
	v_fma_f32 v103, v103, v135, v103
	v_fma_f32 v104, v104, v136, v104
	v_fma_f32 v105, v105, v137, v105
	v_fma_f32 v106, v106, v138, v106
	v_fma_f32 v107, v107, v139, v107
	v_fma_f32 v108, v108, v140, v108
	v_fma_f32 v109, v109, v141, v109
	v_fma_f32 v110, v110, v142, v110
	v_fma_f32 v111, v111, v143, v111
	v_fma_f32 v112, v112, v144, v112
	v_fma_f32 v113, v113, v145, v113
	v_fma_f32 v114, v114, v146, v114
	v_fma_f32 v115, v115, v147, v115
	v_fma_f32 v116, v116, v148, v116
	v_fma_f32 v117, v117, v149, v117
	v_fma_f32 v118, v118, v150, v118
	v_fma_f32 v119, v119, v151, v119
	v_fma_f32 v120, v120, v152, v120
	v_fma_f32 v121, v121, v153, v121
	v_fma_f32 v122, v122, v154, v122
	v_fma_f32 v123, v123, v155, v123
	v_fma_f32 v124, v124, v156, v124
	v_fma_f32 v125, v125, v157, v125
	v_fma_f32 v126, v126, v158, v126
	v_fma_f32 v127, v127, v159, v127
	v_fma_f32 v128, v128, v160, v128
	v_fma_f32 v129, v129, v161, v129
	v_fma_f32 v130, v130, v162, v130
	v_fma_f32 v131, v131, v163, v131
	s_nop 1
	v_add_f32_dpp v236, v236, v236 quad_perm:[1,0,3,2] row_mask:0xf bank_mask:0xf
	s_nop 1
	v_add_f32_dpp v236, v236, v236 quad_perm:[2,3,0,1] row_mask:0xf bank_mask:0xf
	s_nop 1
	v_add_f32_dpp v236, v236, v236 row_half_mirror row_mask:0xf bank_mask:0xf
	s_nop 1
	v_add_f32_dpp v236, v236, v236 row_mirror row_mask:0xf bank_mask:0xf
	s_nop 1
	v_readlane_b32 s0, v236, 0
	v_readlane_b32 s1, v236, 16
	v_readlane_b32 s2, v236, 32
	v_readlane_b32 s3, v236, 48
	s_nop 3
	v_mov_b32_e32 v237, s0
	v_add_f32_e32 v237, s1, v237
	v_add_f32_e32 v237, s2, v237
	v_add_f32_e32 v237, s3, v237
	v_mul_f32_e32 v237, 0x3a000000, v237
	v_add_f32_e32 v237, 0x358637bd, v237
	v_rsq_f32_e32 v237, v237
	s_nop 0
	v_mul_f32_e32 v100, v100, v237
	v_mul_f32_e32 v101, v101, v237
	v_mul_f32_e32 v102, v102, v237
	v_mul_f32_e32 v103, v103, v237
	v_mul_f32_e32 v104, v104, v237
	v_mul_f32_e32 v105, v105, v237
	v_mul_f32_e32 v106, v106, v237
	v_mul_f32_e32 v107, v107, v237
	v_mul_f32_e32 v108, v108, v237
	v_mul_f32_e32 v109, v109, v237
	v_mul_f32_e32 v110, v110, v237
	v_mul_f32_e32 v111, v111, v237
	v_mul_f32_e32 v112, v112, v237
	v_mul_f32_e32 v113, v113, v237
	v_mul_f32_e32 v114, v114, v237
	v_mul_f32_e32 v115, v115, v237
	v_mul_f32_e32 v116, v116, v237
	v_mul_f32_e32 v117, v117, v237
	v_mul_f32_e32 v118, v118, v237
	v_mul_f32_e32 v119, v119, v237
	v_mul_f32_e32 v120, v120, v237
	v_mul_f32_e32 v121, v121, v237
	v_mul_f32_e32 v122, v122, v237
	v_mul_f32_e32 v123, v123, v237
	v_mul_f32_e32 v124, v124, v237
	v_mul_f32_e32 v125, v125, v237
	v_mul_f32_e32 v126, v126, v237
	v_mul_f32_e32 v127, v127, v237
	v_mul_f32_e32 v128, v128, v237
	v_mul_f32_e32 v129, v129, v237
	v_mul_f32_e32 v130, v130, v237
	v_mul_f32_e32 v131, v131, v237
	v_fma_f32 v4, v4, v100, v164
	v_fma_f32 v5, v5, v101, v165
	v_fma_f32 v6, v6, v102, v166
	v_fma_f32 v7, v7, v103, v167
	v_cvt_pk_bf16_f32 v238, v4, v5
	v_cvt_pk_bf16_f32 v239, v6, v7
	global_store_dwordx2 v2, v[238:239], s[22:23]
	v_fma_f32 v8, v8, v104, v168
	v_fma_f32 v9, v9, v105, v169
	v_fma_f32 v10, v10, v106, v170
	v_fma_f32 v11, v11, v107, v171
	v_cvt_pk_bf16_f32 v240, v8, v9
	v_cvt_pk_bf16_f32 v241, v10, v11
	global_store_dwordx2 v2, v[240:241], s[22:23] offset:512
	v_fma_f32 v12, v12, v108, v172
	v_fma_f32 v13, v13, v109, v173
	v_fma_f32 v14, v14, v110, v174
	v_fma_f32 v15, v15, v111, v175
	v_cvt_pk_bf16_f32 v238, v12, v13
	v_cvt_pk_bf16_f32 v239, v14, v15
	global_store_dwordx2 v2, v[238:239], s[22:23] offset:1024
	v_fma_f32 v16, v16, v112, v176
	v_fma_f32 v17, v17, v113, v177
	v_fma_f32 v18, v18, v114, v178
	v_fma_f32 v19, v19, v115, v179
	v_cvt_pk_bf16_f32 v240, v16, v17
	v_cvt_pk_bf16_f32 v241, v18, v19
	global_store_dwordx2 v2, v[240:241], s[22:23] offset:1536
	v_fma_f32 v20, v20, v116, v180
	v_fma_f32 v21, v21, v117, v181
	v_fma_f32 v22, v22, v118, v182
	v_fma_f32 v23, v23, v119, v183
	v_cvt_pk_bf16_f32 v238, v20, v21
	v_cvt_pk_bf16_f32 v239, v22, v23
	global_store_dwordx2 v2, v[238:239], s[22:23] offset:2048
	v_fma_f32 v24, v24, v120, v184
	v_fma_f32 v25, v25, v121, v185
	v_fma_f32 v26, v26, v122, v186
	v_fma_f32 v27, v27, v123, v187
	v_cvt_pk_bf16_f32 v240, v24, v25
	v_cvt_pk_bf16_f32 v241, v26, v27
	global_store_dwordx2 v2, v[240:241], s[22:23] offset:2560
	v_fma_f32 v28, v28, v124, v188
	v_fma_f32 v29, v29, v125, v189
	v_fma_f32 v30, v30, v126, v190
	v_fma_f32 v31, v31, v127, v191
	v_cvt_pk_bf16_f32 v238, v28, v29
	v_cvt_pk_bf16_f32 v239, v30, v31
	global_store_dwordx2 v2, v[238:239], s[22:23] offset:3072
	v_fma_f32 v32, v32, v128, v192
	v_fma_f32 v33, v33, v129, v193
	v_fma_f32 v34, v34, v130, v194
	v_fma_f32 v35, v35, v131, v195
	v_cvt_pk_bf16_f32 v240, v32, v33
	v_cvt_pk_bf16_f32 v241, v34, v35
	global_store_dwordx2 v2, v[240:241], s[22:23] offset:3584
	s_add_i32 s11, s10, 0x2800
	s_lshr_b32 s0, s11, 8
	s_mul_i32 s0, s0, 57
	s_lshr_b32 s44, s0, 9
	s_mul_i32 s1, s44, 0x900
	s_sub_i32 s43, s11, s1
	s_lshl_b32 s1, s11, 13
	s_add_u32 s16, s48, s1
	s_addc_u32 s17, s49, 0
	s_add_u32 s18, s16, 0x1000
	s_addc_u32 s19, s17, 0
	s_lshl_b32 s1, s11, 12
	s_add_u32 s22, s50, s1
	s_addc_u32 s23, s51, 0
	s_cmpk_lt_u32 s43, 0x100
	s_cselect_b32 s0, 8, s44
	s_mul_i32 s1, s0, 0xc000
	s_add_u32 s28, s52, s1
	s_addc_u32 s29, s53, 0
	s_add_u32 s30, s28, 0x1000
	s_addc_u32 s31, s29, 0
	s_add_u32 s72, s54, s1
	s_addc_u32 s73, s55, 0
	s_add_u32 s72, s72, 0xa000
	s_addc_u32 s73, s73, 0
	s_add_u32 s74, s72, 0x1000
	s_addc_u32 s75, s73, 0
	global_load_dwordx4 v[68:71], v1, s[72:73]
	global_load_dwordx4 v[100:103], v1, s[56:57]
	global_load_dwordx4 v[72:75], v1, s[72:73] offset:1024
	global_load_dwordx4 v[104:107], v1, s[56:57] offset:1024
	global_load_dwordx4 v[76:79], v1, s[72:73] offset:2048
	global_load_dwordx4 v[108:111], v1, s[56:57] offset:2048
	global_load_dwordx4 v[80:83], v1, s[72:73] offset:3072
	global_load_dwordx4 v[112:115], v1, s[56:57] offset:3072
	global_load_dwordx4 v[84:87], v1, s[74:75]
	global_load_dwordx4 v[116:119], v1, s[58:59]
	global_load_dwordx4 v[88:91], v1, s[74:75] offset:1024
	global_load_dwordx4 v[120:123], v1, s[58:59] offset:1024
	global_load_dwordx4 v[92:95], v1, s[74:75] offset:2048
	global_load_dwordx4 v[124:127], v1, s[58:59] offset:2048
	global_load_dwordx4 v[96:99], v1, s[74:75] offset:3072
	global_load_dwordx4 v[128:131], v1, s[58:59] offset:3072
	s_add_u32 s84, s28, 0x2000
	s_addc_u32 s85, s29, 0
	s_add_u32 s86, s28, 0x3000
	s_addc_u32 s87, s29, 0
	global_load_dwordx4 v[164:167], v1, s[28:29]
	global_load_dwordx4 v[132:135], v1, s[84:85]
	global_load_dwordx4 v[168:171], v1, s[28:29] offset:1024
	global_load_dwordx4 v[136:139], v1, s[84:85] offset:1024
	global_load_dwordx4 v[172:175], v1, s[28:29] offset:2048
	global_load_dwordx4 v[140:143], v1, s[84:85] offset:2048
	global_load_dwordx4 v[176:179], v1, s[28:29] offset:3072
	global_load_dwordx4 v[144:147], v1, s[84:85] offset:3072
	global_load_dwordx4 v[180:183], v1, s[30:31]
	global_load_dwordx4 v[148:151], v1, s[86:87]
	global_load_dwordx4 v[184:187], v1, s[30:31] offset:1024
	global_load_dwordx4 v[152:155], v1, s[86:87] offset:1024
	global_load_dwordx4 v[188:191], v1, s[30:31] offset:2048
	global_load_dwordx4 v[156:159], v1, s[86:87] offset:2048
	global_load_dwordx4 v[192:195], v1, s[30:31] offset:3072
	global_load_dwordx4 v[160:163], v1, s[86:87] offset:3072
	s_waitcnt vmcnt(56)
	v_cmp_le_i32_e64 s[0:1], 0, v235
	s_nop 1
	s_and_b32 s45, s0, 0xffff
	s_mov_b32 s47, 0
	s_mov_b32 s61, 0
	s_cmp_eq_u32 s45, 0
	s_cbranch_scc1 .Ln1_y0_5
	s_mov_b32 s47, 1
	s_ff1_i32_b32 s0, s45
	s_add_i32 s1, s45, -1
	s_and_b32 s45, s45, s1
	s_nop 0
	v_readlane_b32 s0, v235, s0
	s_nop 3
	s_lshl_b32 s0, s0, 12
	s_add_u32 s76, s64, s0
	s_addc_u32 s77, s65, 0
	global_load_dwordx2 v[196:197], v2, s[76:77]
	global_load_dwordx2 v[198:199], v2, s[76:77] offset:512
	global_load_dwordx2 v[200:201], v2, s[76:77] offset:1024
	global_load_dwordx2 v[202:203], v2, s[76:77] offset:1536
	global_load_dwordx2 v[204:205], v2, s[76:77] offset:2048
	global_load_dwordx2 v[206:207], v2, s[76:77] offset:2560
	global_load_dwordx2 v[208:209], v2, s[76:77] offset:3072
	global_load_dwordx2 v[210:211], v2, s[76:77] offset:3584
	s_cmp_eq_u32 s45, 0
	s_cbranch_scc1 .Ln1_y0_5
	s_mov_b32 s61, 1
	s_ff1_i32_b32 s0, s45
	s_add_i32 s1, s45, -1
	s_and_b32 s45, s45, s1
	s_nop 0
	v_readlane_b32 s0, v235, s0
	s_nop 3
	s_lshl_b32 s0, s0, 12
	s_add_u32 s76, s64, s0
	s_addc_u32 s77, s65, 0
	global_load_dwordx2 v[212:213], v2, s[76:77]
	global_load_dwordx2 v[214:215], v2, s[76:77] offset:512
	global_load_dwordx2 v[216:217], v2, s[76:77] offset:1024
	global_load_dwordx2 v[218:219], v2, s[76:77] offset:1536
	global_load_dwordx2 v[226:227], v2, s[76:77] offset:2048
	global_load_dwordx2 v[228:229], v2, s[76:77] offset:2560
	global_load_dwordx2 v[230:231], v2, s[76:77] offset:3072
	global_load_dwordx2 v[232:233], v2, s[76:77] offset:3584
.Ln1_y0_5:
	s_add_i32 s11, s10, 0x3000
	s_lshr_b32 s0, s11, 8
	s_mul_i32 s0, s0, 57
	s_lshr_b32 s44, s0, 9
	s_mul_i32 s1, s44, 0x900
	s_sub_i32 s43, s11, s1
	s_lshl_b32 s1, s11, 6
	s_add_u32 s78, s62, s1
	s_addc_u32 s79, s63, 0
	global_load_dword v234, v246, s[78:79]
	s_lshl_b32 s1, s11, 13
	s_add_u32 s12, s48, s1
	s_addc_u32 s13, s49, 0
	s_add_u32 s14, s12, 0x1000
	s_addc_u32 s15, s13, 0
	global_load_dwordx4 v[4:7], v1, s[12:13]
	global_load_dwordx4 v[8:11], v1, s[12:13] offset:1024
	global_load_dwordx4 v[12:15], v1, s[12:13] offset:2048
	global_load_dwordx4 v[16:19], v1, s[12:13] offset:3072
	global_load_dwordx4 v[20:23], v1, s[14:15]
	global_load_dwordx4 v[24:27], v1, s[14:15] offset:1024
	global_load_dwordx4 v[28:31], v1, s[14:15] offset:2048
	global_load_dwordx4 v[32:35], v1, s[14:15] offset:3072
	s_waitcnt vmcnt(9)
	s_cmp_eq_u32 s47, 0
	s_cbranch_scc1 .Ln1_a1_5
	v_lshlrev_b32_e32 v238, 16, v196
	v_and_b32_e32 v239, 0xffff0000, v196
	v_fmac_f32_e32 v36, v68, v238
	v_fmac_f32_e32 v37, v69, v239
	v_lshlrev_b32_e32 v238, 16, v197
	v_and_b32_e32 v239, 0xffff0000, v197
	v_fmac_f32_e32 v38, v70, v238
	v_fmac_f32_e32 v39, v71, v239
	v_lshlrev_b32_e32 v238, 16, v198
	v_and_b32_e32 v239, 0xffff0000, v198
	v_fmac_f32_e32 v40, v72, v238
	v_fmac_f32_e32 v41, v73, v239
	v_lshlrev_b32_e32 v238, 16, v199
	v_and_b32_e32 v239, 0xffff0000, v199
	v_fmac_f32_e32 v42, v74, v238
	v_fmac_f32_e32 v43, v75, v239
	v_lshlrev_b32_e32 v238, 16, v200
	v_and_b32_e32 v239, 0xffff0000, v200
	v_fmac_f32_e32 v44, v76, v238
	v_fmac_f32_e32 v45, v77, v239
	v_lshlrev_b32_e32 v238, 16, v201
	v_and_b32_e32 v239, 0xffff0000, v201
	v_fmac_f32_e32 v46, v78, v238
	v_fmac_f32_e32 v47, v79, v239
	v_lshlrev_b32_e32 v238, 16, v202
	v_and_b32_e32 v239, 0xffff0000, v202
	v_fmac_f32_e32 v48, v80, v238
	v_fmac_f32_e32 v49, v81, v239
	v_lshlrev_b32_e32 v238, 16, v203
	v_and_b32_e32 v239, 0xffff0000, v203
	v_fmac_f32_e32 v50, v82, v238
	v_fmac_f32_e32 v51, v83, v239
	v_lshlrev_b32_e32 v238, 16, v204
	v_and_b32_e32 v239, 0xffff0000, v204
	v_fmac_f32_e32 v52, v84, v238
	v_fmac_f32_e32 v53, v85, v239
	v_lshlrev_b32_e32 v238, 16, v205
	v_and_b32_e32 v239, 0xffff0000, v205
	v_fmac_f32_e32 v54, v86, v238
	v_fmac_f32_e32 v55, v87, v239
	v_lshlrev_b32_e32 v238, 16, v206
	v_and_b32_e32 v239, 0xffff0000, v206
	v_fmac_f32_e32 v56, v88, v238
	v_fmac_f32_e32 v57, v89, v239
	v_lshlrev_b32_e32 v238, 16, v207
	v_and_b32_e32 v239, 0xffff0000, v207
	v_fmac_f32_e32 v58, v90, v238
	v_fmac_f32_e32 v59, v91, v239
	v_lshlrev_b32_e32 v238, 16, v208
	v_and_b32_e32 v239, 0xffff0000, v208
	v_fmac_f32_e32 v60, v92, v238
	v_fmac_f32_e32 v61, v93, v239
	v_lshlrev_b32_e32 v238, 16, v209
	v_and_b32_e32 v239, 0xffff0000, v209
	v_fmac_f32_e32 v62, v94, v238
	v_fmac_f32_e32 v63, v95, v239
	v_lshlrev_b32_e32 v238, 16, v210
	v_and_b32_e32 v239, 0xffff0000, v210
	v_fmac_f32_e32 v64, v96, v238
	v_fmac_f32_e32 v65, v97, v239
	v_lshlrev_b32_e32 v238, 16, v211
	v_and_b32_e32 v239, 0xffff0000, v211
	v_fmac_f32_e32 v66, v98, v238
	v_fmac_f32_e32 v67, v99, v239

.Ln1_gd_5:
	global_store_dwordx4 v1, v[36:39], s[16:17]
	global_store_dwordx4 v1, v[40:43], s[16:17] offset:1024
	global_store_dwordx4 v1, v[44:47], s[16:17] offset:2048
	global_store_dwordx4 v1, v[48:51], s[16:17] offset:3072
	global_store_dwordx4 v1, v[52:55], s[18:19]
	global_store_dwordx4 v1, v[56:59], s[18:19] offset:1024
	global_store_dwordx4 v1, v[60:63], s[18:19] offset:2048
	global_store_dwordx4 v1, v[64:67], s[18:19] offset:3072
	v_mul_f32_e32 v236, v36, v36
	v_fmac_f32_e32 v236, v37, v37
	v_fmac_f32_e32 v236, v38, v38
	v_fmac_f32_e32 v236, v39, v39
	v_fmac_f32_e32 v236, v40, v40
	v_fmac_f32_e32 v236, v41, v41
	v_fmac_f32_e32 v236, v42, v42
	v_fmac_f32_e32 v236, v43, v43
	v_fmac_f32_e32 v236, v44, v44
	v_fmac_f32_e32 v236, v45, v45
	v_fmac_f32_e32 v236, v46, v46
	v_fmac_f32_e32 v236, v47, v47
	v_fmac_f32_e32 v236, v48, v48
	v_fmac_f32_e32 v236, v49, v49
	v_fmac_f32_e32 v236, v50, v50
	v_fmac_f32_e32 v236, v51, v51
	v_fmac_f32_e32 v236, v52, v52
	v_fmac_f32_e32 v236, v53, v53
	v_fmac_f32_e32 v236, v54, v54
	v_fmac_f32_e32 v236, v55, v55
	v_fmac_f32_e32 v236, v56, v56
	v_fmac_f32_e32 v236, v57, v57
	v_fmac_f32_e32 v236, v58, v58
	v_fmac_f32_e32 v236, v59, v59
	v_fmac_f32_e32 v236, v60, v60
	v_fmac_f32_e32 v236, v61, v61
	v_fmac_f32_e32 v236, v62, v62
	v_fmac_f32_e32 v236, v63, v63
	v_fmac_f32_e32 v236, v64, v64
	v_fmac_f32_e32 v236, v65, v65
	v_fmac_f32_e32 v236, v66, v66
	v_fmac_f32_e32 v236, v67, v67
	v_fma_f32 v100, v100, v132, v100
	v_fma_f32 v101, v101, v133, v101
	v_fma_f32 v102, v102, v134, v102
	v_fma_f32 v103, v103, v135, v103
	v_fma_f32 v104, v104, v136, v104
	v_fma_f32 v105, v105, v137, v105
	v_fma_f32 v106, v106, v138, v106
	v_fma_f32 v107, v107, v139, v107
	v_fma_f32 v108, v108, v140, v108
	v_fma_f32 v109, v109, v141, v109
	v_fma_f32 v110, v110, v142, v110
	v_fma_f32 v111, v111, v143, v111
	v_fma_f32 v112, v112, v144, v112
	v_fma_f32 v113, v113, v145, v113
	v_fma_f32 v114, v114, v146, v114
	v_fma_f32 v115, v115, v147, v115
	v_fma_f32 v116, v116, v148, v116
	v_fma_f32 v117, v117, v149, v117
	v_fma_f32 v118, v118, v150, v118
	v_fma_f32 v119, v119, v151, v119
	v_fma_f32 v120, v120, v152, v120
	v_fma_f32 v121, v121, v153, v121
	v_fma_f32 v122, v122, v154, v122
	v_fma_f32 v123, v123, v155, v123
	v_fma_f32 v124, v124, v156, v124
	v_fma_f32 v125, v125, v157, v125
	v_fma_f32 v126, v126, v158, v126
	v_fma_f32 v127, v127, v159, v127
	v_fma_f32 v128, v128, v160, v128
	v_fma_f32 v129, v129, v161, v129
	v_fma_f32 v130, v130, v162, v130
	v_fma_f32 v131, v131, v163, v131
	s_nop 1
	v_add_f32_dpp v236, v236, v236 quad_perm:[1,0,3,2] row_mask:0xf bank_mask:0xf
	s_nop 1
	v_add_f32_dpp v236, v236, v236 quad_perm:[2,3,0,1] row_mask:0xf bank_mask:0xf
	s_nop 1
	v_add_f32_dpp v236, v236, v236 row_half_mirror row_mask:0xf bank_mask:0xf
	s_nop 1
	v_add_f32_dpp v236, v236, v236 row_mirror row_mask:0xf bank_mask:0xf
	s_nop 1
	v_readlane_b32 s0, v236, 0
	v_readlane_b32 s1, v236, 16
	v_readlane_b32 s2, v236, 32
	v_readlane_b32 s3, v236, 48
	s_nop 3
	v_mov_b32_e32 v237, s0
	v_add_f32_e32 v237, s1, v237
	v_add_f32_e32 v237, s2, v237
	v_add_f32_e32 v237, s3, v237
	v_mul_f32_e32 v237, 0x3a000000, v237
	v_add_f32_e32 v237, 0x358637bd, v237
	v_rsq_f32_e32 v237, v237
	s_nop 0
	v_mul_f32_e32 v100, v100, v237
	v_mul_f32_e32 v101, v101, v237
	v_mul_f32_e32 v102, v102, v237
	v_mul_f32_e32 v103, v103, v237
	v_mul_f32_e32 v104, v104, v237
	v_mul_f32_e32 v105, v105, v237
	v_mul_f32_e32 v106, v106, v237
	v_mul_f32_e32 v107, v107, v237
	v_mul_f32_e32 v108, v108, v237
	v_mul_f32_e32 v109, v109, v237
	v_mul_f32_e32 v110, v110, v237
	v_mul_f32_e32 v111, v111, v237
	v_mul_f32_e32 v112, v112, v237
	v_mul_f32_e32 v113, v113, v237
	v_mul_f32_e32 v114, v114, v237
	v_mul_f32_e32 v115, v115, v237
	v_mul_f32_e32 v116, v116, v237
	v_mul_f32_e32 v117, v117, v237
	v_mul_f32_e32 v118, v118, v237
	v_mul_f32_e32 v119, v119, v237
	v_mul_f32_e32 v120, v120, v237
	v_mul_f32_e32 v121, v121, v237
	v_mul_f32_e32 v122, v122, v237
	v_mul_f32_e32 v123, v123, v237
	v_mul_f32_e32 v124, v124, v237
	v_mul_f32_e32 v125, v125, v237
	v_mul_f32_e32 v126, v126, v237
	v_mul_f32_e32 v127, v127, v237
	v_mul_f32_e32 v128, v128, v237
	v_mul_f32_e32 v129, v129, v237
	v_mul_f32_e32 v130, v130, v237
	v_mul_f32_e32 v131, v131, v237
	v_fma_f32 v36, v36, v100, v164
	v_fma_f32 v37, v37, v101, v165
	v_fma_f32 v38, v38, v102, v166
	v_fma_f32 v39, v39, v103, v167
	v_cvt_pk_bf16_f32 v238, v36, v37
	v_cvt_pk_bf16_f32 v239, v38, v39
	global_store_dwordx2 v2, v[238:239], s[22:23]
	v_fma_f32 v40, v40, v104, v168
	v_fma_f32 v41, v41, v105, v169
	v_fma_f32 v42, v42, v106, v170
	v_fma_f32 v43, v43, v107, v171
	v_cvt_pk_bf16_f32 v240, v40, v41
	v_cvt_pk_bf16_f32 v241, v42, v43
	global_store_dwordx2 v2, v[240:241], s[22:23] offset:512
	v_fma_f32 v44, v44, v108, v172
	v_fma_f32 v45, v45, v109, v173
	v_fma_f32 v46, v46, v110, v174
	v_fma_f32 v47, v47, v111, v175
	v_cvt_pk_bf16_f32 v238, v44, v45
	v_cvt_pk_bf16_f32 v239, v46, v47
	global_store_dwordx2 v2, v[238:239], s[22:23] offset:1024
	v_fma_f32 v48, v48, v112, v176
	v_fma_f32 v49, v49, v113, v177
	v_fma_f32 v50, v50, v114, v178
	v_fma_f32 v51, v51, v115, v179
	v_cvt_pk_bf16_f32 v240, v48, v49
	v_cvt_pk_bf16_f32 v241, v50, v51
	global_store_dwordx2 v2, v[240:241], s[22:23] offset:1536
	v_fma_f32 v52, v52, v116, v180
	v_fma_f32 v53, v53, v117, v181
	v_fma_f32 v54, v54, v118, v182
	v_fma_f32 v55, v55, v119, v183
	v_cvt_pk_bf16_f32 v238, v52, v53
	v_cvt_pk_bf16_f32 v239, v54, v55
	global_store_dwordx2 v2, v[238:239], s[22:23] offset:2048
	v_fma_f32 v56, v56, v120, v184
	v_fma_f32 v57, v57, v121, v185
	v_fma_f32 v58, v58, v122, v186
	v_fma_f32 v59, v59, v123, v187
	v_cvt_pk_bf16_f32 v240, v56, v57
	v_cvt_pk_bf16_f32 v241, v58, v59
	global_store_dwordx2 v2, v[240:241], s[22:23] offset:2560
	v_fma_f32 v60, v60, v124, v188
	v_fma_f32 v61, v61, v125, v189
	v_fma_f32 v62, v62, v126, v190
	v_fma_f32 v63, v63, v127, v191
	v_cvt_pk_bf16_f32 v238, v60, v61
	v_cvt_pk_bf16_f32 v239, v62, v63
	global_store_dwordx2 v2, v[238:239], s[22:23] offset:3072
	v_fma_f32 v64, v64, v128, v192
	v_fma_f32 v65, v65, v129, v193
	v_fma_f32 v66, v66, v130, v194
	v_fma_f32 v67, v67, v131, v195
	v_cvt_pk_bf16_f32 v240, v64, v65
	v_cvt_pk_bf16_f32 v241, v66, v67
	global_store_dwordx2 v2, v[240:241], s[22:23] offset:3584
	s_add_i32 s11, s10, 0x3000
	s_lshr_b32 s0, s11, 8
	s_mul_i32 s0, s0, 57
	s_lshr_b32 s44, s0, 9
	s_mul_i32 s1, s44, 0x900
	s_sub_i32 s43, s11, s1
	s_lshl_b32 s1, s11, 13
	s_add_u32 s16, s48, s1
	s_addc_u32 s17, s49, 0
	s_add_u32 s18, s16, 0x1000
	s_addc_u32 s19, s17, 0
	s_lshl_b32 s1, s11, 12
	s_add_u32 s22, s50, s1
	s_addc_u32 s23, s51, 0
	s_cmpk_lt_u32 s43, 0x100
	s_cselect_b32 s0, 8, s44
	s_mul_i32 s1, s0, 0xc000
	s_add_u32 s28, s52, s1
	s_addc_u32 s29, s53, 0
	s_add_u32 s30, s28, 0x1000
	s_addc_u32 s31, s29, 0
	s_add_u32 s72, s54, s1
	s_addc_u32 s73, s55, 0
	s_add_u32 s72, s72, 0xa000
	s_addc_u32 s73, s73, 0
	s_add_u32 s74, s72, 0x1000
	s_addc_u32 s75, s73, 0
	global_load_dwordx4 v[68:71], v1, s[72:73]
	global_load_dwordx4 v[100:103], v1, s[56:57]
	global_load_dwordx4 v[72:75], v1, s[72:73] offset:1024
	global_load_dwordx4 v[104:107], v1, s[56:57] offset:1024
	global_load_dwordx4 v[76:79], v1, s[72:73] offset:2048
	global_load_dwordx4 v[108:111], v1, s[56:57] offset:2048
	global_load_dwordx4 v[80:83], v1, s[72:73] offset:3072
	global_load_dwordx4 v[112:115], v1, s[56:57] offset:3072
	global_load_dwordx4 v[84:87], v1, s[74:75]
	global_load_dwordx4 v[116:119], v1, s[58:59]
	global_load_dwordx4 v[88:91], v1, s[74:75] offset:1024
	global_load_dwordx4 v[120:123], v1, s[58:59] offset:1024
	global_load_dwordx4 v[92:95], v1, s[74:75] offset:2048
	global_load_dwordx4 v[124:127], v1, s[58:59] offset:2048
	global_load_dwordx4 v[96:99], v1, s[74:75] offset:3072
	global_load_dwordx4 v[128:131], v1, s[58:59] offset:3072
	s_add_u32 s84, s28, 0x2000
	s_addc_u32 s85, s29, 0
	s_add_u32 s86, s28, 0x3000
	s_addc_u32 s87, s29, 0
	global_load_dwordx4 v[164:167], v1, s[28:29]
	global_load_dwordx4 v[132:135], v1, s[84:85]
	global_load_dwordx4 v[168:171], v1, s[28:29] offset:1024
	global_load_dwordx4 v[136:139], v1, s[84:85] offset:1024
	global_load_dwordx4 v[172:175], v1, s[28:29] offset:2048
	global_load_dwordx4 v[140:143], v1, s[84:85] offset:2048
	global_load_dwordx4 v[176:179], v1, s[28:29] offset:3072
	global_load_dwordx4 v[144:147], v1, s[84:85] offset:3072
	global_load_dwordx4 v[180:183], v1, s[30:31]
	global_load_dwordx4 v[148:151], v1, s[86:87]
	global_load_dwordx4 v[184:187], v1, s[30:31] offset:1024
	global_load_dwordx4 v[152:155], v1, s[86:87] offset:1024
	global_load_dwordx4 v[188:191], v1, s[30:31] offset:2048
	global_load_dwordx4 v[156:159], v1, s[86:87] offset:2048
	global_load_dwordx4 v[192:195], v1, s[30:31] offset:3072
	global_load_dwordx4 v[160:163], v1, s[86:87] offset:3072
	s_waitcnt vmcnt(56)
	v_cmp_le_i32_e64 s[0:1], 0, v234
	s_nop 1
	s_and_b32 s45, s0, 0xffff
	s_mov_b32 s47, 0
	s_mov_b32 s61, 0
	s_cmp_eq_u32 s45, 0
	s_cbranch_scc1 .Ln1_y0_6
	s_mov_b32 s47, 1
	s_ff1_i32_b32 s0, s45
	s_add_i32 s1, s45, -1
	s_and_b32 s45, s45, s1
	s_nop 0
	v_readlane_b32 s0, v234, s0
	s_nop 3
	s_lshl_b32 s0, s0, 12
	s_add_u32 s76, s64, s0
	s_addc_u32 s77, s65, 0
	global_load_dwordx2 v[196:197], v2, s[76:77]
	global_load_dwordx2 v[198:199], v2, s[76:77] offset:512
	global_load_dwordx2 v[200:201], v2, s[76:77] offset:1024
	global_load_dwordx2 v[202:203], v2, s[76:77] offset:1536
	global_load_dwordx2 v[204:205], v2, s[76:77] offset:2048
	global_load_dwordx2 v[206:207], v2, s[76:77] offset:2560
	global_load_dwordx2 v[208:209], v2, s[76:77] offset:3072
	global_load_dwordx2 v[210:211], v2, s[76:77] offset:3584
	s_cmp_eq_u32 s45, 0
	s_cbranch_scc1 .Ln1_y0_6
	s_mov_b32 s61, 1
	s_ff1_i32_b32 s0, s45
	s_add_i32 s1, s45, -1
	s_and_b32 s45, s45, s1
	s_nop 0
	v_readlane_b32 s0, v234, s0
	s_nop 3
	s_lshl_b32 s0, s0, 12
	s_add_u32 s76, s64, s0
	s_addc_u32 s77, s65, 0
	global_load_dwordx2 v[212:213], v2, s[76:77]
	global_load_dwordx2 v[214:215], v2, s[76:77] offset:512
	global_load_dwordx2 v[216:217], v2, s[76:77] offset:1024
	global_load_dwordx2 v[218:219], v2, s[76:77] offset:1536
	global_load_dwordx2 v[226:227], v2, s[76:77] offset:2048
	global_load_dwordx2 v[228:229], v2, s[76:77] offset:2560
	global_load_dwordx2 v[230:231], v2, s[76:77] offset:3072
	global_load_dwordx2 v[232:233], v2, s[76:77] offset:3584
.Ln1_y0_6:
	s_add_i32 s11, s10, 0x3800
	s_lshr_b32 s0, s11, 8
	s_mul_i32 s0, s0, 57
	s_lshr_b32 s44, s0, 9
	s_mul_i32 s1, s44, 0x900
	s_sub_i32 s43, s11, s1
	s_lshl_b32 s1, s11, 6
	s_add_u32 s78, s62, s1
	s_addc_u32 s79, s63, 0
	global_load_dword v235, v246, s[78:79]
	s_lshl_b32 s1, s11, 13
	s_add_u32 s12, s48, s1
	s_addc_u32 s13, s49, 0
	s_add_u32 s14, s12, 0x1000
	s_addc_u32 s15, s13, 0
	global_load_dwordx4 v[36:39], v1, s[12:13]
	global_load_dwordx4 v[40:43], v1, s[12:13] offset:1024
	global_load_dwordx4 v[44:47], v1, s[12:13] offset:2048
	global_load_dwordx4 v[48:51], v1, s[12:13] offset:3072
	global_load_dwordx4 v[52:55], v1, s[14:15]
	global_load_dwordx4 v[56:59], v1, s[14:15] offset:1024
	global_load_dwordx4 v[60:63], v1, s[14:15] offset:2048
	global_load_dwordx4 v[64:67], v1, s[14:15] offset:3072
	s_waitcnt vmcnt(9)
	s_cmp_eq_u32 s47, 0
	s_cbranch_scc1 .Ln1_a1_6
	v_lshlrev_b32_e32 v238, 16, v196
	v_and_b32_e32 v239, 0xffff0000, v196
	v_fmac_f32_e32 v4, v68, v238
	v_fmac_f32_e32 v5, v69, v239
	v_lshlrev_b32_e32 v238, 16, v197
	v_and_b32_e32 v239, 0xffff0000, v197
	v_fmac_f32_e32 v6, v70, v238
	v_fmac_f32_e32 v7, v71, v239
	v_lshlrev_b32_e32 v238, 16, v198
	v_and_b32_e32 v239, 0xffff0000, v198
	v_fmac_f32_e32 v8, v72, v238
	v_fmac_f32_e32 v9, v73, v239
	v_lshlrev_b32_e32 v238, 16, v199
	v_and_b32_e32 v239, 0xffff0000, v199
	v_fmac_f32_e32 v10, v74, v238
	v_fmac_f32_e32 v11, v75, v239
	v_lshlrev_b32_e32 v238, 16, v200
	v_and_b32_e32 v239, 0xffff0000, v200
	v_fmac_f32_e32 v12, v76, v238
	v_fmac_f32_e32 v13, v77, v239
	v_lshlrev_b32_e32 v238, 16, v201
	v_and_b32_e32 v239, 0xffff0000, v201
	v_fmac_f32_e32 v14, v78, v238
	v_fmac_f32_e32 v15, v79, v239
	v_lshlrev_b32_e32 v238, 16, v202
	v_and_b32_e32 v239, 0xffff0000, v202
	v_fmac_f32_e32 v16, v80, v238
	v_fmac_f32_e32 v17, v81, v239
	v_lshlrev_b32_e32 v238, 16, v203
	v_and_b32_e32 v239, 0xffff0000, v203
	v_fmac_f32_e32 v18, v82, v238
	v_fmac_f32_e32 v19, v83, v239
	v_lshlrev_b32_e32 v238, 16, v204
	v_and_b32_e32 v239, 0xffff0000, v204
	v_fmac_f32_e32 v20, v84, v238
	v_fmac_f32_e32 v21, v85, v239
	v_lshlrev_b32_e32 v238, 16, v205
	v_and_b32_e32 v239, 0xffff0000, v205
	v_fmac_f32_e32 v22, v86, v238
	v_fmac_f32_e32 v23, v87, v239
	v_lshlrev_b32_e32 v238, 16, v206
	v_and_b32_e32 v239, 0xffff0000, v206
	v_fmac_f32_e32 v24, v88, v238
	v_fmac_f32_e32 v25, v89, v239
	v_lshlrev_b32_e32 v238, 16, v207
	v_and_b32_e32 v239, 0xffff0000, v207
	v_fmac_f32_e32 v26, v90, v238
	v_fmac_f32_e32 v27, v91, v239
	v_lshlrev_b32_e32 v238, 16, v208
	v_and_b32_e32 v239, 0xffff0000, v208
	v_fmac_f32_e32 v28, v92, v238
	v_fmac_f32_e32 v29, v93, v239
	v_lshlrev_b32_e32 v238, 16, v209
	v_and_b32_e32 v239, 0xffff0000, v209
	v_fmac_f32_e32 v30, v94, v238
	v_fmac_f32_e32 v31, v95, v239
	v_lshlrev_b32_e32 v238, 16, v210
	v_and_b32_e32 v239, 0xffff0000, v210
	v_fmac_f32_e32 v32, v96, v238
	v_fmac_f32_e32 v33, v97, v239
	v_lshlrev_b32_e32 v238, 16, v211
	v_and_b32_e32 v239, 0xffff0000, v211
	v_fmac_f32_e32 v34, v98, v238
	v_fmac_f32_e32 v35, v99, v239

.Ln1_gd_6:
	global_store_dwordx4 v1, v[4:7], s[16:17]
	global_store_dwordx4 v1, v[8:11], s[16:17] offset:1024
	global_store_dwordx4 v1, v[12:15], s[16:17] offset:2048
	global_store_dwordx4 v1, v[16:19], s[16:17] offset:3072
	global_store_dwordx4 v1, v[20:23], s[18:19]
	global_store_dwordx4 v1, v[24:27], s[18:19] offset:1024
	global_store_dwordx4 v1, v[28:31], s[18:19] offset:2048
	global_store_dwordx4 v1, v[32:35], s[18:19] offset:3072
	v_mul_f32_e32 v236, v4, v4
	v_fmac_f32_e32 v236, v5, v5
	v_fmac_f32_e32 v236, v6, v6
	v_fmac_f32_e32 v236, v7, v7
	v_fmac_f32_e32 v236, v8, v8
	v_fmac_f32_e32 v236, v9, v9
	v_fmac_f32_e32 v236, v10, v10
	v_fmac_f32_e32 v236, v11, v11
	v_fmac_f32_e32 v236, v12, v12
	v_fmac_f32_e32 v236, v13, v13
	v_fmac_f32_e32 v236, v14, v14
	v_fmac_f32_e32 v236, v15, v15
	v_fmac_f32_e32 v236, v16, v16
	v_fmac_f32_e32 v236, v17, v17
	v_fmac_f32_e32 v236, v18, v18
	v_fmac_f32_e32 v236, v19, v19
	v_fmac_f32_e32 v236, v20, v20
	v_fmac_f32_e32 v236, v21, v21
	v_fmac_f32_e32 v236, v22, v22
	v_fmac_f32_e32 v236, v23, v23
	v_fmac_f32_e32 v236, v24, v24
	v_fmac_f32_e32 v236, v25, v25
	v_fmac_f32_e32 v236, v26, v26
	v_fmac_f32_e32 v236, v27, v27
	v_fmac_f32_e32 v236, v28, v28
	v_fmac_f32_e32 v236, v29, v29
	v_fmac_f32_e32 v236, v30, v30
	v_fmac_f32_e32 v236, v31, v31
	v_fmac_f32_e32 v236, v32, v32
	v_fmac_f32_e32 v236, v33, v33
	v_fmac_f32_e32 v236, v34, v34
	v_fmac_f32_e32 v236, v35, v35
	v_fma_f32 v100, v100, v132, v100
	v_fma_f32 v101, v101, v133, v101
	v_fma_f32 v102, v102, v134, v102
	v_fma_f32 v103, v103, v135, v103
	v_fma_f32 v104, v104, v136, v104
	v_fma_f32 v105, v105, v137, v105
	v_fma_f32 v106, v106, v138, v106
	v_fma_f32 v107, v107, v139, v107
	v_fma_f32 v108, v108, v140, v108
	v_fma_f32 v109, v109, v141, v109
	v_fma_f32 v110, v110, v142, v110
	v_fma_f32 v111, v111, v143, v111
	v_fma_f32 v112, v112, v144, v112
	v_fma_f32 v113, v113, v145, v113
	v_fma_f32 v114, v114, v146, v114
	v_fma_f32 v115, v115, v147, v115
	v_fma_f32 v116, v116, v148, v116
	v_fma_f32 v117, v117, v149, v117
	v_fma_f32 v118, v118, v150, v118
	v_fma_f32 v119, v119, v151, v119
	v_fma_f32 v120, v120, v152, v120
	v_fma_f32 v121, v121, v153, v121
	v_fma_f32 v122, v122, v154, v122
	v_fma_f32 v123, v123, v155, v123
	v_fma_f32 v124, v124, v156, v124
	v_fma_f32 v125, v125, v157, v125
	v_fma_f32 v126, v126, v158, v126
	v_fma_f32 v127, v127, v159, v127
	v_fma_f32 v128, v128, v160, v128
	v_fma_f32 v129, v129, v161, v129
	v_fma_f32 v130, v130, v162, v130
	v_fma_f32 v131, v131, v163, v131
	s_nop 1
	v_add_f32_dpp v236, v236, v236 quad_perm:[1,0,3,2] row_mask:0xf bank_mask:0xf
	s_nop 1
	v_add_f32_dpp v236, v236, v236 quad_perm:[2,3,0,1] row_mask:0xf bank_mask:0xf
	s_nop 1
	v_add_f32_dpp v236, v236, v236 row_half_mirror row_mask:0xf bank_mask:0xf
	s_nop 1
	v_add_f32_dpp v236, v236, v236 row_mirror row_mask:0xf bank_mask:0xf
	s_nop 1
	v_readlane_b32 s0, v236, 0
	v_readlane_b32 s1, v236, 16
	v_readlane_b32 s2, v236, 32
	v_readlane_b32 s3, v236, 48
	s_nop 3
	v_mov_b32_e32 v237, s0
	v_add_f32_e32 v237, s1, v237
	v_add_f32_e32 v237, s2, v237
	v_add_f32_e32 v237, s3, v237
	v_mul_f32_e32 v237, 0x3a000000, v237
	v_add_f32_e32 v237, 0x358637bd, v237
	v_rsq_f32_e32 v237, v237
	s_nop 0
	v_mul_f32_e32 v100, v100, v237
	v_mul_f32_e32 v101, v101, v237
	v_mul_f32_e32 v102, v102, v237
	v_mul_f32_e32 v103, v103, v237
	v_mul_f32_e32 v104, v104, v237
	v_mul_f32_e32 v105, v105, v237
	v_mul_f32_e32 v106, v106, v237
	v_mul_f32_e32 v107, v107, v237
	v_mul_f32_e32 v108, v108, v237
	v_mul_f32_e32 v109, v109, v237
	v_mul_f32_e32 v110, v110, v237
	v_mul_f32_e32 v111, v111, v237
	v_mul_f32_e32 v112, v112, v237
	v_mul_f32_e32 v113, v113, v237
	v_mul_f32_e32 v114, v114, v237
	v_mul_f32_e32 v115, v115, v237
	v_mul_f32_e32 v116, v116, v237
	v_mul_f32_e32 v117, v117, v237
	v_mul_f32_e32 v118, v118, v237
	v_mul_f32_e32 v119, v119, v237
	v_mul_f32_e32 v120, v120, v237
	v_mul_f32_e32 v121, v121, v237
	v_mul_f32_e32 v122, v122, v237
	v_mul_f32_e32 v123, v123, v237
	v_mul_f32_e32 v124, v124, v237
	v_mul_f32_e32 v125, v125, v237
	v_mul_f32_e32 v126, v126, v237
	v_mul_f32_e32 v127, v127, v237
	v_mul_f32_e32 v128, v128, v237
	v_mul_f32_e32 v129, v129, v237
	v_mul_f32_e32 v130, v130, v237
	v_mul_f32_e32 v131, v131, v237
	v_fma_f32 v4, v4, v100, v164
	v_fma_f32 v5, v5, v101, v165
	v_fma_f32 v6, v6, v102, v166
	v_fma_f32 v7, v7, v103, v167
	v_cvt_pk_bf16_f32 v238, v4, v5
	v_cvt_pk_bf16_f32 v239, v6, v7
	global_store_dwordx2 v2, v[238:239], s[22:23]
	v_fma_f32 v8, v8, v104, v168
	v_fma_f32 v9, v9, v105, v169
	v_fma_f32 v10, v10, v106, v170
	v_fma_f32 v11, v11, v107, v171
	v_cvt_pk_bf16_f32 v240, v8, v9
	v_cvt_pk_bf16_f32 v241, v10, v11
	global_store_dwordx2 v2, v[240:241], s[22:23] offset:512
	v_fma_f32 v12, v12, v108, v172
	v_fma_f32 v13, v13, v109, v173
	v_fma_f32 v14, v14, v110, v174
	v_fma_f32 v15, v15, v111, v175
	v_cvt_pk_bf16_f32 v238, v12, v13
	v_cvt_pk_bf16_f32 v239, v14, v15
	global_store_dwordx2 v2, v[238:239], s[22:23] offset:1024
	v_fma_f32 v16, v16, v112, v176
	v_fma_f32 v17, v17, v113, v177
	v_fma_f32 v18, v18, v114, v178
	v_fma_f32 v19, v19, v115, v179
	v_cvt_pk_bf16_f32 v240, v16, v17
	v_cvt_pk_bf16_f32 v241, v18, v19
	global_store_dwordx2 v2, v[240:241], s[22:23] offset:1536
	v_fma_f32 v20, v20, v116, v180
	v_fma_f32 v21, v21, v117, v181
	v_fma_f32 v22, v22, v118, v182
	v_fma_f32 v23, v23, v119, v183
	v_cvt_pk_bf16_f32 v238, v20, v21
	v_cvt_pk_bf16_f32 v239, v22, v23
	global_store_dwordx2 v2, v[238:239], s[22:23] offset:2048
	v_fma_f32 v24, v24, v120, v184
	v_fma_f32 v25, v25, v121, v185
	v_fma_f32 v26, v26, v122, v186
	v_fma_f32 v27, v27, v123, v187
	v_cvt_pk_bf16_f32 v240, v24, v25
	v_cvt_pk_bf16_f32 v241, v26, v27
	global_store_dwordx2 v2, v[240:241], s[22:23] offset:2560
	v_fma_f32 v28, v28, v124, v188
	v_fma_f32 v29, v29, v125, v189
	v_fma_f32 v30, v30, v126, v190
	v_fma_f32 v31, v31, v127, v191
	v_cvt_pk_bf16_f32 v238, v28, v29
	v_cvt_pk_bf16_f32 v239, v30, v31
	global_store_dwordx2 v2, v[238:239], s[22:23] offset:3072
	v_fma_f32 v32, v32, v128, v192
	v_fma_f32 v33, v33, v129, v193
	v_fma_f32 v34, v34, v130, v194
	v_fma_f32 v35, v35, v131, v195
	v_cvt_pk_bf16_f32 v240, v32, v33
	v_cvt_pk_bf16_f32 v241, v34, v35
	global_store_dwordx2 v2, v[240:241], s[22:23] offset:3584
	s_add_i32 s11, s10, 0x3800
	s_lshr_b32 s0, s11, 8
	s_mul_i32 s0, s0, 57
	s_lshr_b32 s44, s0, 9
	s_mul_i32 s1, s44, 0x900
	s_sub_i32 s43, s11, s1
	s_lshl_b32 s1, s11, 13
	s_add_u32 s16, s48, s1
	s_addc_u32 s17, s49, 0
	s_add_u32 s18, s16, 0x1000
	s_addc_u32 s19, s17, 0
	s_lshl_b32 s1, s11, 12
	s_add_u32 s22, s50, s1
	s_addc_u32 s23, s51, 0
	s_cmpk_lt_u32 s43, 0x100
	s_cselect_b32 s0, 8, s44
	s_mul_i32 s1, s0, 0xc000
	s_add_u32 s28, s52, s1
	s_addc_u32 s29, s53, 0
	s_add_u32 s30, s28, 0x1000
	s_addc_u32 s31, s29, 0
	s_add_u32 s72, s54, s1
	s_addc_u32 s73, s55, 0
	s_add_u32 s72, s72, 0xa000
	s_addc_u32 s73, s73, 0
	s_add_u32 s74, s72, 0x1000
	s_addc_u32 s75, s73, 0
	global_load_dwordx4 v[68:71], v1, s[72:73]
	global_load_dwordx4 v[100:103], v1, s[56:57]
	global_load_dwordx4 v[72:75], v1, s[72:73] offset:1024
	global_load_dwordx4 v[104:107], v1, s[56:57] offset:1024
	global_load_dwordx4 v[76:79], v1, s[72:73] offset:2048
	global_load_dwordx4 v[108:111], v1, s[56:57] offset:2048
	global_load_dwordx4 v[80:83], v1, s[72:73] offset:3072
	global_load_dwordx4 v[112:115], v1, s[56:57] offset:3072
	global_load_dwordx4 v[84:87], v1, s[74:75]
	global_load_dwordx4 v[116:119], v1, s[58:59]
	global_load_dwordx4 v[88:91], v1, s[74:75] offset:1024
	global_load_dwordx4 v[120:123], v1, s[58:59] offset:1024
	global_load_dwordx4 v[92:95], v1, s[74:75] offset:2048
	global_load_dwordx4 v[124:127], v1, s[58:59] offset:2048
	global_load_dwordx4 v[96:99], v1, s[74:75] offset:3072
	global_load_dwordx4 v[128:131], v1, s[58:59] offset:3072
	s_add_u32 s84, s28, 0x2000
	s_addc_u32 s85, s29, 0
	s_add_u32 s86, s28, 0x3000
	s_addc_u32 s87, s29, 0
	global_load_dwordx4 v[164:167], v1, s[28:29]
	global_load_dwordx4 v[132:135], v1, s[84:85]
	global_load_dwordx4 v[168:171], v1, s[28:29] offset:1024
	global_load_dwordx4 v[136:139], v1, s[84:85] offset:1024
	global_load_dwordx4 v[172:175], v1, s[28:29] offset:2048
	global_load_dwordx4 v[140:143], v1, s[84:85] offset:2048
	global_load_dwordx4 v[176:179], v1, s[28:29] offset:3072
	global_load_dwordx4 v[144:147], v1, s[84:85] offset:3072
	global_load_dwordx4 v[180:183], v1, s[30:31]
	global_load_dwordx4 v[148:151], v1, s[86:87]
	global_load_dwordx4 v[184:187], v1, s[30:31] offset:1024
	global_load_dwordx4 v[152:155], v1, s[86:87] offset:1024
	global_load_dwordx4 v[188:191], v1, s[30:31] offset:2048
	global_load_dwordx4 v[156:159], v1, s[86:87] offset:2048
	global_load_dwordx4 v[192:195], v1, s[30:31] offset:3072
	global_load_dwordx4 v[160:163], v1, s[86:87] offset:3072
	s_waitcnt vmcnt(56)
	v_cmp_le_i32_e64 s[0:1], 0, v235
	s_nop 1
	s_and_b32 s45, s0, 0xffff
	s_mov_b32 s47, 0
	s_mov_b32 s61, 0
	s_cmp_eq_u32 s45, 0
	s_cbranch_scc1 .Ln1_y0_7
	s_mov_b32 s47, 1
	s_ff1_i32_b32 s0, s45
	s_add_i32 s1, s45, -1
	s_and_b32 s45, s45, s1
	s_nop 0
	v_readlane_b32 s0, v235, s0
	s_nop 3
	s_lshl_b32 s0, s0, 12
	s_add_u32 s76, s64, s0
	s_addc_u32 s77, s65, 0
	global_load_dwordx2 v[196:197], v2, s[76:77]
	global_load_dwordx2 v[198:199], v2, s[76:77] offset:512
	global_load_dwordx2 v[200:201], v2, s[76:77] offset:1024
	global_load_dwordx2 v[202:203], v2, s[76:77] offset:1536
	global_load_dwordx2 v[204:205], v2, s[76:77] offset:2048
	global_load_dwordx2 v[206:207], v2, s[76:77] offset:2560
	global_load_dwordx2 v[208:209], v2, s[76:77] offset:3072
	global_load_dwordx2 v[210:211], v2, s[76:77] offset:3584
	s_cmp_eq_u32 s45, 0
	s_cbranch_scc1 .Ln1_y0_7
	s_mov_b32 s61, 1
	s_ff1_i32_b32 s0, s45
	s_add_i32 s1, s45, -1
	s_and_b32 s45, s45, s1
	s_nop 0
	v_readlane_b32 s0, v235, s0
	s_nop 3
	s_lshl_b32 s0, s0, 12
	s_add_u32 s76, s64, s0
	s_addc_u32 s77, s65, 0
	global_load_dwordx2 v[212:213], v2, s[76:77]
	global_load_dwordx2 v[214:215], v2, s[76:77] offset:512
	global_load_dwordx2 v[216:217], v2, s[76:77] offset:1024
	global_load_dwordx2 v[218:219], v2, s[76:77] offset:1536
	global_load_dwordx2 v[226:227], v2, s[76:77] offset:2048
	global_load_dwordx2 v[228:229], v2, s[76:77] offset:2560
	global_load_dwordx2 v[230:231], v2, s[76:77] offset:3072
	global_load_dwordx2 v[232:233], v2, s[76:77] offset:3584
.Ln1_y0_7:
	s_add_i32 s11, s10, 0x4000
	s_lshr_b32 s0, s11, 8
	s_mul_i32 s0, s0, 57
	s_lshr_b32 s44, s0, 9
	s_mul_i32 s1, s44, 0x900
	s_sub_i32 s43, s11, s1
	s_lshl_b32 s1, s11, 6
	s_add_u32 s78, s62, s1
	s_addc_u32 s79, s63, 0
	global_load_dword v234, v246, s[78:79]
	s_lshl_b32 s1, s11, 13
	s_add_u32 s12, s48, s1
	s_addc_u32 s13, s49, 0
	s_add_u32 s14, s12, 0x1000
	s_addc_u32 s15, s13, 0
	global_load_dwordx4 v[4:7], v1, s[12:13]
	global_load_dwordx4 v[8:11], v1, s[12:13] offset:1024
	global_load_dwordx4 v[12:15], v1, s[12:13] offset:2048
	global_load_dwordx4 v[16:19], v1, s[12:13] offset:3072
	global_load_dwordx4 v[20:23], v1, s[14:15]
	global_load_dwordx4 v[24:27], v1, s[14:15] offset:1024
	global_load_dwordx4 v[28:31], v1, s[14:15] offset:2048
	global_load_dwordx4 v[32:35], v1, s[14:15] offset:3072
	s_waitcnt vmcnt(9)
	s_cmp_eq_u32 s47, 0
	s_cbranch_scc1 .Ln1_a1_7
	v_lshlrev_b32_e32 v238, 16, v196
	v_and_b32_e32 v239, 0xffff0000, v196
	v_fmac_f32_e32 v36, v68, v238
	v_fmac_f32_e32 v37, v69, v239
	v_lshlrev_b32_e32 v238, 16, v197
	v_and_b32_e32 v239, 0xffff0000, v197
	v_fmac_f32_e32 v38, v70, v238
	v_fmac_f32_e32 v39, v71, v239
	v_lshlrev_b32_e32 v238, 16, v198
	v_and_b32_e32 v239, 0xffff0000, v198
	v_fmac_f32_e32 v40, v72, v238
	v_fmac_f32_e32 v41, v73, v239
	v_lshlrev_b32_e32 v238, 16, v199
	v_and_b32_e32 v239, 0xffff0000, v199
	v_fmac_f32_e32 v42, v74, v238
	v_fmac_f32_e32 v43, v75, v239
	v_lshlrev_b32_e32 v238, 16, v200
	v_and_b32_e32 v239, 0xffff0000, v200
	v_fmac_f32_e32 v44, v76, v238
	v_fmac_f32_e32 v45, v77, v239
	v_lshlrev_b32_e32 v238, 16, v201
	v_and_b32_e32 v239, 0xffff0000, v201
	v_fmac_f32_e32 v46, v78, v238
	v_fmac_f32_e32 v47, v79, v239
	v_lshlrev_b32_e32 v238, 16, v202
	v_and_b32_e32 v239, 0xffff0000, v202
	v_fmac_f32_e32 v48, v80, v238
	v_fmac_f32_e32 v49, v81, v239
	v_lshlrev_b32_e32 v238, 16, v203
	v_and_b32_e32 v239, 0xffff0000, v203
	v_fmac_f32_e32 v50, v82, v238
	v_fmac_f32_e32 v51, v83, v239
	v_lshlrev_b32_e32 v238, 16, v204
	v_and_b32_e32 v239, 0xffff0000, v204
	v_fmac_f32_e32 v52, v84, v238
	v_fmac_f32_e32 v53, v85, v239
	v_lshlrev_b32_e32 v238, 16, v205
	v_and_b32_e32 v239, 0xffff0000, v205
	v_fmac_f32_e32 v54, v86, v238
	v_fmac_f32_e32 v55, v87, v239
	v_lshlrev_b32_e32 v238, 16, v206
	v_and_b32_e32 v239, 0xffff0000, v206
	v_fmac_f32_e32 v56, v88, v238
	v_fmac_f32_e32 v57, v89, v239
	v_lshlrev_b32_e32 v238, 16, v207
	v_and_b32_e32 v239, 0xffff0000, v207
	v_fmac_f32_e32 v58, v90, v238
	v_fmac_f32_e32 v59, v91, v239
	v_lshlrev_b32_e32 v238, 16, v208
	v_and_b32_e32 v239, 0xffff0000, v208
	v_fmac_f32_e32 v60, v92, v238
	v_fmac_f32_e32 v61, v93, v239
	v_lshlrev_b32_e32 v238, 16, v209
	v_and_b32_e32 v239, 0xffff0000, v209
	v_fmac_f32_e32 v62, v94, v238
	v_fmac_f32_e32 v63, v95, v239
	v_lshlrev_b32_e32 v238, 16, v210
	v_and_b32_e32 v239, 0xffff0000, v210
	v_fmac_f32_e32 v64, v96, v238
	v_fmac_f32_e32 v65, v97, v239
	v_lshlrev_b32_e32 v238, 16, v211
	v_and_b32_e32 v239, 0xffff0000, v211
	v_fmac_f32_e32 v66, v98, v238
	v_fmac_f32_e32 v67, v99, v239

.Ln1_gd_7:
	global_store_dwordx4 v1, v[36:39], s[16:17]
	global_store_dwordx4 v1, v[40:43], s[16:17] offset:1024
	global_store_dwordx4 v1, v[44:47], s[16:17] offset:2048
	global_store_dwordx4 v1, v[48:51], s[16:17] offset:3072
	global_store_dwordx4 v1, v[52:55], s[18:19]
	global_store_dwordx4 v1, v[56:59], s[18:19] offset:1024
	global_store_dwordx4 v1, v[60:63], s[18:19] offset:2048
	global_store_dwordx4 v1, v[64:67], s[18:19] offset:3072
	v_mul_f32_e32 v236, v36, v36
	v_fmac_f32_e32 v236, v37, v37
	v_fmac_f32_e32 v236, v38, v38
	v_fmac_f32_e32 v236, v39, v39
	v_fmac_f32_e32 v236, v40, v40
	v_fmac_f32_e32 v236, v41, v41
	v_fmac_f32_e32 v236, v42, v42
	v_fmac_f32_e32 v236, v43, v43
	v_fmac_f32_e32 v236, v44, v44
	v_fmac_f32_e32 v236, v45, v45
	v_fmac_f32_e32 v236, v46, v46
	v_fmac_f32_e32 v236, v47, v47
	v_fmac_f32_e32 v236, v48, v48
	v_fmac_f32_e32 v236, v49, v49
	v_fmac_f32_e32 v236, v50, v50
	v_fmac_f32_e32 v236, v51, v51
	v_fmac_f32_e32 v236, v52, v52
	v_fmac_f32_e32 v236, v53, v53
	v_fmac_f32_e32 v236, v54, v54
	v_fmac_f32_e32 v236, v55, v55
	v_fmac_f32_e32 v236, v56, v56
	v_fmac_f32_e32 v236, v57, v57
	v_fmac_f32_e32 v236, v58, v58
	v_fmac_f32_e32 v236, v59, v59
	v_fmac_f32_e32 v236, v60, v60
	v_fmac_f32_e32 v236, v61, v61
	v_fmac_f32_e32 v236, v62, v62
	v_fmac_f32_e32 v236, v63, v63
	v_fmac_f32_e32 v236, v64, v64
	v_fmac_f32_e32 v236, v65, v65
	v_fmac_f32_e32 v236, v66, v66
	v_fmac_f32_e32 v236, v67, v67
	v_fma_f32 v100, v100, v132, v100
	v_fma_f32 v101, v101, v133, v101
	v_fma_f32 v102, v102, v134, v102
	v_fma_f32 v103, v103, v135, v103
	v_fma_f32 v104, v104, v136, v104
	v_fma_f32 v105, v105, v137, v105
	v_fma_f32 v106, v106, v138, v106
	v_fma_f32 v107, v107, v139, v107
	v_fma_f32 v108, v108, v140, v108
	v_fma_f32 v109, v109, v141, v109
	v_fma_f32 v110, v110, v142, v110
	v_fma_f32 v111, v111, v143, v111
	v_fma_f32 v112, v112, v144, v112
	v_fma_f32 v113, v113, v145, v113
	v_fma_f32 v114, v114, v146, v114
	v_fma_f32 v115, v115, v147, v115
	v_fma_f32 v116, v116, v148, v116
	v_fma_f32 v117, v117, v149, v117
	v_fma_f32 v118, v118, v150, v118
	v_fma_f32 v119, v119, v151, v119
	v_fma_f32 v120, v120, v152, v120
	v_fma_f32 v121, v121, v153, v121
	v_fma_f32 v122, v122, v154, v122
	v_fma_f32 v123, v123, v155, v123
	v_fma_f32 v124, v124, v156, v124
	v_fma_f32 v125, v125, v157, v125
	v_fma_f32 v126, v126, v158, v126
	v_fma_f32 v127, v127, v159, v127
	v_fma_f32 v128, v128, v160, v128
	v_fma_f32 v129, v129, v161, v129
	v_fma_f32 v130, v130, v162, v130
	v_fma_f32 v131, v131, v163, v131
	s_nop 1
	v_add_f32_dpp v236, v236, v236 quad_perm:[1,0,3,2] row_mask:0xf bank_mask:0xf
	s_nop 1
	v_add_f32_dpp v236, v236, v236 quad_perm:[2,3,0,1] row_mask:0xf bank_mask:0xf
	s_nop 1
	v_add_f32_dpp v236, v236, v236 row_half_mirror row_mask:0xf bank_mask:0xf
	s_nop 1
	v_add_f32_dpp v236, v236, v236 row_mirror row_mask:0xf bank_mask:0xf
	s_nop 1
	v_readlane_b32 s0, v236, 0
	v_readlane_b32 s1, v236, 16
	v_readlane_b32 s2, v236, 32
	v_readlane_b32 s3, v236, 48
	s_nop 3
	v_mov_b32_e32 v237, s0
	v_add_f32_e32 v237, s1, v237
	v_add_f32_e32 v237, s2, v237
	v_add_f32_e32 v237, s3, v237
	v_mul_f32_e32 v237, 0x3a000000, v237
	v_add_f32_e32 v237, 0x358637bd, v237
	v_rsq_f32_e32 v237, v237
	s_nop 0
	v_mul_f32_e32 v100, v100, v237
	v_mul_f32_e32 v101, v101, v237
	v_mul_f32_e32 v102, v102, v237
	v_mul_f32_e32 v103, v103, v237
	v_mul_f32_e32 v104, v104, v237
	v_mul_f32_e32 v105, v105, v237
	v_mul_f32_e32 v106, v106, v237
	v_mul_f32_e32 v107, v107, v237
	v_mul_f32_e32 v108, v108, v237
	v_mul_f32_e32 v109, v109, v237
	v_mul_f32_e32 v110, v110, v237
	v_mul_f32_e32 v111, v111, v237
	v_mul_f32_e32 v112, v112, v237
	v_mul_f32_e32 v113, v113, v237
	v_mul_f32_e32 v114, v114, v237
	v_mul_f32_e32 v115, v115, v237
	v_mul_f32_e32 v116, v116, v237
	v_mul_f32_e32 v117, v117, v237
	v_mul_f32_e32 v118, v118, v237
	v_mul_f32_e32 v119, v119, v237
	v_mul_f32_e32 v120, v120, v237
	v_mul_f32_e32 v121, v121, v237
	v_mul_f32_e32 v122, v122, v237
	v_mul_f32_e32 v123, v123, v237
	v_mul_f32_e32 v124, v124, v237
	v_mul_f32_e32 v125, v125, v237
	v_mul_f32_e32 v126, v126, v237
	v_mul_f32_e32 v127, v127, v237
	v_mul_f32_e32 v128, v128, v237
	v_mul_f32_e32 v129, v129, v237
	v_mul_f32_e32 v130, v130, v237
	v_mul_f32_e32 v131, v131, v237
	v_fma_f32 v36, v36, v100, v164
	v_fma_f32 v37, v37, v101, v165
	v_fma_f32 v38, v38, v102, v166
	v_fma_f32 v39, v39, v103, v167
	v_cvt_pk_bf16_f32 v238, v36, v37
	v_cvt_pk_bf16_f32 v239, v38, v39
	global_store_dwordx2 v2, v[238:239], s[22:23]
	v_fma_f32 v40, v40, v104, v168
	v_fma_f32 v41, v41, v105, v169
	v_fma_f32 v42, v42, v106, v170
	v_fma_f32 v43, v43, v107, v171
	v_cvt_pk_bf16_f32 v240, v40, v41
	v_cvt_pk_bf16_f32 v241, v42, v43
	global_store_dwordx2 v2, v[240:241], s[22:23] offset:512
	v_fma_f32 v44, v44, v108, v172
	v_fma_f32 v45, v45, v109, v173
	v_fma_f32 v46, v46, v110, v174
	v_fma_f32 v47, v47, v111, v175
	v_cvt_pk_bf16_f32 v238, v44, v45
	v_cvt_pk_bf16_f32 v239, v46, v47
	global_store_dwordx2 v2, v[238:239], s[22:23] offset:1024
	v_fma_f32 v48, v48, v112, v176
	v_fma_f32 v49, v49, v113, v177
	v_fma_f32 v50, v50, v114, v178
	v_fma_f32 v51, v51, v115, v179
	v_cvt_pk_bf16_f32 v240, v48, v49
	v_cvt_pk_bf16_f32 v241, v50, v51
	global_store_dwordx2 v2, v[240:241], s[22:23] offset:1536
	v_fma_f32 v52, v52, v116, v180
	v_fma_f32 v53, v53, v117, v181
	v_fma_f32 v54, v54, v118, v182
	v_fma_f32 v55, v55, v119, v183
	v_cvt_pk_bf16_f32 v238, v52, v53
	v_cvt_pk_bf16_f32 v239, v54, v55
	global_store_dwordx2 v2, v[238:239], s[22:23] offset:2048
	v_fma_f32 v56, v56, v120, v184
	v_fma_f32 v57, v57, v121, v185
	v_fma_f32 v58, v58, v122, v186
	v_fma_f32 v59, v59, v123, v187
	v_cvt_pk_bf16_f32 v240, v56, v57
	v_cvt_pk_bf16_f32 v241, v58, v59
	global_store_dwordx2 v2, v[240:241], s[22:23] offset:2560
	v_fma_f32 v60, v60, v124, v188
	v_fma_f32 v61, v61, v125, v189
	v_fma_f32 v62, v62, v126, v190
	v_fma_f32 v63, v63, v127, v191
	v_cvt_pk_bf16_f32 v238, v60, v61
	v_cvt_pk_bf16_f32 v239, v62, v63
	global_store_dwordx2 v2, v[238:239], s[22:23] offset:3072
	v_fma_f32 v64, v64, v128, v192
	v_fma_f32 v65, v65, v129, v193
	v_fma_f32 v66, v66, v130, v194
	v_fma_f32 v67, v67, v131, v195
	v_cvt_pk_bf16_f32 v240, v64, v65
	v_cvt_pk_bf16_f32 v241, v66, v67
	global_store_dwordx2 v2, v[240:241], s[22:23] offset:3584
	s_add_i32 s11, s10, 0x4000
	s_lshr_b32 s0, s11, 8
	s_mul_i32 s0, s0, 57
	s_lshr_b32 s44, s0, 9
	s_mul_i32 s1, s44, 0x900
	s_sub_i32 s43, s11, s1
	s_lshl_b32 s1, s11, 13
	s_add_u32 s16, s48, s1
	s_addc_u32 s17, s49, 0
	s_add_u32 s18, s16, 0x1000
	s_addc_u32 s19, s17, 0
	s_lshl_b32 s1, s11, 12
	s_add_u32 s22, s50, s1
	s_addc_u32 s23, s51, 0
	s_cmpk_lt_u32 s43, 0x100
	s_cselect_b32 s0, 8, s44
	s_mul_i32 s1, s0, 0xc000
	s_add_u32 s28, s52, s1
	s_addc_u32 s29, s53, 0
	s_add_u32 s30, s28, 0x1000
	s_addc_u32 s31, s29, 0
	s_add_u32 s72, s54, s1
	s_addc_u32 s73, s55, 0
	s_add_u32 s72, s72, 0xa000
	s_addc_u32 s73, s73, 0
	s_add_u32 s74, s72, 0x1000
	s_addc_u32 s75, s73, 0
	global_load_dwordx4 v[68:71], v1, s[72:73]
	global_load_dwordx4 v[100:103], v1, s[56:57]
	global_load_dwordx4 v[72:75], v1, s[72:73] offset:1024
	global_load_dwordx4 v[104:107], v1, s[56:57] offset:1024
	global_load_dwordx4 v[76:79], v1, s[72:73] offset:2048
	global_load_dwordx4 v[108:111], v1, s[56:57] offset:2048
	global_load_dwordx4 v[80:83], v1, s[72:73] offset:3072
	global_load_dwordx4 v[112:115], v1, s[56:57] offset:3072
	global_load_dwordx4 v[84:87], v1, s[74:75]
	global_load_dwordx4 v[116:119], v1, s[58:59]
	global_load_dwordx4 v[88:91], v1, s[74:75] offset:1024
	global_load_dwordx4 v[120:123], v1, s[58:59] offset:1024
	global_load_dwordx4 v[92:95], v1, s[74:75] offset:2048
	global_load_dwordx4 v[124:127], v1, s[58:59] offset:2048
	global_load_dwordx4 v[96:99], v1, s[74:75] offset:3072
	global_load_dwordx4 v[128:131], v1, s[58:59] offset:3072
	s_add_u32 s84, s28, 0x2000
	s_addc_u32 s85, s29, 0
	s_add_u32 s86, s28, 0x3000
	s_addc_u32 s87, s29, 0
	global_load_dwordx4 v[164:167], v1, s[28:29]
	global_load_dwordx4 v[132:135], v1, s[84:85]
	global_load_dwordx4 v[168:171], v1, s[28:29] offset:1024
	global_load_dwordx4 v[136:139], v1, s[84:85] offset:1024
	global_load_dwordx4 v[172:175], v1, s[28:29] offset:2048
	global_load_dwordx4 v[140:143], v1, s[84:85] offset:2048
	global_load_dwordx4 v[176:179], v1, s[28:29] offset:3072
	global_load_dwordx4 v[144:147], v1, s[84:85] offset:3072
	global_load_dwordx4 v[180:183], v1, s[30:31]
	global_load_dwordx4 v[148:151], v1, s[86:87]
	global_load_dwordx4 v[184:187], v1, s[30:31] offset:1024
	global_load_dwordx4 v[152:155], v1, s[86:87] offset:1024
	global_load_dwordx4 v[188:191], v1, s[30:31] offset:2048
	global_load_dwordx4 v[156:159], v1, s[86:87] offset:2048
	global_load_dwordx4 v[192:195], v1, s[30:31] offset:3072
	global_load_dwordx4 v[160:163], v1, s[86:87] offset:3072
	s_waitcnt vmcnt(56)
	v_cmp_le_i32_e64 s[0:1], 0, v234
	s_nop 1
	s_and_b32 s45, s0, 0xffff
	s_mov_b32 s47, 0
	s_mov_b32 s61, 0
	s_cmp_eq_u32 s45, 0
	s_cbranch_scc1 .Ln1_y0_8
	s_mov_b32 s47, 1
	s_ff1_i32_b32 s0, s45
	s_add_i32 s1, s45, -1
	s_and_b32 s45, s45, s1
	s_nop 0
	v_readlane_b32 s0, v234, s0
	s_nop 3
	s_lshl_b32 s0, s0, 12
	s_add_u32 s76, s64, s0
	s_addc_u32 s77, s65, 0
	global_load_dwordx2 v[196:197], v2, s[76:77]
	global_load_dwordx2 v[198:199], v2, s[76:77] offset:512
	global_load_dwordx2 v[200:201], v2, s[76:77] offset:1024
	global_load_dwordx2 v[202:203], v2, s[76:77] offset:1536
	global_load_dwordx2 v[204:205], v2, s[76:77] offset:2048
	global_load_dwordx2 v[206:207], v2, s[76:77] offset:2560
	global_load_dwordx2 v[208:209], v2, s[76:77] offset:3072
	global_load_dwordx2 v[210:211], v2, s[76:77] offset:3584
	s_cmp_eq_u32 s45, 0
	s_cbranch_scc1 .Ln1_y0_8
	s_mov_b32 s61, 1
	s_ff1_i32_b32 s0, s45
	s_add_i32 s1, s45, -1
	s_and_b32 s45, s45, s1
	s_nop 0
	v_readlane_b32 s0, v234, s0
	s_nop 3
	s_lshl_b32 s0, s0, 12
	s_add_u32 s76, s64, s0
	s_addc_u32 s77, s65, 0
	global_load_dwordx2 v[212:213], v2, s[76:77]
	global_load_dwordx2 v[214:215], v2, s[76:77] offset:512
	global_load_dwordx2 v[216:217], v2, s[76:77] offset:1024
	global_load_dwordx2 v[218:219], v2, s[76:77] offset:1536
	global_load_dwordx2 v[226:227], v2, s[76:77] offset:2048
	global_load_dwordx2 v[228:229], v2, s[76:77] offset:2560
	global_load_dwordx2 v[230:231], v2, s[76:77] offset:3072
	global_load_dwordx2 v[232:233], v2, s[76:77] offset:3584
.Ln1_y0_8:
	s_waitcnt vmcnt(0)
	s_cmp_eq_u32 s47, 0
	s_cbranch_scc1 .Ln1_a1_8
	v_lshlrev_b32_e32 v238, 16, v196
	v_and_b32_e32 v239, 0xffff0000, v196
	v_fmac_f32_e32 v4, v68, v238
	v_fmac_f32_e32 v5, v69, v239
	v_lshlrev_b32_e32 v238, 16, v197
	v_and_b32_e32 v239, 0xffff0000, v197
	v_fmac_f32_e32 v6, v70, v238
	v_fmac_f32_e32 v7, v71, v239
	v_lshlrev_b32_e32 v238, 16, v198
	v_and_b32_e32 v239, 0xffff0000, v198
	v_fmac_f32_e32 v8, v72, v238
	v_fmac_f32_e32 v9, v73, v239
	v_lshlrev_b32_e32 v238, 16, v199
	v_and_b32_e32 v239, 0xffff0000, v199
	v_fmac_f32_e32 v10, v74, v238
	v_fmac_f32_e32 v11, v75, v239
	v_lshlrev_b32_e32 v238, 16, v200
	v_and_b32_e32 v239, 0xffff0000, v200
	v_fmac_f32_e32 v12, v76, v238
	v_fmac_f32_e32 v13, v77, v239
	v_lshlrev_b32_e32 v238, 16, v201
	v_and_b32_e32 v239, 0xffff0000, v201
	v_fmac_f32_e32 v14, v78, v238
	v_fmac_f32_e32 v15, v79, v239
	v_lshlrev_b32_e32 v238, 16, v202
	v_and_b32_e32 v239, 0xffff0000, v202
	v_fmac_f32_e32 v16, v80, v238
	v_fmac_f32_e32 v17, v81, v239
	v_lshlrev_b32_e32 v238, 16, v203
	v_and_b32_e32 v239, 0xffff0000, v203
	v_fmac_f32_e32 v18, v82, v238
	v_fmac_f32_e32 v19, v83, v239
	v_lshlrev_b32_e32 v238, 16, v204
	v_and_b32_e32 v239, 0xffff0000, v204
	v_fmac_f32_e32 v20, v84, v238
	v_fmac_f32_e32 v21, v85, v239
	v_lshlrev_b32_e32 v238, 16, v205
	v_and_b32_e32 v239, 0xffff0000, v205
	v_fmac_f32_e32 v22, v86, v238
	v_fmac_f32_e32 v23, v87, v239
	v_lshlrev_b32_e32 v238, 16, v206
	v_and_b32_e32 v239, 0xffff0000, v206
	v_fmac_f32_e32 v24, v88, v238
	v_fmac_f32_e32 v25, v89, v239
	v_lshlrev_b32_e32 v238, 16, v207
	v_and_b32_e32 v239, 0xffff0000, v207
	v_fmac_f32_e32 v26, v90, v238
	v_fmac_f32_e32 v27, v91, v239
	v_lshlrev_b32_e32 v238, 16, v208
	v_and_b32_e32 v239, 0xffff0000, v208
	v_fmac_f32_e32 v28, v92, v238
	v_fmac_f32_e32 v29, v93, v239
	v_lshlrev_b32_e32 v238, 16, v209
	v_and_b32_e32 v239, 0xffff0000, v209
	v_fmac_f32_e32 v30, v94, v238
	v_fmac_f32_e32 v31, v95, v239
	v_lshlrev_b32_e32 v238, 16, v210
	v_and_b32_e32 v239, 0xffff0000, v210
	v_fmac_f32_e32 v32, v96, v238
	v_fmac_f32_e32 v33, v97, v239
	v_lshlrev_b32_e32 v238, 16, v211
	v_and_b32_e32 v239, 0xffff0000, v211
	v_fmac_f32_e32 v34, v98, v238
	v_fmac_f32_e32 v35, v99, v239

.Ln1_gd_8:
	global_store_dwordx4 v1, v[4:7], s[16:17]
	global_store_dwordx4 v1, v[8:11], s[16:17] offset:1024
	global_store_dwordx4 v1, v[12:15], s[16:17] offset:2048
	global_store_dwordx4 v1, v[16:19], s[16:17] offset:3072
	global_store_dwordx4 v1, v[20:23], s[18:19]
	global_store_dwordx4 v1, v[24:27], s[18:19] offset:1024
	global_store_dwordx4 v1, v[28:31], s[18:19] offset:2048
	global_store_dwordx4 v1, v[32:35], s[18:19] offset:3072
	v_mul_f32_e32 v236, v4, v4
	v_fmac_f32_e32 v236, v5, v5
	v_fmac_f32_e32 v236, v6, v6
	v_fmac_f32_e32 v236, v7, v7
	v_fmac_f32_e32 v236, v8, v8
	v_fmac_f32_e32 v236, v9, v9
	v_fmac_f32_e32 v236, v10, v10
	v_fmac_f32_e32 v236, v11, v11
	v_fmac_f32_e32 v236, v12, v12
	v_fmac_f32_e32 v236, v13, v13
	v_fmac_f32_e32 v236, v14, v14
	v_fmac_f32_e32 v236, v15, v15
	v_fmac_f32_e32 v236, v16, v16
	v_fmac_f32_e32 v236, v17, v17
	v_fmac_f32_e32 v236, v18, v18
	v_fmac_f32_e32 v236, v19, v19
	v_fmac_f32_e32 v236, v20, v20
	v_fmac_f32_e32 v236, v21, v21
	v_fmac_f32_e32 v236, v22, v22
	v_fmac_f32_e32 v236, v23, v23
	v_fmac_f32_e32 v236, v24, v24
	v_fmac_f32_e32 v236, v25, v25
	v_fmac_f32_e32 v236, v26, v26
	v_fmac_f32_e32 v236, v27, v27
	v_fmac_f32_e32 v236, v28, v28
	v_fmac_f32_e32 v236, v29, v29
	v_fmac_f32_e32 v236, v30, v30
	v_fmac_f32_e32 v236, v31, v31
	v_fmac_f32_e32 v236, v32, v32
	v_fmac_f32_e32 v236, v33, v33
	v_fmac_f32_e32 v236, v34, v34
	v_fmac_f32_e32 v236, v35, v35
	v_fma_f32 v100, v100, v132, v100
	v_fma_f32 v101, v101, v133, v101
	v_fma_f32 v102, v102, v134, v102
	v_fma_f32 v103, v103, v135, v103
	v_fma_f32 v104, v104, v136, v104
	v_fma_f32 v105, v105, v137, v105
	v_fma_f32 v106, v106, v138, v106
	v_fma_f32 v107, v107, v139, v107
	v_fma_f32 v108, v108, v140, v108
	v_fma_f32 v109, v109, v141, v109
	v_fma_f32 v110, v110, v142, v110
	v_fma_f32 v111, v111, v143, v111
	v_fma_f32 v112, v112, v144, v112
	v_fma_f32 v113, v113, v145, v113
	v_fma_f32 v114, v114, v146, v114
	v_fma_f32 v115, v115, v147, v115
	v_fma_f32 v116, v116, v148, v116
	v_fma_f32 v117, v117, v149, v117
	v_fma_f32 v118, v118, v150, v118
	v_fma_f32 v119, v119, v151, v119
	v_fma_f32 v120, v120, v152, v120
	v_fma_f32 v121, v121, v153, v121
	v_fma_f32 v122, v122, v154, v122
	v_fma_f32 v123, v123, v155, v123
	v_fma_f32 v124, v124, v156, v124
	v_fma_f32 v125, v125, v157, v125
	v_fma_f32 v126, v126, v158, v126
	v_fma_f32 v127, v127, v159, v127
	v_fma_f32 v128, v128, v160, v128
	v_fma_f32 v129, v129, v161, v129
	v_fma_f32 v130, v130, v162, v130
	v_fma_f32 v131, v131, v163, v131
	s_nop 1
	v_add_f32_dpp v236, v236, v236 quad_perm:[1,0,3,2] row_mask:0xf bank_mask:0xf
	s_nop 1
	v_add_f32_dpp v236, v236, v236 quad_perm:[2,3,0,1] row_mask:0xf bank_mask:0xf
	s_nop 1
	v_add_f32_dpp v236, v236, v236 row_half_mirror row_mask:0xf bank_mask:0xf
	s_nop 1
	v_add_f32_dpp v236, v236, v236 row_mirror row_mask:0xf bank_mask:0xf
	s_nop 1
	v_readlane_b32 s0, v236, 0
	v_readlane_b32 s1, v236, 16
	v_readlane_b32 s2, v236, 32
	v_readlane_b32 s3, v236, 48
	s_nop 3
	v_mov_b32_e32 v237, s0
	v_add_f32_e32 v237, s1, v237
	v_add_f32_e32 v237, s2, v237
	v_add_f32_e32 v237, s3, v237
	v_mul_f32_e32 v237, 0x3a000000, v237
	v_add_f32_e32 v237, 0x358637bd, v237
	v_rsq_f32_e32 v237, v237
	s_nop 0
	v_mul_f32_e32 v100, v100, v237
	v_mul_f32_e32 v101, v101, v237
	v_mul_f32_e32 v102, v102, v237
	v_mul_f32_e32 v103, v103, v237
	v_mul_f32_e32 v104, v104, v237
	v_mul_f32_e32 v105, v105, v237
	v_mul_f32_e32 v106, v106, v237
	v_mul_f32_e32 v107, v107, v237
	v_mul_f32_e32 v108, v108, v237
	v_mul_f32_e32 v109, v109, v237
	v_mul_f32_e32 v110, v110, v237
	v_mul_f32_e32 v111, v111, v237
	v_mul_f32_e32 v112, v112, v237
	v_mul_f32_e32 v113, v113, v237
	v_mul_f32_e32 v114, v114, v237
	v_mul_f32_e32 v115, v115, v237
	v_mul_f32_e32 v116, v116, v237
	v_mul_f32_e32 v117, v117, v237
	v_mul_f32_e32 v118, v118, v237
	v_mul_f32_e32 v119, v119, v237
	v_mul_f32_e32 v120, v120, v237
	v_mul_f32_e32 v121, v121, v237
	v_mul_f32_e32 v122, v122, v237
	v_mul_f32_e32 v123, v123, v237
	v_mul_f32_e32 v124, v124, v237
	v_mul_f32_e32 v125, v125, v237
	v_mul_f32_e32 v126, v126, v237
	v_mul_f32_e32 v127, v127, v237
	v_mul_f32_e32 v128, v128, v237
	v_mul_f32_e32 v129, v129, v237
	v_mul_f32_e32 v130, v130, v237
	v_mul_f32_e32 v131, v131, v237
	v_fma_f32 v4, v4, v100, v164
	v_fma_f32 v5, v5, v101, v165
	v_fma_f32 v6, v6, v102, v166
	v_fma_f32 v7, v7, v103, v167
	v_cvt_pk_bf16_f32 v238, v4, v5
	v_cvt_pk_bf16_f32 v239, v6, v7
	global_store_dwordx2 v2, v[238:239], s[22:23]
	v_fma_f32 v8, v8, v104, v168
	v_fma_f32 v9, v9, v105, v169
	v_fma_f32 v10, v10, v106, v170
	v_fma_f32 v11, v11, v107, v171
	v_cvt_pk_bf16_f32 v240, v8, v9
	v_cvt_pk_bf16_f32 v241, v10, v11
	global_store_dwordx2 v2, v[240:241], s[22:23] offset:512
	v_fma_f32 v12, v12, v108, v172
	v_fma_f32 v13, v13, v109, v173
	v_fma_f32 v14, v14, v110, v174
	v_fma_f32 v15, v15, v111, v175
	v_cvt_pk_bf16_f32 v238, v12, v13
	v_cvt_pk_bf16_f32 v239, v14, v15
	global_store_dwordx2 v2, v[238:239], s[22:23] offset:1024
	v_fma_f32 v16, v16, v112, v176
	v_fma_f32 v17, v17, v113, v177
	v_fma_f32 v18, v18, v114, v178
	v_fma_f32 v19, v19, v115, v179
	v_cvt_pk_bf16_f32 v240, v16, v17
	v_cvt_pk_bf16_f32 v241, v18, v19
	global_store_dwordx2 v2, v[240:241], s[22:23] offset:1536
	v_fma_f32 v20, v20, v116, v180
	v_fma_f32 v21, v21, v117, v181
	v_fma_f32 v22, v22, v118, v182
	v_fma_f32 v23, v23, v119, v183
	v_cvt_pk_bf16_f32 v238, v20, v21
	v_cvt_pk_bf16_f32 v239, v22, v23
	global_store_dwordx2 v2, v[238:239], s[22:23] offset:2048
	v_fma_f32 v24, v24, v120, v184
	v_fma_f32 v25, v25, v121, v185
	v_fma_f32 v26, v26, v122, v186
	v_fma_f32 v27, v27, v123, v187
	v_cvt_pk_bf16_f32 v240, v24, v25
	v_cvt_pk_bf16_f32 v241, v26, v27
	global_store_dwordx2 v2, v[240:241], s[22:23] offset:2560
	v_fma_f32 v28, v28, v124, v188
	v_fma_f32 v29, v29, v125, v189
	v_fma_f32 v30, v30, v126, v190
	v_fma_f32 v31, v31, v127, v191
	v_cvt_pk_bf16_f32 v238, v28, v29
	v_cvt_pk_bf16_f32 v239, v30, v31
	global_store_dwordx2 v2, v[238:239], s[22:23] offset:3072
	v_fma_f32 v32, v32, v128, v192
	v_fma_f32 v33, v33, v129, v193
	v_fma_f32 v34, v34, v130, v194
	v_fma_f32 v35, v35, v131, v195
	v_cvt_pk_bf16_f32 v240, v32, v33
	v_cvt_pk_bf16_f32 v241, v34, v35
	global_store_dwordx2 v2, v[240:241], s[22:23] offset:3584
	s_mov_b64 s[0:1], 0
.LBB0_2858:
	s_and_b64 vcc, exec, s[0:1]
	s_cbranch_vccz .LBB0_2864
	v_readlane_b32 s4, v251, 59
	v_readlane_b32 s5, v251, 60
	v_readlane_b32 s8, v255, 20
	v_readlane_b32 s10, v251, 61
	v_readfirstlane_b32 s0, v0
	v_readlane_b32 s56, v251, 53
	v_readlane_b32 s57, v251, 54
	v_readlane_b32 s68, v251, 41
	v_readlane_b32 s69, v251, 42
	v_readlane_b32 s70, v251, 45
	v_readlane_b32 s71, v251, 46
	s_nop 3
	s_lshr_b32 s0, s0, 6
	s_add_i32 s10, s10, s0
	s_lshl_b32 s1, s8, 13
	s_add_u32 s56, s56, s1
	s_addc_u32 s57, s57, 0
	s_add_u32 s58, s56, 0x1000
	s_addc_u32 s59, s57, 0
	s_add_u32 s50, s4, 0x3cc90000
	s_addc_u32 s51, s5, 0
	s_mul_i32 s1, s8, 0x6c000
	s_add_i32 s1, s1, 0x10000
	s_add_u32 s52, s4, s1
	s_addc_u32 s53, s5, 0
	v_and_b32_e32 v238, 63, v0
	v_lshlrev_b32_e32 v1, 4, v238
	v_lshlrev_b32_e32 v2, 3, v238
	v_lshlrev_b32_e32 v246, 2, v238
	s_add_i32 s11, s10, 0x0
	s_lshr_b32 s0, s11, 8
	s_mul_i32 s0, s0, 57
	s_lshr_b32 s44, s0, 9
	s_mul_i32 s1, s44, 0x900
	s_sub_i32 s43, s11, s1
	s_lshl_b32 s0, s44, 21
	s_lshl_b32 s1, s43, 13
	s_add_i32 s0, s0, s1
	s_lshl_b32 s2, s44, 24
	s_add_i32 s3, s43, 0xffffff00
	s_lshl_b32 s3, s3, 13
	s_add_i32 s2, s2, s3
	s_cmpk_lt_u32 s43, 0x100
	s_cselect_b32 s0, s0, s2
	s_cselect_b32 s1, s70, s68
	s_cselect_b32 s2, s71, s69
	s_add_u32 s12, s1, s0
	s_addc_u32 s13, s2, 0
	s_add_u32 s14, s12, 0x1000
	s_addc_u32 s15, s13, 0
	global_load_dwordx4 v[4:7], v1, s[12:13]
	global_load_dwordx4 v[8:11], v1, s[12:13] offset:1024
	global_load_dwordx4 v[12:15], v1, s[12:13] offset:2048
	global_load_dwordx4 v[16:19], v1, s[12:13] offset:3072
	global_load_dwordx4 v[20:23], v1, s[14:15]
	global_load_dwordx4 v[24:27], v1, s[14:15] offset:1024
	global_load_dwordx4 v[28:31], v1, s[14:15] offset:2048
	global_load_dwordx4 v[32:35], v1, s[14:15] offset:3072
	s_add_i32 s11, s10, 0x0
	s_lshr_b32 s0, s11, 8
	s_mul_i32 s0, s0, 57
	s_lshr_b32 s44, s0, 9
	s_mul_i32 s1, s44, 0x900
	s_sub_i32 s43, s11, s1
	s_lshl_b32 s1, s11, 12
	s_add_u32 s22, s50, s1
	s_addc_u32 s23, s51, 0
	s_cmpk_lt_u32 s43, 0x100
	s_cselect_b32 s0, 8, s44
	s_mul_i32 s1, s0, 0xc000
	s_add_u32 s28, s52, s1
	s_addc_u32 s29, s53, 0
	s_add_u32 s30, s28, 0x1000
	s_addc_u32 s31, s29, 0
	global_load_dwordx4 v[100:103], v1, s[56:57]
	global_load_dwordx4 v[104:107], v1, s[56:57] offset:1024
	global_load_dwordx4 v[108:111], v1, s[56:57] offset:2048
	global_load_dwordx4 v[112:115], v1, s[56:57] offset:3072
	global_load_dwordx4 v[116:119], v1, s[58:59]
	global_load_dwordx4 v[120:123], v1, s[58:59] offset:1024
	global_load_dwordx4 v[124:127], v1, s[58:59] offset:2048
	global_load_dwordx4 v[128:131], v1, s[58:59] offset:3072
	s_add_u32 s84, s28, 0x2000
	s_addc_u32 s85, s29, 0
	s_add_u32 s86, s28, 0x3000
	s_addc_u32 s87, s29, 0
	global_load_dwordx4 v[68:71], v1, s[28:29]
	global_load_dwordx4 v[132:135], v1, s[84:85]
	global_load_dwordx4 v[72:75], v1, s[28:29] offset:1024
	global_load_dwordx4 v[136:139], v1, s[84:85] offset:1024
	global_load_dwordx4 v[76:79], v1, s[28:29] offset:2048
	global_load_dwordx4 v[140:143], v1, s[84:85] offset:2048
	global_load_dwordx4 v[80:83], v1, s[28:29] offset:3072
	global_load_dwordx4 v[144:147], v1, s[84:85] offset:3072
	global_load_dwordx4 v[84:87], v1, s[30:31]
	global_load_dwordx4 v[148:151], v1, s[86:87]
	global_load_dwordx4 v[88:91], v1, s[30:31] offset:1024
	global_load_dwordx4 v[152:155], v1, s[86:87] offset:1024
	global_load_dwordx4 v[92:95], v1, s[30:31] offset:2048
	global_load_dwordx4 v[156:159], v1, s[86:87] offset:2048
	global_load_dwordx4 v[96:99], v1, s[30:31] offset:3072
	global_load_dwordx4 v[160:163], v1, s[86:87] offset:3072
	s_add_i32 s11, s10, 0x800
	s_lshr_b32 s0, s11, 8
	s_mul_i32 s0, s0, 57
	s_lshr_b32 s44, s0, 9
	s_mul_i32 s1, s44, 0x900
	s_sub_i32 s43, s11, s1
	s_lshl_b32 s0, s44, 21
	s_lshl_b32 s1, s43, 13
	s_add_i32 s0, s0, s1
	s_lshl_b32 s2, s44, 24
	s_add_i32 s3, s43, 0xffffff00
	s_lshl_b32 s3, s3, 13
	s_add_i32 s2, s2, s3
	s_cmpk_lt_u32 s43, 0x100
	s_cselect_b32 s0, s0, s2
	s_cselect_b32 s1, s70, s68
	s_cselect_b32 s2, s71, s69
	s_add_u32 s12, s1, s0
	s_addc_u32 s13, s2, 0
	s_add_u32 s14, s12, 0x1000
	s_addc_u32 s15, s13, 0
	global_load_dwordx4 v[36:39], v1, s[12:13]
	global_load_dwordx4 v[40:43], v1, s[12:13] offset:1024
	global_load_dwordx4 v[44:47], v1, s[12:13] offset:2048
	global_load_dwordx4 v[48:51], v1, s[12:13] offset:3072
	global_load_dwordx4 v[52:55], v1, s[14:15]
	global_load_dwordx4 v[56:59], v1, s[14:15] offset:1024
	global_load_dwordx4 v[60:63], v1, s[14:15] offset:2048
	global_load_dwordx4 v[64:67], v1, s[14:15] offset:3072
	s_waitcnt vmcnt(8)
	v_mul_f32_e32 v236, v4, v4
	v_fmac_f32_e32 v236, v5, v5
	v_fmac_f32_e32 v236, v6, v6
	v_fmac_f32_e32 v236, v7, v7
	v_fmac_f32_e32 v236, v8, v8
	v_fmac_f32_e32 v236, v9, v9
	v_fmac_f32_e32 v236, v10, v10
	v_fmac_f32_e32 v236, v11, v11
	v_fmac_f32_e32 v236, v12, v12
	v_fmac_f32_e32 v236, v13, v13
	v_fmac_f32_e32 v236, v14, v14
	v_fmac_f32_e32 v236, v15, v15
	v_fmac_f32_e32 v236, v16, v16
	v_fmac_f32_e32 v236, v17, v17
	v_fmac_f32_e32 v236, v18, v18
	v_fmac_f32_e32 v236, v19, v19
	v_fmac_f32_e32 v236, v20, v20
	v_fmac_f32_e32 v236, v21, v21
	v_fmac_f32_e32 v236, v22, v22
	v_fmac_f32_e32 v236, v23, v23
	v_fmac_f32_e32 v236, v24, v24
	v_fmac_f32_e32 v236, v25, v25
	v_fmac_f32_e32 v236, v26, v26
	v_fmac_f32_e32 v236, v27, v27
	v_fmac_f32_e32 v236, v28, v28
	v_fmac_f32_e32 v236, v29, v29
	v_fmac_f32_e32 v236, v30, v30
	v_fmac_f32_e32 v236, v31, v31
	v_fmac_f32_e32 v236, v32, v32
	v_fmac_f32_e32 v236, v33, v33
	v_fmac_f32_e32 v236, v34, v34
	v_fmac_f32_e32 v236, v35, v35
	v_fma_f32 v100, v100, v132, v100
	v_fma_f32 v101, v101, v133, v101
	v_fma_f32 v102, v102, v134, v102
	v_fma_f32 v103, v103, v135, v103
	v_fma_f32 v104, v104, v136, v104
	v_fma_f32 v105, v105, v137, v105
	v_fma_f32 v106, v106, v138, v106
	v_fma_f32 v107, v107, v139, v107
	v_fma_f32 v108, v108, v140, v108
	v_fma_f32 v109, v109, v141, v109
	v_fma_f32 v110, v110, v142, v110
	v_fma_f32 v111, v111, v143, v111
	v_fma_f32 v112, v112, v144, v112
	v_fma_f32 v113, v113, v145, v113
	v_fma_f32 v114, v114, v146, v114
	v_fma_f32 v115, v115, v147, v115
	v_fma_f32 v116, v116, v148, v116
	v_fma_f32 v117, v117, v149, v117
	v_fma_f32 v118, v118, v150, v118
	v_fma_f32 v119, v119, v151, v119
	v_fma_f32 v120, v120, v152, v120
	v_fma_f32 v121, v121, v153, v121
	v_fma_f32 v122, v122, v154, v122
	v_fma_f32 v123, v123, v155, v123
	v_fma_f32 v124, v124, v156, v124
	v_fma_f32 v125, v125, v157, v125
	v_fma_f32 v126, v126, v158, v126
	v_fma_f32 v127, v127, v159, v127
	v_fma_f32 v128, v128, v160, v128
	v_fma_f32 v129, v129, v161, v129
	v_fma_f32 v130, v130, v162, v130
	v_fma_f32 v131, v131, v163, v131
	s_nop 1
	v_add_f32_dpp v236, v236, v236 quad_perm:[1,0,3,2] row_mask:0xf bank_mask:0xf
	s_nop 1
	v_add_f32_dpp v236, v236, v236 quad_perm:[2,3,0,1] row_mask:0xf bank_mask:0xf
	s_nop 1
	v_add_f32_dpp v236, v236, v236 row_half_mirror row_mask:0xf bank_mask:0xf
	s_nop 1
	v_add_f32_dpp v236, v236, v236 row_mirror row_mask:0xf bank_mask:0xf
	s_nop 1
	v_readlane_b32 s0, v236, 0
	v_readlane_b32 s1, v236, 16
	v_readlane_b32 s2, v236, 32
	v_readlane_b32 s3, v236, 48
	s_nop 3
	v_mov_b32_e32 v237, s0
	v_add_f32_e32 v237, s1, v237
	v_add_f32_e32 v237, s2, v237
	v_add_f32_e32 v237, s3, v237
	v_mul_f32_e32 v237, 0x3a000000, v237
	v_add_f32_e32 v237, 0x358637bd, v237
	v_rsq_f32_e32 v237, v237
	s_nop 0
	v_mul_f32_e32 v100, v100, v237
	v_mul_f32_e32 v101, v101, v237
	v_mul_f32_e32 v102, v102, v237
	v_mul_f32_e32 v103, v103, v237
	v_mul_f32_e32 v104, v104, v237
	v_mul_f32_e32 v105, v105, v237
	v_mul_f32_e32 v106, v106, v237
	v_mul_f32_e32 v107, v107, v237
	v_mul_f32_e32 v108, v108, v237
	v_mul_f32_e32 v109, v109, v237
	v_mul_f32_e32 v110, v110, v237
	v_mul_f32_e32 v111, v111, v237
	v_mul_f32_e32 v112, v112, v237
	v_mul_f32_e32 v113, v113, v237
	v_mul_f32_e32 v114, v114, v237
	v_mul_f32_e32 v115, v115, v237
	v_mul_f32_e32 v116, v116, v237
	v_mul_f32_e32 v117, v117, v237
	v_mul_f32_e32 v118, v118, v237
	v_mul_f32_e32 v119, v119, v237
	v_mul_f32_e32 v120, v120, v237
	v_mul_f32_e32 v121, v121, v237
	v_mul_f32_e32 v122, v122, v237
	v_mul_f32_e32 v123, v123, v237
	v_mul_f32_e32 v124, v124, v237
	v_mul_f32_e32 v125, v125, v237
	v_mul_f32_e32 v126, v126, v237
	v_mul_f32_e32 v127, v127, v237
	v_mul_f32_e32 v128, v128, v237
	v_mul_f32_e32 v129, v129, v237
	v_mul_f32_e32 v130, v130, v237
	v_mul_f32_e32 v131, v131, v237
	v_fma_f32 v4, v4, v100, v68
	v_fma_f32 v5, v5, v101, v69
	v_fma_f32 v6, v6, v102, v70
	v_fma_f32 v7, v7, v103, v71
	v_cvt_pk_bf16_f32 v238, v4, v5
	v_cvt_pk_bf16_f32 v239, v6, v7
	global_store_dwordx2 v2, v[238:239], s[22:23]
	v_fma_f32 v8, v8, v104, v72
	v_fma_f32 v9, v9, v105, v73
	v_fma_f32 v10, v10, v106, v74
	v_fma_f32 v11, v11, v107, v75
	v_cvt_pk_bf16_f32 v240, v8, v9
	v_cvt_pk_bf16_f32 v241, v10, v11
	global_store_dwordx2 v2, v[240:241], s[22:23] offset:512
	v_fma_f32 v12, v12, v108, v76
	v_fma_f32 v13, v13, v109, v77
	v_fma_f32 v14, v14, v110, v78
	v_fma_f32 v15, v15, v111, v79
	v_cvt_pk_bf16_f32 v238, v12, v13
	v_cvt_pk_bf16_f32 v239, v14, v15
	global_store_dwordx2 v2, v[238:239], s[22:23] offset:1024
	v_fma_f32 v16, v16, v112, v80
	v_fma_f32 v17, v17, v113, v81
	v_fma_f32 v18, v18, v114, v82
	v_fma_f32 v19, v19, v115, v83
	v_cvt_pk_bf16_f32 v240, v16, v17
	v_cvt_pk_bf16_f32 v241, v18, v19
	global_store_dwordx2 v2, v[240:241], s[22:23] offset:1536
	v_fma_f32 v20, v20, v116, v84
	v_fma_f32 v21, v21, v117, v85
	v_fma_f32 v22, v22, v118, v86
	v_fma_f32 v23, v23, v119, v87
	v_cvt_pk_bf16_f32 v238, v20, v21
	v_cvt_pk_bf16_f32 v239, v22, v23
	global_store_dwordx2 v2, v[238:239], s[22:23] offset:2048
	v_fma_f32 v24, v24, v120, v88
	v_fma_f32 v25, v25, v121, v89
	v_fma_f32 v26, v26, v122, v90
	v_fma_f32 v27, v27, v123, v91
	v_cvt_pk_bf16_f32 v240, v24, v25
	v_cvt_pk_bf16_f32 v241, v26, v27
	global_store_dwordx2 v2, v[240:241], s[22:23] offset:2560
	v_fma_f32 v28, v28, v124, v92
	v_fma_f32 v29, v29, v125, v93
	v_fma_f32 v30, v30, v126, v94
	v_fma_f32 v31, v31, v127, v95
	v_cvt_pk_bf16_f32 v238, v28, v29
	v_cvt_pk_bf16_f32 v239, v30, v31
	global_store_dwordx2 v2, v[238:239], s[22:23] offset:3072
	v_fma_f32 v32, v32, v128, v96
	v_fma_f32 v33, v33, v129, v97
	v_fma_f32 v34, v34, v130, v98
	v_fma_f32 v35, v35, v131, v99
	v_cvt_pk_bf16_f32 v240, v32, v33
	v_cvt_pk_bf16_f32 v241, v34, v35
	global_store_dwordx2 v2, v[240:241], s[22:23] offset:3584
	s_add_i32 s11, s10, 0x800
	s_lshr_b32 s0, s11, 8
	s_mul_i32 s0, s0, 57
	s_lshr_b32 s44, s0, 9
	s_mul_i32 s1, s44, 0x900
	s_sub_i32 s43, s11, s1
	s_lshl_b32 s1, s11, 12
	s_add_u32 s22, s50, s1
	s_addc_u32 s23, s51, 0
	s_cmpk_lt_u32 s43, 0x100
	s_cselect_b32 s0, 8, s44
	s_mul_i32 s1, s0, 0xc000
	s_add_u32 s28, s52, s1
	s_addc_u32 s29, s53, 0
	s_add_u32 s30, s28, 0x1000
	s_addc_u32 s31, s29, 0
	global_load_dwordx4 v[100:103], v1, s[56:57]
	global_load_dwordx4 v[104:107], v1, s[56:57] offset:1024
	global_load_dwordx4 v[108:111], v1, s[56:57] offset:2048
	global_load_dwordx4 v[112:115], v1, s[56:57] offset:3072
	global_load_dwordx4 v[116:119], v1, s[58:59]
	global_load_dwordx4 v[120:123], v1, s[58:59] offset:1024
	global_load_dwordx4 v[124:127], v1, s[58:59] offset:2048
	global_load_dwordx4 v[128:131], v1, s[58:59] offset:3072
	s_add_u32 s84, s28, 0x2000
	s_addc_u32 s85, s29, 0
	s_add_u32 s86, s28, 0x3000
	s_addc_u32 s87, s29, 0
	global_load_dwordx4 v[68:71], v1, s[28:29]
	global_load_dwordx4 v[132:135], v1, s[84:85]
	global_load_dwordx4 v[72:75], v1, s[28:29] offset:1024
	global_load_dwordx4 v[136:139], v1, s[84:85] offset:1024
	global_load_dwordx4 v[76:79], v1, s[28:29] offset:2048
	global_load_dwordx4 v[140:143], v1, s[84:85] offset:2048
	global_load_dwordx4 v[80:83], v1, s[28:29] offset:3072
	global_load_dwordx4 v[144:147], v1, s[84:85] offset:3072
	global_load_dwordx4 v[84:87], v1, s[30:31]
	global_load_dwordx4 v[148:151], v1, s[86:87]
	global_load_dwordx4 v[88:91], v1, s[30:31] offset:1024
	global_load_dwordx4 v[152:155], v1, s[86:87] offset:1024
	global_load_dwordx4 v[92:95], v1, s[30:31] offset:2048
	global_load_dwordx4 v[156:159], v1, s[86:87] offset:2048
	global_load_dwordx4 v[96:99], v1, s[30:31] offset:3072
	global_load_dwordx4 v[160:163], v1, s[86:87] offset:3072
	s_add_i32 s11, s10, 0x1000
	s_lshr_b32 s0, s11, 8
	s_mul_i32 s0, s0, 57
	s_lshr_b32 s44, s0, 9
	s_mul_i32 s1, s44, 0x900
	s_sub_i32 s43, s11, s1
	s_lshl_b32 s0, s44, 21
	s_lshl_b32 s1, s43, 13
	s_add_i32 s0, s0, s1
	s_lshl_b32 s2, s44, 24
	s_add_i32 s3, s43, 0xffffff00
	s_lshl_b32 s3, s3, 13
	s_add_i32 s2, s2, s3
	s_cmpk_lt_u32 s43, 0x100
	s_cselect_b32 s0, s0, s2
	s_cselect_b32 s1, s70, s68
	s_cselect_b32 s2, s71, s69
	s_add_u32 s12, s1, s0
	s_addc_u32 s13, s2, 0
	s_add_u32 s14, s12, 0x1000
	s_addc_u32 s15, s13, 0
	global_load_dwordx4 v[4:7], v1, s[12:13]
	global_load_dwordx4 v[8:11], v1, s[12:13] offset:1024
	global_load_dwordx4 v[12:15], v1, s[12:13] offset:2048
	global_load_dwordx4 v[16:19], v1, s[12:13] offset:3072
	global_load_dwordx4 v[20:23], v1, s[14:15]
	global_load_dwordx4 v[24:27], v1, s[14:15] offset:1024
	global_load_dwordx4 v[28:31], v1, s[14:15] offset:2048
	global_load_dwordx4 v[32:35], v1, s[14:15] offset:3072
	s_waitcnt vmcnt(8)
	v_mul_f32_e32 v236, v36, v36
	v_fmac_f32_e32 v236, v37, v37
	v_fmac_f32_e32 v236, v38, v38
	v_fmac_f32_e32 v236, v39, v39
	v_fmac_f32_e32 v236, v40, v40
	v_fmac_f32_e32 v236, v41, v41
	v_fmac_f32_e32 v236, v42, v42
	v_fmac_f32_e32 v236, v43, v43
	v_fmac_f32_e32 v236, v44, v44
	v_fmac_f32_e32 v236, v45, v45
	v_fmac_f32_e32 v236, v46, v46
	v_fmac_f32_e32 v236, v47, v47
	v_fmac_f32_e32 v236, v48, v48
	v_fmac_f32_e32 v236, v49, v49
	v_fmac_f32_e32 v236, v50, v50
	v_fmac_f32_e32 v236, v51, v51
	v_fmac_f32_e32 v236, v52, v52
	v_fmac_f32_e32 v236, v53, v53
	v_fmac_f32_e32 v236, v54, v54
	v_fmac_f32_e32 v236, v55, v55
	v_fmac_f32_e32 v236, v56, v56
	v_fmac_f32_e32 v236, v57, v57
	v_fmac_f32_e32 v236, v58, v58
	v_fmac_f32_e32 v236, v59, v59
	v_fmac_f32_e32 v236, v60, v60
	v_fmac_f32_e32 v236, v61, v61
	v_fmac_f32_e32 v236, v62, v62
	v_fmac_f32_e32 v236, v63, v63
	v_fmac_f32_e32 v236, v64, v64
	v_fmac_f32_e32 v236, v65, v65
	v_fmac_f32_e32 v236, v66, v66
	v_fmac_f32_e32 v236, v67, v67
	v_fma_f32 v100, v100, v132, v100
	v_fma_f32 v101, v101, v133, v101
	v_fma_f32 v102, v102, v134, v102
	v_fma_f32 v103, v103, v135, v103
	v_fma_f32 v104, v104, v136, v104
	v_fma_f32 v105, v105, v137, v105
	v_fma_f32 v106, v106, v138, v106
	v_fma_f32 v107, v107, v139, v107
	v_fma_f32 v108, v108, v140, v108
	v_fma_f32 v109, v109, v141, v109
	v_fma_f32 v110, v110, v142, v110
	v_fma_f32 v111, v111, v143, v111
	v_fma_f32 v112, v112, v144, v112
	v_fma_f32 v113, v113, v145, v113
	v_fma_f32 v114, v114, v146, v114
	v_fma_f32 v115, v115, v147, v115
	v_fma_f32 v116, v116, v148, v116
	v_fma_f32 v117, v117, v149, v117
	v_fma_f32 v118, v118, v150, v118
	v_fma_f32 v119, v119, v151, v119
	v_fma_f32 v120, v120, v152, v120
	v_fma_f32 v121, v121, v153, v121
	v_fma_f32 v122, v122, v154, v122
	v_fma_f32 v123, v123, v155, v123
	v_fma_f32 v124, v124, v156, v124
	v_fma_f32 v125, v125, v157, v125
	v_fma_f32 v126, v126, v158, v126
	v_fma_f32 v127, v127, v159, v127
	v_fma_f32 v128, v128, v160, v128
	v_fma_f32 v129, v129, v161, v129
	v_fma_f32 v130, v130, v162, v130
	v_fma_f32 v131, v131, v163, v131
	s_nop 1
	v_add_f32_dpp v236, v236, v236 quad_perm:[1,0,3,2] row_mask:0xf bank_mask:0xf
	s_nop 1
	v_add_f32_dpp v236, v236, v236 quad_perm:[2,3,0,1] row_mask:0xf bank_mask:0xf
	s_nop 1
	v_add_f32_dpp v236, v236, v236 row_half_mirror row_mask:0xf bank_mask:0xf
	s_nop 1
	v_add_f32_dpp v236, v236, v236 row_mirror row_mask:0xf bank_mask:0xf
	s_nop 1
	v_readlane_b32 s0, v236, 0
	v_readlane_b32 s1, v236, 16
	v_readlane_b32 s2, v236, 32
	v_readlane_b32 s3, v236, 48
	s_nop 3
	v_mov_b32_e32 v237, s0
	v_add_f32_e32 v237, s1, v237
	v_add_f32_e32 v237, s2, v237
	v_add_f32_e32 v237, s3, v237
	v_mul_f32_e32 v237, 0x3a000000, v237
	v_add_f32_e32 v237, 0x358637bd, v237
	v_rsq_f32_e32 v237, v237
	s_nop 0
	v_mul_f32_e32 v100, v100, v237
	v_mul_f32_e32 v101, v101, v237
	v_mul_f32_e32 v102, v102, v237
	v_mul_f32_e32 v103, v103, v237
	v_mul_f32_e32 v104, v104, v237
	v_mul_f32_e32 v105, v105, v237
	v_mul_f32_e32 v106, v106, v237
	v_mul_f32_e32 v107, v107, v237
	v_mul_f32_e32 v108, v108, v237
	v_mul_f32_e32 v109, v109, v237
	v_mul_f32_e32 v110, v110, v237
	v_mul_f32_e32 v111, v111, v237
	v_mul_f32_e32 v112, v112, v237
	v_mul_f32_e32 v113, v113, v237
	v_mul_f32_e32 v114, v114, v237
	v_mul_f32_e32 v115, v115, v237
	v_mul_f32_e32 v116, v116, v237
	v_mul_f32_e32 v117, v117, v237
	v_mul_f32_e32 v118, v118, v237
	v_mul_f32_e32 v119, v119, v237
	v_mul_f32_e32 v120, v120, v237
	v_mul_f32_e32 v121, v121, v237
	v_mul_f32_e32 v122, v122, v237
	v_mul_f32_e32 v123, v123, v237
	v_mul_f32_e32 v124, v124, v237
	v_mul_f32_e32 v125, v125, v237
	v_mul_f32_e32 v126, v126, v237
	v_mul_f32_e32 v127, v127, v237
	v_mul_f32_e32 v128, v128, v237
	v_mul_f32_e32 v129, v129, v237
	v_mul_f32_e32 v130, v130, v237
	v_mul_f32_e32 v131, v131, v237
	v_fma_f32 v36, v36, v100, v68
	v_fma_f32 v37, v37, v101, v69
	v_fma_f32 v38, v38, v102, v70
	v_fma_f32 v39, v39, v103, v71
	v_cvt_pk_bf16_f32 v238, v36, v37
	v_cvt_pk_bf16_f32 v239, v38, v39
	global_store_dwordx2 v2, v[238:239], s[22:23]
	v_fma_f32 v40, v40, v104, v72
	v_fma_f32 v41, v41, v105, v73
	v_fma_f32 v42, v42, v106, v74
	v_fma_f32 v43, v43, v107, v75
	v_cvt_pk_bf16_f32 v240, v40, v41
	v_cvt_pk_bf16_f32 v241, v42, v43
	global_store_dwordx2 v2, v[240:241], s[22:23] offset:512
	v_fma_f32 v44, v44, v108, v76
	v_fma_f32 v45, v45, v109, v77
	v_fma_f32 v46, v46, v110, v78
	v_fma_f32 v47, v47, v111, v79
	v_cvt_pk_bf16_f32 v238, v44, v45
	v_cvt_pk_bf16_f32 v239, v46, v47
	global_store_dwordx2 v2, v[238:239], s[22:23] offset:1024
	v_fma_f32 v48, v48, v112, v80
	v_fma_f32 v49, v49, v113, v81
	v_fma_f32 v50, v50, v114, v82
	v_fma_f32 v51, v51, v115, v83
	v_cvt_pk_bf16_f32 v240, v48, v49
	v_cvt_pk_bf16_f32 v241, v50, v51
	global_store_dwordx2 v2, v[240:241], s[22:23] offset:1536
	v_fma_f32 v52, v52, v116, v84
	v_fma_f32 v53, v53, v117, v85
	v_fma_f32 v54, v54, v118, v86
	v_fma_f32 v55, v55, v119, v87
	v_cvt_pk_bf16_f32 v238, v52, v53
	v_cvt_pk_bf16_f32 v239, v54, v55
	global_store_dwordx2 v2, v[238:239], s[22:23] offset:2048
	v_fma_f32 v56, v56, v120, v88
	v_fma_f32 v57, v57, v121, v89
	v_fma_f32 v58, v58, v122, v90
	v_fma_f32 v59, v59, v123, v91
	v_cvt_pk_bf16_f32 v240, v56, v57
	v_cvt_pk_bf16_f32 v241, v58, v59
	global_store_dwordx2 v2, v[240:241], s[22:23] offset:2560
	v_fma_f32 v60, v60, v124, v92
	v_fma_f32 v61, v61, v125, v93
	v_fma_f32 v62, v62, v126, v94
	v_fma_f32 v63, v63, v127, v95
	v_cvt_pk_bf16_f32 v238, v60, v61
	v_cvt_pk_bf16_f32 v239, v62, v63
	global_store_dwordx2 v2, v[238:239], s[22:23] offset:3072
	v_fma_f32 v64, v64, v128, v96
	v_fma_f32 v65, v65, v129, v97
	v_fma_f32 v66, v66, v130, v98
	v_fma_f32 v67, v67, v131, v99
	v_cvt_pk_bf16_f32 v240, v64, v65
	v_cvt_pk_bf16_f32 v241, v66, v67
	global_store_dwordx2 v2, v[240:241], s[22:23] offset:3584
	s_add_i32 s11, s10, 0x1000
	s_lshr_b32 s0, s11, 8
	s_mul_i32 s0, s0, 57
	s_lshr_b32 s44, s0, 9
	s_mul_i32 s1, s44, 0x900
	s_sub_i32 s43, s11, s1
	s_lshl_b32 s1, s11, 12
	s_add_u32 s22, s50, s1
	s_addc_u32 s23, s51, 0
	s_cmpk_lt_u32 s43, 0x100
	s_cselect_b32 s0, 8, s44
	s_mul_i32 s1, s0, 0xc000
	s_add_u32 s28, s52, s1
	s_addc_u32 s29, s53, 0
	s_add_u32 s30, s28, 0x1000
	s_addc_u32 s31, s29, 0
	global_load_dwordx4 v[100:103], v1, s[56:57]
	global_load_dwordx4 v[104:107], v1, s[56:57] offset:1024
	global_load_dwordx4 v[108:111], v1, s[56:57] offset:2048
	global_load_dwordx4 v[112:115], v1, s[56:57] offset:3072
	global_load_dwordx4 v[116:119], v1, s[58:59]
	global_load_dwordx4 v[120:123], v1, s[58:59] offset:1024
	global_load_dwordx4 v[124:127], v1, s[58:59] offset:2048
	global_load_dwordx4 v[128:131], v1, s[58:59] offset:3072
	s_add_u32 s84, s28, 0x2000
	s_addc_u32 s85, s29, 0
	s_add_u32 s86, s28, 0x3000
	s_addc_u32 s87, s29, 0
	global_load_dwordx4 v[68:71], v1, s[28:29]
	global_load_dwordx4 v[132:135], v1, s[84:85]
	global_load_dwordx4 v[72:75], v1, s[28:29] offset:1024
	global_load_dwordx4 v[136:139], v1, s[84:85] offset:1024
	global_load_dwordx4 v[76:79], v1, s[28:29] offset:2048
	global_load_dwordx4 v[140:143], v1, s[84:85] offset:2048
	global_load_dwordx4 v[80:83], v1, s[28:29] offset:3072
	global_load_dwordx4 v[144:147], v1, s[84:85] offset:3072
	global_load_dwordx4 v[84:87], v1, s[30:31]
	global_load_dwordx4 v[148:151], v1, s[86:87]
	global_load_dwordx4 v[88:91], v1, s[30:31] offset:1024
	global_load_dwordx4 v[152:155], v1, s[86:87] offset:1024
	global_load_dwordx4 v[92:95], v1, s[30:31] offset:2048
	global_load_dwordx4 v[156:159], v1, s[86:87] offset:2048
	global_load_dwordx4 v[96:99], v1, s[30:31] offset:3072
	global_load_dwordx4 v[160:163], v1, s[86:87] offset:3072
	s_add_i32 s11, s10, 0x1800
	s_lshr_b32 s0, s11, 8
	s_mul_i32 s0, s0, 57
	s_lshr_b32 s44, s0, 9
	s_mul_i32 s1, s44, 0x900
	s_sub_i32 s43, s11, s1
	s_lshl_b32 s0, s44, 21
	s_lshl_b32 s1, s43, 13
	s_add_i32 s0, s0, s1
	s_lshl_b32 s2, s44, 24
	s_add_i32 s3, s43, 0xffffff00
	s_lshl_b32 s3, s3, 13
	s_add_i32 s2, s2, s3
	s_cmpk_lt_u32 s43, 0x100
	s_cselect_b32 s0, s0, s2
	s_cselect_b32 s1, s70, s68
	s_cselect_b32 s2, s71, s69
	s_add_u32 s12, s1, s0
	s_addc_u32 s13, s2, 0
	s_add_u32 s14, s12, 0x1000
	s_addc_u32 s15, s13, 0
	global_load_dwordx4 v[36:39], v1, s[12:13]
	global_load_dwordx4 v[40:43], v1, s[12:13] offset:1024
	global_load_dwordx4 v[44:47], v1, s[12:13] offset:2048
	global_load_dwordx4 v[48:51], v1, s[12:13] offset:3072
	global_load_dwordx4 v[52:55], v1, s[14:15]
	global_load_dwordx4 v[56:59], v1, s[14:15] offset:1024
	global_load_dwordx4 v[60:63], v1, s[14:15] offset:2048
	global_load_dwordx4 v[64:67], v1, s[14:15] offset:3072
	s_waitcnt vmcnt(8)
	v_mul_f32_e32 v236, v4, v4
	v_fmac_f32_e32 v236, v5, v5
	v_fmac_f32_e32 v236, v6, v6
	v_fmac_f32_e32 v236, v7, v7
	v_fmac_f32_e32 v236, v8, v8
	v_fmac_f32_e32 v236, v9, v9
	v_fmac_f32_e32 v236, v10, v10
	v_fmac_f32_e32 v236, v11, v11
	v_fmac_f32_e32 v236, v12, v12
	v_fmac_f32_e32 v236, v13, v13
	v_fmac_f32_e32 v236, v14, v14
	v_fmac_f32_e32 v236, v15, v15
	v_fmac_f32_e32 v236, v16, v16
	v_fmac_f32_e32 v236, v17, v17
	v_fmac_f32_e32 v236, v18, v18
	v_fmac_f32_e32 v236, v19, v19
	v_fmac_f32_e32 v236, v20, v20
	v_fmac_f32_e32 v236, v21, v21
	v_fmac_f32_e32 v236, v22, v22
	v_fmac_f32_e32 v236, v23, v23
	v_fmac_f32_e32 v236, v24, v24
	v_fmac_f32_e32 v236, v25, v25
	v_fmac_f32_e32 v236, v26, v26
	v_fmac_f32_e32 v236, v27, v27
	v_fmac_f32_e32 v236, v28, v28
	v_fmac_f32_e32 v236, v29, v29
	v_fmac_f32_e32 v236, v30, v30
	v_fmac_f32_e32 v236, v31, v31
	v_fmac_f32_e32 v236, v32, v32
	v_fmac_f32_e32 v236, v33, v33
	v_fmac_f32_e32 v236, v34, v34
	v_fmac_f32_e32 v236, v35, v35
	v_fma_f32 v100, v100, v132, v100
	v_fma_f32 v101, v101, v133, v101
	v_fma_f32 v102, v102, v134, v102
	v_fma_f32 v103, v103, v135, v103
	v_fma_f32 v104, v104, v136, v104
	v_fma_f32 v105, v105, v137, v105
	v_fma_f32 v106, v106, v138, v106
	v_fma_f32 v107, v107, v139, v107
	v_fma_f32 v108, v108, v140, v108
	v_fma_f32 v109, v109, v141, v109
	v_fma_f32 v110, v110, v142, v110
	v_fma_f32 v111, v111, v143, v111
	v_fma_f32 v112, v112, v144, v112
	v_fma_f32 v113, v113, v145, v113
	v_fma_f32 v114, v114, v146, v114
	v_fma_f32 v115, v115, v147, v115
	v_fma_f32 v116, v116, v148, v116
	v_fma_f32 v117, v117, v149, v117
	v_fma_f32 v118, v118, v150, v118
	v_fma_f32 v119, v119, v151, v119
	v_fma_f32 v120, v120, v152, v120
	v_fma_f32 v121, v121, v153, v121
	v_fma_f32 v122, v122, v154, v122
	v_fma_f32 v123, v123, v155, v123
	v_fma_f32 v124, v124, v156, v124
	v_fma_f32 v125, v125, v157, v125
	v_fma_f32 v126, v126, v158, v126
	v_fma_f32 v127, v127, v159, v127
	v_fma_f32 v128, v128, v160, v128
	v_fma_f32 v129, v129, v161, v129
	v_fma_f32 v130, v130, v162, v130
	v_fma_f32 v131, v131, v163, v131
	s_nop 1
	v_add_f32_dpp v236, v236, v236 quad_perm:[1,0,3,2] row_mask:0xf bank_mask:0xf
	s_nop 1
	v_add_f32_dpp v236, v236, v236 quad_perm:[2,3,0,1] row_mask:0xf bank_mask:0xf
	s_nop 1
	v_add_f32_dpp v236, v236, v236 row_half_mirror row_mask:0xf bank_mask:0xf
	s_nop 1
	v_add_f32_dpp v236, v236, v236 row_mirror row_mask:0xf bank_mask:0xf
	s_nop 1
	v_readlane_b32 s0, v236, 0
	v_readlane_b32 s1, v236, 16
	v_readlane_b32 s2, v236, 32
	v_readlane_b32 s3, v236, 48
	s_nop 3
	v_mov_b32_e32 v237, s0
	v_add_f32_e32 v237, s1, v237
	v_add_f32_e32 v237, s2, v237
	v_add_f32_e32 v237, s3, v237
	v_mul_f32_e32 v237, 0x3a000000, v237
	v_add_f32_e32 v237, 0x358637bd, v237
	v_rsq_f32_e32 v237, v237
	s_nop 0
	v_mul_f32_e32 v100, v100, v237
	v_mul_f32_e32 v101, v101, v237
	v_mul_f32_e32 v102, v102, v237
	v_mul_f32_e32 v103, v103, v237
	v_mul_f32_e32 v104, v104, v237
	v_mul_f32_e32 v105, v105, v237
	v_mul_f32_e32 v106, v106, v237
	v_mul_f32_e32 v107, v107, v237
	v_mul_f32_e32 v108, v108, v237
	v_mul_f32_e32 v109, v109, v237
	v_mul_f32_e32 v110, v110, v237
	v_mul_f32_e32 v111, v111, v237
	v_mul_f32_e32 v112, v112, v237
	v_mul_f32_e32 v113, v113, v237
	v_mul_f32_e32 v114, v114, v237
	v_mul_f32_e32 v115, v115, v237
	v_mul_f32_e32 v116, v116, v237
	v_mul_f32_e32 v117, v117, v237
	v_mul_f32_e32 v118, v118, v237
	v_mul_f32_e32 v119, v119, v237
	v_mul_f32_e32 v120, v120, v237
	v_mul_f32_e32 v121, v121, v237
	v_mul_f32_e32 v122, v122, v237
	v_mul_f32_e32 v123, v123, v237
	v_mul_f32_e32 v124, v124, v237
	v_mul_f32_e32 v125, v125, v237
	v_mul_f32_e32 v126, v126, v237
	v_mul_f32_e32 v127, v127, v237
	v_mul_f32_e32 v128, v128, v237
	v_mul_f32_e32 v129, v129, v237
	v_mul_f32_e32 v130, v130, v237
	v_mul_f32_e32 v131, v131, v237
	v_fma_f32 v4, v4, v100, v68
	v_fma_f32 v5, v5, v101, v69
	v_fma_f32 v6, v6, v102, v70
	v_fma_f32 v7, v7, v103, v71
	v_cvt_pk_bf16_f32 v238, v4, v5
	v_cvt_pk_bf16_f32 v239, v6, v7
	global_store_dwordx2 v2, v[238:239], s[22:23]
	v_fma_f32 v8, v8, v104, v72
	v_fma_f32 v9, v9, v105, v73
	v_fma_f32 v10, v10, v106, v74
	v_fma_f32 v11, v11, v107, v75
	v_cvt_pk_bf16_f32 v240, v8, v9
	v_cvt_pk_bf16_f32 v241, v10, v11
	global_store_dwordx2 v2, v[240:241], s[22:23] offset:512
	v_fma_f32 v12, v12, v108, v76
	v_fma_f32 v13, v13, v109, v77
	v_fma_f32 v14, v14, v110, v78
	v_fma_f32 v15, v15, v111, v79
	v_cvt_pk_bf16_f32 v238, v12, v13
	v_cvt_pk_bf16_f32 v239, v14, v15
	global_store_dwordx2 v2, v[238:239], s[22:23] offset:1024
	v_fma_f32 v16, v16, v112, v80
	v_fma_f32 v17, v17, v113, v81
	v_fma_f32 v18, v18, v114, v82
	v_fma_f32 v19, v19, v115, v83
	v_cvt_pk_bf16_f32 v240, v16, v17
	v_cvt_pk_bf16_f32 v241, v18, v19
	global_store_dwordx2 v2, v[240:241], s[22:23] offset:1536
	v_fma_f32 v20, v20, v116, v84
	v_fma_f32 v21, v21, v117, v85
	v_fma_f32 v22, v22, v118, v86
	v_fma_f32 v23, v23, v119, v87
	v_cvt_pk_bf16_f32 v238, v20, v21
	v_cvt_pk_bf16_f32 v239, v22, v23
	global_store_dwordx2 v2, v[238:239], s[22:23] offset:2048
	v_fma_f32 v24, v24, v120, v88
	v_fma_f32 v25, v25, v121, v89
	v_fma_f32 v26, v26, v122, v90
	v_fma_f32 v27, v27, v123, v91
	v_cvt_pk_bf16_f32 v240, v24, v25
	v_cvt_pk_bf16_f32 v241, v26, v27
	global_store_dwordx2 v2, v[240:241], s[22:23] offset:2560
	v_fma_f32 v28, v28, v124, v92
	v_fma_f32 v29, v29, v125, v93
	v_fma_f32 v30, v30, v126, v94
	v_fma_f32 v31, v31, v127, v95
	v_cvt_pk_bf16_f32 v238, v28, v29
	v_cvt_pk_bf16_f32 v239, v30, v31
	global_store_dwordx2 v2, v[238:239], s[22:23] offset:3072
	v_fma_f32 v32, v32, v128, v96
	v_fma_f32 v33, v33, v129, v97
	v_fma_f32 v34, v34, v130, v98
	v_fma_f32 v35, v35, v131, v99
	v_cvt_pk_bf16_f32 v240, v32, v33
	v_cvt_pk_bf16_f32 v241, v34, v35
	global_store_dwordx2 v2, v[240:241], s[22:23] offset:3584
	s_add_i32 s11, s10, 0x1800
	s_lshr_b32 s0, s11, 8
	s_mul_i32 s0, s0, 57
	s_lshr_b32 s44, s0, 9
	s_mul_i32 s1, s44, 0x900
	s_sub_i32 s43, s11, s1
	s_lshl_b32 s1, s11, 12
	s_add_u32 s22, s50, s1
	s_addc_u32 s23, s51, 0
	s_cmpk_lt_u32 s43, 0x100
	s_cselect_b32 s0, 8, s44
	s_mul_i32 s1, s0, 0xc000
	s_add_u32 s28, s52, s1
	s_addc_u32 s29, s53, 0
	s_add_u32 s30, s28, 0x1000
	s_addc_u32 s31, s29, 0
	global_load_dwordx4 v[100:103], v1, s[56:57]
	global_load_dwordx4 v[104:107], v1, s[56:57] offset:1024
	global_load_dwordx4 v[108:111], v1, s[56:57] offset:2048
	global_load_dwordx4 v[112:115], v1, s[56:57] offset:3072
	global_load_dwordx4 v[116:119], v1, s[58:59]
	global_load_dwordx4 v[120:123], v1, s[58:59] offset:1024
	global_load_dwordx4 v[124:127], v1, s[58:59] offset:2048
	global_load_dwordx4 v[128:131], v1, s[58:59] offset:3072
	s_add_u32 s84, s28, 0x2000
	s_addc_u32 s85, s29, 0
	s_add_u32 s86, s28, 0x3000
	s_addc_u32 s87, s29, 0
	global_load_dwordx4 v[68:71], v1, s[28:29]
	global_load_dwordx4 v[132:135], v1, s[84:85]
	global_load_dwordx4 v[72:75], v1, s[28:29] offset:1024
	global_load_dwordx4 v[136:139], v1, s[84:85] offset:1024
	global_load_dwordx4 v[76:79], v1, s[28:29] offset:2048
	global_load_dwordx4 v[140:143], v1, s[84:85] offset:2048
	global_load_dwordx4 v[80:83], v1, s[28:29] offset:3072
	global_load_dwordx4 v[144:147], v1, s[84:85] offset:3072
	global_load_dwordx4 v[84:87], v1, s[30:31]
	global_load_dwordx4 v[148:151], v1, s[86:87]
	global_load_dwordx4 v[88:91], v1, s[30:31] offset:1024
	global_load_dwordx4 v[152:155], v1, s[86:87] offset:1024
	global_load_dwordx4 v[92:95], v1, s[30:31] offset:2048
	global_load_dwordx4 v[156:159], v1, s[86:87] offset:2048
	global_load_dwordx4 v[96:99], v1, s[30:31] offset:3072
	global_load_dwordx4 v[160:163], v1, s[86:87] offset:3072
	s_add_i32 s11, s10, 0x2000
	s_lshr_b32 s0, s11, 8
	s_mul_i32 s0, s0, 57
	s_lshr_b32 s44, s0, 9
	s_mul_i32 s1, s44, 0x900
	s_sub_i32 s43, s11, s1
	s_lshl_b32 s0, s44, 21
	s_lshl_b32 s1, s43, 13
	s_add_i32 s0, s0, s1
	s_lshl_b32 s2, s44, 24
	s_add_i32 s3, s43, 0xffffff00
	s_lshl_b32 s3, s3, 13
	s_add_i32 s2, s2, s3
	s_cmpk_lt_u32 s43, 0x100
	s_cselect_b32 s0, s0, s2
	s_cselect_b32 s1, s70, s68
	s_cselect_b32 s2, s71, s69
	s_add_u32 s12, s1, s0
	s_addc_u32 s13, s2, 0
	s_add_u32 s14, s12, 0x1000
	s_addc_u32 s15, s13, 0
	global_load_dwordx4 v[4:7], v1, s[12:13]
	global_load_dwordx4 v[8:11], v1, s[12:13] offset:1024
	global_load_dwordx4 v[12:15], v1, s[12:13] offset:2048
	global_load_dwordx4 v[16:19], v1, s[12:13] offset:3072
	global_load_dwordx4 v[20:23], v1, s[14:15]
	global_load_dwordx4 v[24:27], v1, s[14:15] offset:1024
	global_load_dwordx4 v[28:31], v1, s[14:15] offset:2048
	global_load_dwordx4 v[32:35], v1, s[14:15] offset:3072
	s_waitcnt vmcnt(8)
	v_mul_f32_e32 v236, v36, v36
	v_fmac_f32_e32 v236, v37, v37
	v_fmac_f32_e32 v236, v38, v38
	v_fmac_f32_e32 v236, v39, v39
	v_fmac_f32_e32 v236, v40, v40
	v_fmac_f32_e32 v236, v41, v41
	v_fmac_f32_e32 v236, v42, v42
	v_fmac_f32_e32 v236, v43, v43
	v_fmac_f32_e32 v236, v44, v44
	v_fmac_f32_e32 v236, v45, v45
	v_fmac_f32_e32 v236, v46, v46
	v_fmac_f32_e32 v236, v47, v47
	v_fmac_f32_e32 v236, v48, v48
	v_fmac_f32_e32 v236, v49, v49
	v_fmac_f32_e32 v236, v50, v50
	v_fmac_f32_e32 v236, v51, v51
	v_fmac_f32_e32 v236, v52, v52
	v_fmac_f32_e32 v236, v53, v53
	v_fmac_f32_e32 v236, v54, v54
	v_fmac_f32_e32 v236, v55, v55
	v_fmac_f32_e32 v236, v56, v56
	v_fmac_f32_e32 v236, v57, v57
	v_fmac_f32_e32 v236, v58, v58
	v_fmac_f32_e32 v236, v59, v59
	v_fmac_f32_e32 v236, v60, v60
	v_fmac_f32_e32 v236, v61, v61
	v_fmac_f32_e32 v236, v62, v62
	v_fmac_f32_e32 v236, v63, v63
	v_fmac_f32_e32 v236, v64, v64
	v_fmac_f32_e32 v236, v65, v65
	v_fmac_f32_e32 v236, v66, v66
	v_fmac_f32_e32 v236, v67, v67
	v_fma_f32 v100, v100, v132, v100
	v_fma_f32 v101, v101, v133, v101
	v_fma_f32 v102, v102, v134, v102
	v_fma_f32 v103, v103, v135, v103
	v_fma_f32 v104, v104, v136, v104
	v_fma_f32 v105, v105, v137, v105
	v_fma_f32 v106, v106, v138, v106
	v_fma_f32 v107, v107, v139, v107
	v_fma_f32 v108, v108, v140, v108
	v_fma_f32 v109, v109, v141, v109
	v_fma_f32 v110, v110, v142, v110
	v_fma_f32 v111, v111, v143, v111
	v_fma_f32 v112, v112, v144, v112
	v_fma_f32 v113, v113, v145, v113
	v_fma_f32 v114, v114, v146, v114
	v_fma_f32 v115, v115, v147, v115
	v_fma_f32 v116, v116, v148, v116
	v_fma_f32 v117, v117, v149, v117
	v_fma_f32 v118, v118, v150, v118
	v_fma_f32 v119, v119, v151, v119
	v_fma_f32 v120, v120, v152, v120
	v_fma_f32 v121, v121, v153, v121
	v_fma_f32 v122, v122, v154, v122
	v_fma_f32 v123, v123, v155, v123
	v_fma_f32 v124, v124, v156, v124
	v_fma_f32 v125, v125, v157, v125
	v_fma_f32 v126, v126, v158, v126
	v_fma_f32 v127, v127, v159, v127
	v_fma_f32 v128, v128, v160, v128
	v_fma_f32 v129, v129, v161, v129
	v_fma_f32 v130, v130, v162, v130
	v_fma_f32 v131, v131, v163, v131
	s_nop 1
	v_add_f32_dpp v236, v236, v236 quad_perm:[1,0,3,2] row_mask:0xf bank_mask:0xf
	s_nop 1
	v_add_f32_dpp v236, v236, v236 quad_perm:[2,3,0,1] row_mask:0xf bank_mask:0xf
	s_nop 1
	v_add_f32_dpp v236, v236, v236 row_half_mirror row_mask:0xf bank_mask:0xf
	s_nop 1
	v_add_f32_dpp v236, v236, v236 row_mirror row_mask:0xf bank_mask:0xf
	s_nop 1
	v_readlane_b32 s0, v236, 0
	v_readlane_b32 s1, v236, 16
	v_readlane_b32 s2, v236, 32
	v_readlane_b32 s3, v236, 48
	s_nop 3
	v_mov_b32_e32 v237, s0
	v_add_f32_e32 v237, s1, v237
	v_add_f32_e32 v237, s2, v237
	v_add_f32_e32 v237, s3, v237
	v_mul_f32_e32 v237, 0x3a000000, v237
	v_add_f32_e32 v237, 0x358637bd, v237
	v_rsq_f32_e32 v237, v237
	s_nop 0
	v_mul_f32_e32 v100, v100, v237
	v_mul_f32_e32 v101, v101, v237
	v_mul_f32_e32 v102, v102, v237
	v_mul_f32_e32 v103, v103, v237
	v_mul_f32_e32 v104, v104, v237
	v_mul_f32_e32 v105, v105, v237
	v_mul_f32_e32 v106, v106, v237
	v_mul_f32_e32 v107, v107, v237
	v_mul_f32_e32 v108, v108, v237
	v_mul_f32_e32 v109, v109, v237
	v_mul_f32_e32 v110, v110, v237
	v_mul_f32_e32 v111, v111, v237
	v_mul_f32_e32 v112, v112, v237
	v_mul_f32_e32 v113, v113, v237
	v_mul_f32_e32 v114, v114, v237
	v_mul_f32_e32 v115, v115, v237
	v_mul_f32_e32 v116, v116, v237
	v_mul_f32_e32 v117, v117, v237
	v_mul_f32_e32 v118, v118, v237
	v_mul_f32_e32 v119, v119, v237
	v_mul_f32_e32 v120, v120, v237
	v_mul_f32_e32 v121, v121, v237
	v_mul_f32_e32 v122, v122, v237
	v_mul_f32_e32 v123, v123, v237
	v_mul_f32_e32 v124, v124, v237
	v_mul_f32_e32 v125, v125, v237
	v_mul_f32_e32 v126, v126, v237
	v_mul_f32_e32 v127, v127, v237
	v_mul_f32_e32 v128, v128, v237
	v_mul_f32_e32 v129, v129, v237
	v_mul_f32_e32 v130, v130, v237
	v_mul_f32_e32 v131, v131, v237
	v_fma_f32 v36, v36, v100, v68
	v_fma_f32 v37, v37, v101, v69
	v_fma_f32 v38, v38, v102, v70
	v_fma_f32 v39, v39, v103, v71
	v_cvt_pk_bf16_f32 v238, v36, v37
	v_cvt_pk_bf16_f32 v239, v38, v39
	global_store_dwordx2 v2, v[238:239], s[22:23]
	v_fma_f32 v40, v40, v104, v72
	v_fma_f32 v41, v41, v105, v73
	v_fma_f32 v42, v42, v106, v74
	v_fma_f32 v43, v43, v107, v75
	v_cvt_pk_bf16_f32 v240, v40, v41
	v_cvt_pk_bf16_f32 v241, v42, v43
	global_store_dwordx2 v2, v[240:241], s[22:23] offset:512
	v_fma_f32 v44, v44, v108, v76
	v_fma_f32 v45, v45, v109, v77
	v_fma_f32 v46, v46, v110, v78
	v_fma_f32 v47, v47, v111, v79
	v_cvt_pk_bf16_f32 v238, v44, v45
	v_cvt_pk_bf16_f32 v239, v46, v47
	global_store_dwordx2 v2, v[238:239], s[22:23] offset:1024
	v_fma_f32 v48, v48, v112, v80
	v_fma_f32 v49, v49, v113, v81
	v_fma_f32 v50, v50, v114, v82
	v_fma_f32 v51, v51, v115, v83
	v_cvt_pk_bf16_f32 v240, v48, v49
	v_cvt_pk_bf16_f32 v241, v50, v51
	global_store_dwordx2 v2, v[240:241], s[22:23] offset:1536
	v_fma_f32 v52, v52, v116, v84
	v_fma_f32 v53, v53, v117, v85
	v_fma_f32 v54, v54, v118, v86
	v_fma_f32 v55, v55, v119, v87
	v_cvt_pk_bf16_f32 v238, v52, v53
	v_cvt_pk_bf16_f32 v239, v54, v55
	global_store_dwordx2 v2, v[238:239], s[22:23] offset:2048
	v_fma_f32 v56, v56, v120, v88
	v_fma_f32 v57, v57, v121, v89
	v_fma_f32 v58, v58, v122, v90
	v_fma_f32 v59, v59, v123, v91
	v_cvt_pk_bf16_f32 v240, v56, v57
	v_cvt_pk_bf16_f32 v241, v58, v59
	global_store_dwordx2 v2, v[240:241], s[22:23] offset:2560
	v_fma_f32 v60, v60, v124, v92
	v_fma_f32 v61, v61, v125, v93
	v_fma_f32 v62, v62, v126, v94
	v_fma_f32 v63, v63, v127, v95
	v_cvt_pk_bf16_f32 v238, v60, v61
	v_cvt_pk_bf16_f32 v239, v62, v63
	global_store_dwordx2 v2, v[238:239], s[22:23] offset:3072
	v_fma_f32 v64, v64, v128, v96
	v_fma_f32 v65, v65, v129, v97
	v_fma_f32 v66, v66, v130, v98
	v_fma_f32 v67, v67, v131, v99
	v_cvt_pk_bf16_f32 v240, v64, v65
	v_cvt_pk_bf16_f32 v241, v66, v67
	global_store_dwordx2 v2, v[240:241], s[22:23] offset:3584
	s_add_i32 s11, s10, 0x2000
	s_lshr_b32 s0, s11, 8
	s_mul_i32 s0, s0, 57
	s_lshr_b32 s44, s0, 9
	s_mul_i32 s1, s44, 0x900
	s_sub_i32 s43, s11, s1
	s_lshl_b32 s1, s11, 12
	s_add_u32 s22, s50, s1
	s_addc_u32 s23, s51, 0
	s_cmpk_lt_u32 s43, 0x100
	s_cselect_b32 s0, 8, s44
	s_mul_i32 s1, s0, 0xc000
	s_add_u32 s28, s52, s1
	s_addc_u32 s29, s53, 0
	s_add_u32 s30, s28, 0x1000
	s_addc_u32 s31, s29, 0
	global_load_dwordx4 v[100:103], v1, s[56:57]
	global_load_dwordx4 v[104:107], v1, s[56:57] offset:1024
	global_load_dwordx4 v[108:111], v1, s[56:57] offset:2048
	global_load_dwordx4 v[112:115], v1, s[56:57] offset:3072
	global_load_dwordx4 v[116:119], v1, s[58:59]
	global_load_dwordx4 v[120:123], v1, s[58:59] offset:1024
	global_load_dwordx4 v[124:127], v1, s[58:59] offset:2048
	global_load_dwordx4 v[128:131], v1, s[58:59] offset:3072
	s_add_u32 s84, s28, 0x2000
	s_addc_u32 s85, s29, 0
	s_add_u32 s86, s28, 0x3000
	s_addc_u32 s87, s29, 0
	global_load_dwordx4 v[68:71], v1, s[28:29]
	global_load_dwordx4 v[132:135], v1, s[84:85]
	global_load_dwordx4 v[72:75], v1, s[28:29] offset:1024
	global_load_dwordx4 v[136:139], v1, s[84:85] offset:1024
	global_load_dwordx4 v[76:79], v1, s[28:29] offset:2048
	global_load_dwordx4 v[140:143], v1, s[84:85] offset:2048
	global_load_dwordx4 v[80:83], v1, s[28:29] offset:3072
	global_load_dwordx4 v[144:147], v1, s[84:85] offset:3072
	global_load_dwordx4 v[84:87], v1, s[30:31]
	global_load_dwordx4 v[148:151], v1, s[86:87]
	global_load_dwordx4 v[88:91], v1, s[30:31] offset:1024
	global_load_dwordx4 v[152:155], v1, s[86:87] offset:1024
	global_load_dwordx4 v[92:95], v1, s[30:31] offset:2048
	global_load_dwordx4 v[156:159], v1, s[86:87] offset:2048
	global_load_dwordx4 v[96:99], v1, s[30:31] offset:3072
	global_load_dwordx4 v[160:163], v1, s[86:87] offset:3072
	s_add_i32 s11, s10, 0x2800
	s_lshr_b32 s0, s11, 8
	s_mul_i32 s0, s0, 57
	s_lshr_b32 s44, s0, 9
	s_mul_i32 s1, s44, 0x900
	s_sub_i32 s43, s11, s1
	s_lshl_b32 s0, s44, 21
	s_lshl_b32 s1, s43, 13
	s_add_i32 s0, s0, s1
	s_lshl_b32 s2, s44, 24
	s_add_i32 s3, s43, 0xffffff00
	s_lshl_b32 s3, s3, 13
	s_add_i32 s2, s2, s3
	s_cmpk_lt_u32 s43, 0x100
	s_cselect_b32 s0, s0, s2
	s_cselect_b32 s1, s70, s68
	s_cselect_b32 s2, s71, s69
	s_add_u32 s12, s1, s0
	s_addc_u32 s13, s2, 0
	s_add_u32 s14, s12, 0x1000
	s_addc_u32 s15, s13, 0
	global_load_dwordx4 v[36:39], v1, s[12:13]
	global_load_dwordx4 v[40:43], v1, s[12:13] offset:1024
	global_load_dwordx4 v[44:47], v1, s[12:13] offset:2048
	global_load_dwordx4 v[48:51], v1, s[12:13] offset:3072
	global_load_dwordx4 v[52:55], v1, s[14:15]
	global_load_dwordx4 v[56:59], v1, s[14:15] offset:1024
	global_load_dwordx4 v[60:63], v1, s[14:15] offset:2048
	global_load_dwordx4 v[64:67], v1, s[14:15] offset:3072
	s_waitcnt vmcnt(8)
	v_mul_f32_e32 v236, v4, v4
	v_fmac_f32_e32 v236, v5, v5
	v_fmac_f32_e32 v236, v6, v6
	v_fmac_f32_e32 v236, v7, v7
	v_fmac_f32_e32 v236, v8, v8
	v_fmac_f32_e32 v236, v9, v9
	v_fmac_f32_e32 v236, v10, v10
	v_fmac_f32_e32 v236, v11, v11
	v_fmac_f32_e32 v236, v12, v12
	v_fmac_f32_e32 v236, v13, v13
	v_fmac_f32_e32 v236, v14, v14
	v_fmac_f32_e32 v236, v15, v15
	v_fmac_f32_e32 v236, v16, v16
	v_fmac_f32_e32 v236, v17, v17
	v_fmac_f32_e32 v236, v18, v18
	v_fmac_f32_e32 v236, v19, v19
	v_fmac_f32_e32 v236, v20, v20
	v_fmac_f32_e32 v236, v21, v21
	v_fmac_f32_e32 v236, v22, v22
	v_fmac_f32_e32 v236, v23, v23
	v_fmac_f32_e32 v236, v24, v24
	v_fmac_f32_e32 v236, v25, v25
	v_fmac_f32_e32 v236, v26, v26
	v_fmac_f32_e32 v236, v27, v27
	v_fmac_f32_e32 v236, v28, v28
	v_fmac_f32_e32 v236, v29, v29
	v_fmac_f32_e32 v236, v30, v30
	v_fmac_f32_e32 v236, v31, v31
	v_fmac_f32_e32 v236, v32, v32
	v_fmac_f32_e32 v236, v33, v33
	v_fmac_f32_e32 v236, v34, v34
	v_fmac_f32_e32 v236, v35, v35
	v_fma_f32 v100, v100, v132, v100
	v_fma_f32 v101, v101, v133, v101
	v_fma_f32 v102, v102, v134, v102
	v_fma_f32 v103, v103, v135, v103
	v_fma_f32 v104, v104, v136, v104
	v_fma_f32 v105, v105, v137, v105
	v_fma_f32 v106, v106, v138, v106
	v_fma_f32 v107, v107, v139, v107
	v_fma_f32 v108, v108, v140, v108
	v_fma_f32 v109, v109, v141, v109
	v_fma_f32 v110, v110, v142, v110
	v_fma_f32 v111, v111, v143, v111
	v_fma_f32 v112, v112, v144, v112
	v_fma_f32 v113, v113, v145, v113
	v_fma_f32 v114, v114, v146, v114
	v_fma_f32 v115, v115, v147, v115
	v_fma_f32 v116, v116, v148, v116
	v_fma_f32 v117, v117, v149, v117
	v_fma_f32 v118, v118, v150, v118
	v_fma_f32 v119, v119, v151, v119
	v_fma_f32 v120, v120, v152, v120
	v_fma_f32 v121, v121, v153, v121
	v_fma_f32 v122, v122, v154, v122
	v_fma_f32 v123, v123, v155, v123
	v_fma_f32 v124, v124, v156, v124
	v_fma_f32 v125, v125, v157, v125
	v_fma_f32 v126, v126, v158, v126
	v_fma_f32 v127, v127, v159, v127
	v_fma_f32 v128, v128, v160, v128
	v_fma_f32 v129, v129, v161, v129
	v_fma_f32 v130, v130, v162, v130
	v_fma_f32 v131, v131, v163, v131
	s_nop 1
	v_add_f32_dpp v236, v236, v236 quad_perm:[1,0,3,2] row_mask:0xf bank_mask:0xf
	s_nop 1
	v_add_f32_dpp v236, v236, v236 quad_perm:[2,3,0,1] row_mask:0xf bank_mask:0xf
	s_nop 1
	v_add_f32_dpp v236, v236, v236 row_half_mirror row_mask:0xf bank_mask:0xf
	s_nop 1
	v_add_f32_dpp v236, v236, v236 row_mirror row_mask:0xf bank_mask:0xf
	s_nop 1
	v_readlane_b32 s0, v236, 0
	v_readlane_b32 s1, v236, 16
	v_readlane_b32 s2, v236, 32
	v_readlane_b32 s3, v236, 48
	s_nop 3
	v_mov_b32_e32 v237, s0
	v_add_f32_e32 v237, s1, v237
	v_add_f32_e32 v237, s2, v237
	v_add_f32_e32 v237, s3, v237
	v_mul_f32_e32 v237, 0x3a000000, v237
	v_add_f32_e32 v237, 0x358637bd, v237
	v_rsq_f32_e32 v237, v237
	s_nop 0
	v_mul_f32_e32 v100, v100, v237
	v_mul_f32_e32 v101, v101, v237
	v_mul_f32_e32 v102, v102, v237
	v_mul_f32_e32 v103, v103, v237
	v_mul_f32_e32 v104, v104, v237
	v_mul_f32_e32 v105, v105, v237
	v_mul_f32_e32 v106, v106, v237
	v_mul_f32_e32 v107, v107, v237
	v_mul_f32_e32 v108, v108, v237
	v_mul_f32_e32 v109, v109, v237
	v_mul_f32_e32 v110, v110, v237
	v_mul_f32_e32 v111, v111, v237
	v_mul_f32_e32 v112, v112, v237
	v_mul_f32_e32 v113, v113, v237
	v_mul_f32_e32 v114, v114, v237
	v_mul_f32_e32 v115, v115, v237
	v_mul_f32_e32 v116, v116, v237
	v_mul_f32_e32 v117, v117, v237
	v_mul_f32_e32 v118, v118, v237
	v_mul_f32_e32 v119, v119, v237
	v_mul_f32_e32 v120, v120, v237
	v_mul_f32_e32 v121, v121, v237
	v_mul_f32_e32 v122, v122, v237
	v_mul_f32_e32 v123, v123, v237
	v_mul_f32_e32 v124, v124, v237
	v_mul_f32_e32 v125, v125, v237
	v_mul_f32_e32 v126, v126, v237
	v_mul_f32_e32 v127, v127, v237
	v_mul_f32_e32 v128, v128, v237
	v_mul_f32_e32 v129, v129, v237
	v_mul_f32_e32 v130, v130, v237
	v_mul_f32_e32 v131, v131, v237
	v_fma_f32 v4, v4, v100, v68
	v_fma_f32 v5, v5, v101, v69
	v_fma_f32 v6, v6, v102, v70
	v_fma_f32 v7, v7, v103, v71
	v_cvt_pk_bf16_f32 v238, v4, v5
	v_cvt_pk_bf16_f32 v239, v6, v7
	global_store_dwordx2 v2, v[238:239], s[22:23]
	v_fma_f32 v8, v8, v104, v72
	v_fma_f32 v9, v9, v105, v73
	v_fma_f32 v10, v10, v106, v74
	v_fma_f32 v11, v11, v107, v75
	v_cvt_pk_bf16_f32 v240, v8, v9
	v_cvt_pk_bf16_f32 v241, v10, v11
	global_store_dwordx2 v2, v[240:241], s[22:23] offset:512
	v_fma_f32 v12, v12, v108, v76
	v_fma_f32 v13, v13, v109, v77
	v_fma_f32 v14, v14, v110, v78
	v_fma_f32 v15, v15, v111, v79
	v_cvt_pk_bf16_f32 v238, v12, v13
	v_cvt_pk_bf16_f32 v239, v14, v15
	global_store_dwordx2 v2, v[238:239], s[22:23] offset:1024
	v_fma_f32 v16, v16, v112, v80
	v_fma_f32 v17, v17, v113, v81
	v_fma_f32 v18, v18, v114, v82
	v_fma_f32 v19, v19, v115, v83
	v_cvt_pk_bf16_f32 v240, v16, v17
	v_cvt_pk_bf16_f32 v241, v18, v19
	global_store_dwordx2 v2, v[240:241], s[22:23] offset:1536
	v_fma_f32 v20, v20, v116, v84
	v_fma_f32 v21, v21, v117, v85
	v_fma_f32 v22, v22, v118, v86
	v_fma_f32 v23, v23, v119, v87
	v_cvt_pk_bf16_f32 v238, v20, v21
	v_cvt_pk_bf16_f32 v239, v22, v23
	global_store_dwordx2 v2, v[238:239], s[22:23] offset:2048
	v_fma_f32 v24, v24, v120, v88
	v_fma_f32 v25, v25, v121, v89
	v_fma_f32 v26, v26, v122, v90
	v_fma_f32 v27, v27, v123, v91
	v_cvt_pk_bf16_f32 v240, v24, v25
	v_cvt_pk_bf16_f32 v241, v26, v27
	global_store_dwordx2 v2, v[240:241], s[22:23] offset:2560
	v_fma_f32 v28, v28, v124, v92
	v_fma_f32 v29, v29, v125, v93
	v_fma_f32 v30, v30, v126, v94
	v_fma_f32 v31, v31, v127, v95
	v_cvt_pk_bf16_f32 v238, v28, v29
	v_cvt_pk_bf16_f32 v239, v30, v31
	global_store_dwordx2 v2, v[238:239], s[22:23] offset:3072
	v_fma_f32 v32, v32, v128, v96
	v_fma_f32 v33, v33, v129, v97
	v_fma_f32 v34, v34, v130, v98
	v_fma_f32 v35, v35, v131, v99
	v_cvt_pk_bf16_f32 v240, v32, v33
	v_cvt_pk_bf16_f32 v241, v34, v35
	global_store_dwordx2 v2, v[240:241], s[22:23] offset:3584
	s_add_i32 s11, s10, 0x2800
	s_lshr_b32 s0, s11, 8
	s_mul_i32 s0, s0, 57
	s_lshr_b32 s44, s0, 9
	s_mul_i32 s1, s44, 0x900
	s_sub_i32 s43, s11, s1
	s_lshl_b32 s1, s11, 12
	s_add_u32 s22, s50, s1
	s_addc_u32 s23, s51, 0
	s_cmpk_lt_u32 s43, 0x100
	s_cselect_b32 s0, 8, s44
	s_mul_i32 s1, s0, 0xc000
	s_add_u32 s28, s52, s1
	s_addc_u32 s29, s53, 0
	s_add_u32 s30, s28, 0x1000
	s_addc_u32 s31, s29, 0
	global_load_dwordx4 v[100:103], v1, s[56:57]
	global_load_dwordx4 v[104:107], v1, s[56:57] offset:1024
	global_load_dwordx4 v[108:111], v1, s[56:57] offset:2048
	global_load_dwordx4 v[112:115], v1, s[56:57] offset:3072
	global_load_dwordx4 v[116:119], v1, s[58:59]
	global_load_dwordx4 v[120:123], v1, s[58:59] offset:1024
	global_load_dwordx4 v[124:127], v1, s[58:59] offset:2048
	global_load_dwordx4 v[128:131], v1, s[58:59] offset:3072
	s_add_u32 s84, s28, 0x2000
	s_addc_u32 s85, s29, 0
	s_add_u32 s86, s28, 0x3000
	s_addc_u32 s87, s29, 0
	global_load_dwordx4 v[68:71], v1, s[28:29]
	global_load_dwordx4 v[132:135], v1, s[84:85]
	global_load_dwordx4 v[72:75], v1, s[28:29] offset:1024
	global_load_dwordx4 v[136:139], v1, s[84:85] offset:1024
	global_load_dwordx4 v[76:79], v1, s[28:29] offset:2048
	global_load_dwordx4 v[140:143], v1, s[84:85] offset:2048
	global_load_dwordx4 v[80:83], v1, s[28:29] offset:3072
	global_load_dwordx4 v[144:147], v1, s[84:85] offset:3072
	global_load_dwordx4 v[84:87], v1, s[30:31]
	global_load_dwordx4 v[148:151], v1, s[86:87]
	global_load_dwordx4 v[88:91], v1, s[30:31] offset:1024
	global_load_dwordx4 v[152:155], v1, s[86:87] offset:1024
	global_load_dwordx4 v[92:95], v1, s[30:31] offset:2048
	global_load_dwordx4 v[156:159], v1, s[86:87] offset:2048
	global_load_dwordx4 v[96:99], v1, s[30:31] offset:3072
	global_load_dwordx4 v[160:163], v1, s[86:87] offset:3072
	s_add_i32 s11, s10, 0x3000
	s_lshr_b32 s0, s11, 8
	s_mul_i32 s0, s0, 57
	s_lshr_b32 s44, s0, 9
	s_mul_i32 s1, s44, 0x900
	s_sub_i32 s43, s11, s1
	s_lshl_b32 s0, s44, 21
	s_lshl_b32 s1, s43, 13
	s_add_i32 s0, s0, s1
	s_lshl_b32 s2, s44, 24
	s_add_i32 s3, s43, 0xffffff00
	s_lshl_b32 s3, s3, 13
	s_add_i32 s2, s2, s3
	s_cmpk_lt_u32 s43, 0x100
	s_cselect_b32 s0, s0, s2
	s_cselect_b32 s1, s70, s68
	s_cselect_b32 s2, s71, s69
	s_add_u32 s12, s1, s0
	s_addc_u32 s13, s2, 0
	s_add_u32 s14, s12, 0x1000
	s_addc_u32 s15, s13, 0
	global_load_dwordx4 v[4:7], v1, s[12:13]
	global_load_dwordx4 v[8:11], v1, s[12:13] offset:1024
	global_load_dwordx4 v[12:15], v1, s[12:13] offset:2048
	global_load_dwordx4 v[16:19], v1, s[12:13] offset:3072
	global_load_dwordx4 v[20:23], v1, s[14:15]
	global_load_dwordx4 v[24:27], v1, s[14:15] offset:1024
	global_load_dwordx4 v[28:31], v1, s[14:15] offset:2048
	global_load_dwordx4 v[32:35], v1, s[14:15] offset:3072
	s_waitcnt vmcnt(8)
	v_mul_f32_e32 v236, v36, v36
	v_fmac_f32_e32 v236, v37, v37
	v_fmac_f32_e32 v236, v38, v38
	v_fmac_f32_e32 v236, v39, v39
	v_fmac_f32_e32 v236, v40, v40
	v_fmac_f32_e32 v236, v41, v41
	v_fmac_f32_e32 v236, v42, v42
	v_fmac_f32_e32 v236, v43, v43
	v_fmac_f32_e32 v236, v44, v44
	v_fmac_f32_e32 v236, v45, v45
	v_fmac_f32_e32 v236, v46, v46
	v_fmac_f32_e32 v236, v47, v47
	v_fmac_f32_e32 v236, v48, v48
	v_fmac_f32_e32 v236, v49, v49
	v_fmac_f32_e32 v236, v50, v50
	v_fmac_f32_e32 v236, v51, v51
	v_fmac_f32_e32 v236, v52, v52
	v_fmac_f32_e32 v236, v53, v53
	v_fmac_f32_e32 v236, v54, v54
	v_fmac_f32_e32 v236, v55, v55
	v_fmac_f32_e32 v236, v56, v56
	v_fmac_f32_e32 v236, v57, v57
	v_fmac_f32_e32 v236, v58, v58
	v_fmac_f32_e32 v236, v59, v59
	v_fmac_f32_e32 v236, v60, v60
	v_fmac_f32_e32 v236, v61, v61
	v_fmac_f32_e32 v236, v62, v62
	v_fmac_f32_e32 v236, v63, v63
	v_fmac_f32_e32 v236, v64, v64
	v_fmac_f32_e32 v236, v65, v65
	v_fmac_f32_e32 v236, v66, v66
	v_fmac_f32_e32 v236, v67, v67
	v_fma_f32 v100, v100, v132, v100
	v_fma_f32 v101, v101, v133, v101
	v_fma_f32 v102, v102, v134, v102
	v_fma_f32 v103, v103, v135, v103
	v_fma_f32 v104, v104, v136, v104
	v_fma_f32 v105, v105, v137, v105
	v_fma_f32 v106, v106, v138, v106
	v_fma_f32 v107, v107, v139, v107
	v_fma_f32 v108, v108, v140, v108
	v_fma_f32 v109, v109, v141, v109
	v_fma_f32 v110, v110, v142, v110
	v_fma_f32 v111, v111, v143, v111
	v_fma_f32 v112, v112, v144, v112
	v_fma_f32 v113, v113, v145, v113
	v_fma_f32 v114, v114, v146, v114
	v_fma_f32 v115, v115, v147, v115
	v_fma_f32 v116, v116, v148, v116
	v_fma_f32 v117, v117, v149, v117
	v_fma_f32 v118, v118, v150, v118
	v_fma_f32 v119, v119, v151, v119
	v_fma_f32 v120, v120, v152, v120
	v_fma_f32 v121, v121, v153, v121
	v_fma_f32 v122, v122, v154, v122
	v_fma_f32 v123, v123, v155, v123
	v_fma_f32 v124, v124, v156, v124
	v_fma_f32 v125, v125, v157, v125
	v_fma_f32 v126, v126, v158, v126
	v_fma_f32 v127, v127, v159, v127
	v_fma_f32 v128, v128, v160, v128
	v_fma_f32 v129, v129, v161, v129
	v_fma_f32 v130, v130, v162, v130
	v_fma_f32 v131, v131, v163, v131
	s_nop 1
	v_add_f32_dpp v236, v236, v236 quad_perm:[1,0,3,2] row_mask:0xf bank_mask:0xf
	s_nop 1
	v_add_f32_dpp v236, v236, v236 quad_perm:[2,3,0,1] row_mask:0xf bank_mask:0xf
	s_nop 1
	v_add_f32_dpp v236, v236, v236 row_half_mirror row_mask:0xf bank_mask:0xf
	s_nop 1
	v_add_f32_dpp v236, v236, v236 row_mirror row_mask:0xf bank_mask:0xf
	s_nop 1
	v_readlane_b32 s0, v236, 0
	v_readlane_b32 s1, v236, 16
	v_readlane_b32 s2, v236, 32
	v_readlane_b32 s3, v236, 48
	s_nop 3
	v_mov_b32_e32 v237, s0
	v_add_f32_e32 v237, s1, v237
	v_add_f32_e32 v237, s2, v237
	v_add_f32_e32 v237, s3, v237
	v_mul_f32_e32 v237, 0x3a000000, v237
	v_add_f32_e32 v237, 0x358637bd, v237
	v_rsq_f32_e32 v237, v237
	s_nop 0
	v_mul_f32_e32 v100, v100, v237
	v_mul_f32_e32 v101, v101, v237
	v_mul_f32_e32 v102, v102, v237
	v_mul_f32_e32 v103, v103, v237
	v_mul_f32_e32 v104, v104, v237
	v_mul_f32_e32 v105, v105, v237
	v_mul_f32_e32 v106, v106, v237
	v_mul_f32_e32 v107, v107, v237
	v_mul_f32_e32 v108, v108, v237
	v_mul_f32_e32 v109, v109, v237
	v_mul_f32_e32 v110, v110, v237
	v_mul_f32_e32 v111, v111, v237
	v_mul_f32_e32 v112, v112, v237
	v_mul_f32_e32 v113, v113, v237
	v_mul_f32_e32 v114, v114, v237
	v_mul_f32_e32 v115, v115, v237
	v_mul_f32_e32 v116, v116, v237
	v_mul_f32_e32 v117, v117, v237
	v_mul_f32_e32 v118, v118, v237
	v_mul_f32_e32 v119, v119, v237
	v_mul_f32_e32 v120, v120, v237
	v_mul_f32_e32 v121, v121, v237
	v_mul_f32_e32 v122, v122, v237
	v_mul_f32_e32 v123, v123, v237
	v_mul_f32_e32 v124, v124, v237
	v_mul_f32_e32 v125, v125, v237
	v_mul_f32_e32 v126, v126, v237
	v_mul_f32_e32 v127, v127, v237
	v_mul_f32_e32 v128, v128, v237
	v_mul_f32_e32 v129, v129, v237
	v_mul_f32_e32 v130, v130, v237
	v_mul_f32_e32 v131, v131, v237
	v_fma_f32 v36, v36, v100, v68
	v_fma_f32 v37, v37, v101, v69
	v_fma_f32 v38, v38, v102, v70
	v_fma_f32 v39, v39, v103, v71
	v_cvt_pk_bf16_f32 v238, v36, v37
	v_cvt_pk_bf16_f32 v239, v38, v39
	global_store_dwordx2 v2, v[238:239], s[22:23]
	v_fma_f32 v40, v40, v104, v72
	v_fma_f32 v41, v41, v105, v73
	v_fma_f32 v42, v42, v106, v74
	v_fma_f32 v43, v43, v107, v75
	v_cvt_pk_bf16_f32 v240, v40, v41
	v_cvt_pk_bf16_f32 v241, v42, v43
	global_store_dwordx2 v2, v[240:241], s[22:23] offset:512
	v_fma_f32 v44, v44, v108, v76
	v_fma_f32 v45, v45, v109, v77
	v_fma_f32 v46, v46, v110, v78
	v_fma_f32 v47, v47, v111, v79
	v_cvt_pk_bf16_f32 v238, v44, v45
	v_cvt_pk_bf16_f32 v239, v46, v47
	global_store_dwordx2 v2, v[238:239], s[22:23] offset:1024
	v_fma_f32 v48, v48, v112, v80
	v_fma_f32 v49, v49, v113, v81
	v_fma_f32 v50, v50, v114, v82
	v_fma_f32 v51, v51, v115, v83
	v_cvt_pk_bf16_f32 v240, v48, v49
	v_cvt_pk_bf16_f32 v241, v50, v51
	global_store_dwordx2 v2, v[240:241], s[22:23] offset:1536
	v_fma_f32 v52, v52, v116, v84
	v_fma_f32 v53, v53, v117, v85
	v_fma_f32 v54, v54, v118, v86
	v_fma_f32 v55, v55, v119, v87
	v_cvt_pk_bf16_f32 v238, v52, v53
	v_cvt_pk_bf16_f32 v239, v54, v55
	global_store_dwordx2 v2, v[238:239], s[22:23] offset:2048
	v_fma_f32 v56, v56, v120, v88
	v_fma_f32 v57, v57, v121, v89
	v_fma_f32 v58, v58, v122, v90
	v_fma_f32 v59, v59, v123, v91
	v_cvt_pk_bf16_f32 v240, v56, v57
	v_cvt_pk_bf16_f32 v241, v58, v59
	global_store_dwordx2 v2, v[240:241], s[22:23] offset:2560
	v_fma_f32 v60, v60, v124, v92
	v_fma_f32 v61, v61, v125, v93
	v_fma_f32 v62, v62, v126, v94
	v_fma_f32 v63, v63, v127, v95
	v_cvt_pk_bf16_f32 v238, v60, v61
	v_cvt_pk_bf16_f32 v239, v62, v63
	global_store_dwordx2 v2, v[238:239], s[22:23] offset:3072
	v_fma_f32 v64, v64, v128, v96
	v_fma_f32 v65, v65, v129, v97
	v_fma_f32 v66, v66, v130, v98
	v_fma_f32 v67, v67, v131, v99
	v_cvt_pk_bf16_f32 v240, v64, v65
	v_cvt_pk_bf16_f32 v241, v66, v67
	global_store_dwordx2 v2, v[240:241], s[22:23] offset:3584
	s_add_i32 s11, s10, 0x3000
	s_lshr_b32 s0, s11, 8
	s_mul_i32 s0, s0, 57
	s_lshr_b32 s44, s0, 9
	s_mul_i32 s1, s44, 0x900
	s_sub_i32 s43, s11, s1
	s_lshl_b32 s1, s11, 12
	s_add_u32 s22, s50, s1
	s_addc_u32 s23, s51, 0
	s_cmpk_lt_u32 s43, 0x100
	s_cselect_b32 s0, 8, s44
	s_mul_i32 s1, s0, 0xc000
	s_add_u32 s28, s52, s1
	s_addc_u32 s29, s53, 0
	s_add_u32 s30, s28, 0x1000
	s_addc_u32 s31, s29, 0
	global_load_dwordx4 v[100:103], v1, s[56:57]
	global_load_dwordx4 v[104:107], v1, s[56:57] offset:1024
	global_load_dwordx4 v[108:111], v1, s[56:57] offset:2048
	global_load_dwordx4 v[112:115], v1, s[56:57] offset:3072
	global_load_dwordx4 v[116:119], v1, s[58:59]
	global_load_dwordx4 v[120:123], v1, s[58:59] offset:1024
	global_load_dwordx4 v[124:127], v1, s[58:59] offset:2048
	global_load_dwordx4 v[128:131], v1, s[58:59] offset:3072
	s_add_u32 s84, s28, 0x2000
	s_addc_u32 s85, s29, 0
	s_add_u32 s86, s28, 0x3000
	s_addc_u32 s87, s29, 0
	global_load_dwordx4 v[68:71], v1, s[28:29]
	global_load_dwordx4 v[132:135], v1, s[84:85]
	global_load_dwordx4 v[72:75], v1, s[28:29] offset:1024
	global_load_dwordx4 v[136:139], v1, s[84:85] offset:1024
	global_load_dwordx4 v[76:79], v1, s[28:29] offset:2048
	global_load_dwordx4 v[140:143], v1, s[84:85] offset:2048
	global_load_dwordx4 v[80:83], v1, s[28:29] offset:3072
	global_load_dwordx4 v[144:147], v1, s[84:85] offset:3072
	global_load_dwordx4 v[84:87], v1, s[30:31]
	global_load_dwordx4 v[148:151], v1, s[86:87]
	global_load_dwordx4 v[88:91], v1, s[30:31] offset:1024
	global_load_dwordx4 v[152:155], v1, s[86:87] offset:1024
	global_load_dwordx4 v[92:95], v1, s[30:31] offset:2048
	global_load_dwordx4 v[156:159], v1, s[86:87] offset:2048
	global_load_dwordx4 v[96:99], v1, s[30:31] offset:3072
	global_load_dwordx4 v[160:163], v1, s[86:87] offset:3072
	s_add_i32 s11, s10, 0x3800
	s_lshr_b32 s0, s11, 8
	s_mul_i32 s0, s0, 57
	s_lshr_b32 s44, s0, 9
	s_mul_i32 s1, s44, 0x900
	s_sub_i32 s43, s11, s1
	s_lshl_b32 s0, s44, 21
	s_lshl_b32 s1, s43, 13
	s_add_i32 s0, s0, s1
	s_lshl_b32 s2, s44, 24
	s_add_i32 s3, s43, 0xffffff00
	s_lshl_b32 s3, s3, 13
	s_add_i32 s2, s2, s3
	s_cmpk_lt_u32 s43, 0x100
	s_cselect_b32 s0, s0, s2
	s_cselect_b32 s1, s70, s68
	s_cselect_b32 s2, s71, s69
	s_add_u32 s12, s1, s0
	s_addc_u32 s13, s2, 0
	s_add_u32 s14, s12, 0x1000
	s_addc_u32 s15, s13, 0
	global_load_dwordx4 v[36:39], v1, s[12:13]
	global_load_dwordx4 v[40:43], v1, s[12:13] offset:1024
	global_load_dwordx4 v[44:47], v1, s[12:13] offset:2048
	global_load_dwordx4 v[48:51], v1, s[12:13] offset:3072
	global_load_dwordx4 v[52:55], v1, s[14:15]
	global_load_dwordx4 v[56:59], v1, s[14:15] offset:1024
	global_load_dwordx4 v[60:63], v1, s[14:15] offset:2048
	global_load_dwordx4 v[64:67], v1, s[14:15] offset:3072
	s_waitcnt vmcnt(8)
	v_mul_f32_e32 v236, v4, v4
	v_fmac_f32_e32 v236, v5, v5
	v_fmac_f32_e32 v236, v6, v6
	v_fmac_f32_e32 v236, v7, v7
	v_fmac_f32_e32 v236, v8, v8
	v_fmac_f32_e32 v236, v9, v9
	v_fmac_f32_e32 v236, v10, v10
	v_fmac_f32_e32 v236, v11, v11
	v_fmac_f32_e32 v236, v12, v12
	v_fmac_f32_e32 v236, v13, v13
	v_fmac_f32_e32 v236, v14, v14
	v_fmac_f32_e32 v236, v15, v15
	v_fmac_f32_e32 v236, v16, v16
	v_fmac_f32_e32 v236, v17, v17
	v_fmac_f32_e32 v236, v18, v18
	v_fmac_f32_e32 v236, v19, v19
	v_fmac_f32_e32 v236, v20, v20
	v_fmac_f32_e32 v236, v21, v21
	v_fmac_f32_e32 v236, v22, v22
	v_fmac_f32_e32 v236, v23, v23
	v_fmac_f32_e32 v236, v24, v24
	v_fmac_f32_e32 v236, v25, v25
	v_fmac_f32_e32 v236, v26, v26
	v_fmac_f32_e32 v236, v27, v27
	v_fmac_f32_e32 v236, v28, v28
	v_fmac_f32_e32 v236, v29, v29
	v_fmac_f32_e32 v236, v30, v30
	v_fmac_f32_e32 v236, v31, v31
	v_fmac_f32_e32 v236, v32, v32
	v_fmac_f32_e32 v236, v33, v33
	v_fmac_f32_e32 v236, v34, v34
	v_fmac_f32_e32 v236, v35, v35
	v_fma_f32 v100, v100, v132, v100
	v_fma_f32 v101, v101, v133, v101
	v_fma_f32 v102, v102, v134, v102
	v_fma_f32 v103, v103, v135, v103
	v_fma_f32 v104, v104, v136, v104
	v_fma_f32 v105, v105, v137, v105
	v_fma_f32 v106, v106, v138, v106
	v_fma_f32 v107, v107, v139, v107
	v_fma_f32 v108, v108, v140, v108
	v_fma_f32 v109, v109, v141, v109
	v_fma_f32 v110, v110, v142, v110
	v_fma_f32 v111, v111, v143, v111
	v_fma_f32 v112, v112, v144, v112
	v_fma_f32 v113, v113, v145, v113
	v_fma_f32 v114, v114, v146, v114
	v_fma_f32 v115, v115, v147, v115
	v_fma_f32 v116, v116, v148, v116
	v_fma_f32 v117, v117, v149, v117
	v_fma_f32 v118, v118, v150, v118
	v_fma_f32 v119, v119, v151, v119
	v_fma_f32 v120, v120, v152, v120
	v_fma_f32 v121, v121, v153, v121
	v_fma_f32 v122, v122, v154, v122
	v_fma_f32 v123, v123, v155, v123
	v_fma_f32 v124, v124, v156, v124
	v_fma_f32 v125, v125, v157, v125
	v_fma_f32 v126, v126, v158, v126
	v_fma_f32 v127, v127, v159, v127
	v_fma_f32 v128, v128, v160, v128
	v_fma_f32 v129, v129, v161, v129
	v_fma_f32 v130, v130, v162, v130
	v_fma_f32 v131, v131, v163, v131
	s_nop 1
	v_add_f32_dpp v236, v236, v236 quad_perm:[1,0,3,2] row_mask:0xf bank_mask:0xf
	s_nop 1
	v_add_f32_dpp v236, v236, v236 quad_perm:[2,3,0,1] row_mask:0xf bank_mask:0xf
	s_nop 1
	v_add_f32_dpp v236, v236, v236 row_half_mirror row_mask:0xf bank_mask:0xf
	s_nop 1
	v_add_f32_dpp v236, v236, v236 row_mirror row_mask:0xf bank_mask:0xf
	s_nop 1
	v_readlane_b32 s0, v236, 0
	v_readlane_b32 s1, v236, 16
	v_readlane_b32 s2, v236, 32
	v_readlane_b32 s3, v236, 48
	s_nop 3
	v_mov_b32_e32 v237, s0
	v_add_f32_e32 v237, s1, v237
	v_add_f32_e32 v237, s2, v237
	v_add_f32_e32 v237, s3, v237
	v_mul_f32_e32 v237, 0x3a000000, v237
	v_add_f32_e32 v237, 0x358637bd, v237
	v_rsq_f32_e32 v237, v237
	s_nop 0
	v_mul_f32_e32 v100, v100, v237
	v_mul_f32_e32 v101, v101, v237
	v_mul_f32_e32 v102, v102, v237
	v_mul_f32_e32 v103, v103, v237
	v_mul_f32_e32 v104, v104, v237
	v_mul_f32_e32 v105, v105, v237
	v_mul_f32_e32 v106, v106, v237
	v_mul_f32_e32 v107, v107, v237
	v_mul_f32_e32 v108, v108, v237
	v_mul_f32_e32 v109, v109, v237
	v_mul_f32_e32 v110, v110, v237
	v_mul_f32_e32 v111, v111, v237
	v_mul_f32_e32 v112, v112, v237
	v_mul_f32_e32 v113, v113, v237
	v_mul_f32_e32 v114, v114, v237
	v_mul_f32_e32 v115, v115, v237
	v_mul_f32_e32 v116, v116, v237
	v_mul_f32_e32 v117, v117, v237
	v_mul_f32_e32 v118, v118, v237
	v_mul_f32_e32 v119, v119, v237
	v_mul_f32_e32 v120, v120, v237
	v_mul_f32_e32 v121, v121, v237
	v_mul_f32_e32 v122, v122, v237
	v_mul_f32_e32 v123, v123, v237
	v_mul_f32_e32 v124, v124, v237
	v_mul_f32_e32 v125, v125, v237
	v_mul_f32_e32 v126, v126, v237
	v_mul_f32_e32 v127, v127, v237
	v_mul_f32_e32 v128, v128, v237
	v_mul_f32_e32 v129, v129, v237
	v_mul_f32_e32 v130, v130, v237
	v_mul_f32_e32 v131, v131, v237
	v_fma_f32 v4, v4, v100, v68
	v_fma_f32 v5, v5, v101, v69
	v_fma_f32 v6, v6, v102, v70
	v_fma_f32 v7, v7, v103, v71
	v_cvt_pk_bf16_f32 v238, v4, v5
	v_cvt_pk_bf16_f32 v239, v6, v7
	global_store_dwordx2 v2, v[238:239], s[22:23]
	v_fma_f32 v8, v8, v104, v72
	v_fma_f32 v9, v9, v105, v73
	v_fma_f32 v10, v10, v106, v74
	v_fma_f32 v11, v11, v107, v75
	v_cvt_pk_bf16_f32 v240, v8, v9
	v_cvt_pk_bf16_f32 v241, v10, v11
	global_store_dwordx2 v2, v[240:241], s[22:23] offset:512
	v_fma_f32 v12, v12, v108, v76
	v_fma_f32 v13, v13, v109, v77
	v_fma_f32 v14, v14, v110, v78
	v_fma_f32 v15, v15, v111, v79
	v_cvt_pk_bf16_f32 v238, v12, v13
	v_cvt_pk_bf16_f32 v239, v14, v15
	global_store_dwordx2 v2, v[238:239], s[22:23] offset:1024
	v_fma_f32 v16, v16, v112, v80
	v_fma_f32 v17, v17, v113, v81
	v_fma_f32 v18, v18, v114, v82
	v_fma_f32 v19, v19, v115, v83
	v_cvt_pk_bf16_f32 v240, v16, v17
	v_cvt_pk_bf16_f32 v241, v18, v19
	global_store_dwordx2 v2, v[240:241], s[22:23] offset:1536
	v_fma_f32 v20, v20, v116, v84
	v_fma_f32 v21, v21, v117, v85
	v_fma_f32 v22, v22, v118, v86
	v_fma_f32 v23, v23, v119, v87
	v_cvt_pk_bf16_f32 v238, v20, v21
	v_cvt_pk_bf16_f32 v239, v22, v23
	global_store_dwordx2 v2, v[238:239], s[22:23] offset:2048
	v_fma_f32 v24, v24, v120, v88
	v_fma_f32 v25, v25, v121, v89
	v_fma_f32 v26, v26, v122, v90
	v_fma_f32 v27, v27, v123, v91
	v_cvt_pk_bf16_f32 v240, v24, v25
	v_cvt_pk_bf16_f32 v241, v26, v27
	global_store_dwordx2 v2, v[240:241], s[22:23] offset:2560
	v_fma_f32 v28, v28, v124, v92
	v_fma_f32 v29, v29, v125, v93
	v_fma_f32 v30, v30, v126, v94
	v_fma_f32 v31, v31, v127, v95
	v_cvt_pk_bf16_f32 v238, v28, v29
	v_cvt_pk_bf16_f32 v239, v30, v31
	global_store_dwordx2 v2, v[238:239], s[22:23] offset:3072
	v_fma_f32 v32, v32, v128, v96
	v_fma_f32 v33, v33, v129, v97
	v_fma_f32 v34, v34, v130, v98
	v_fma_f32 v35, v35, v131, v99
	v_cvt_pk_bf16_f32 v240, v32, v33
	v_cvt_pk_bf16_f32 v241, v34, v35
	global_store_dwordx2 v2, v[240:241], s[22:23] offset:3584
	s_add_i32 s11, s10, 0x3800
	s_lshr_b32 s0, s11, 8
	s_mul_i32 s0, s0, 57
	s_lshr_b32 s44, s0, 9
	s_mul_i32 s1, s44, 0x900
	s_sub_i32 s43, s11, s1
	s_lshl_b32 s1, s11, 12
	s_add_u32 s22, s50, s1
	s_addc_u32 s23, s51, 0
	s_cmpk_lt_u32 s43, 0x100
	s_cselect_b32 s0, 8, s44
	s_mul_i32 s1, s0, 0xc000
	s_add_u32 s28, s52, s1
	s_addc_u32 s29, s53, 0
	s_add_u32 s30, s28, 0x1000
	s_addc_u32 s31, s29, 0
	global_load_dwordx4 v[100:103], v1, s[56:57]
	global_load_dwordx4 v[104:107], v1, s[56:57] offset:1024
	global_load_dwordx4 v[108:111], v1, s[56:57] offset:2048
	global_load_dwordx4 v[112:115], v1, s[56:57] offset:3072
	global_load_dwordx4 v[116:119], v1, s[58:59]
	global_load_dwordx4 v[120:123], v1, s[58:59] offset:1024
	global_load_dwordx4 v[124:127], v1, s[58:59] offset:2048
	global_load_dwordx4 v[128:131], v1, s[58:59] offset:3072
	s_add_u32 s84, s28, 0x2000
	s_addc_u32 s85, s29, 0
	s_add_u32 s86, s28, 0x3000
	s_addc_u32 s87, s29, 0
	global_load_dwordx4 v[68:71], v1, s[28:29]
	global_load_dwordx4 v[132:135], v1, s[84:85]
	global_load_dwordx4 v[72:75], v1, s[28:29] offset:1024
	global_load_dwordx4 v[136:139], v1, s[84:85] offset:1024
	global_load_dwordx4 v[76:79], v1, s[28:29] offset:2048
	global_load_dwordx4 v[140:143], v1, s[84:85] offset:2048
	global_load_dwordx4 v[80:83], v1, s[28:29] offset:3072
	global_load_dwordx4 v[144:147], v1, s[84:85] offset:3072
	global_load_dwordx4 v[84:87], v1, s[30:31]
	global_load_dwordx4 v[148:151], v1, s[86:87]
	global_load_dwordx4 v[88:91], v1, s[30:31] offset:1024
	global_load_dwordx4 v[152:155], v1, s[86:87] offset:1024
	global_load_dwordx4 v[92:95], v1, s[30:31] offset:2048
	global_load_dwordx4 v[156:159], v1, s[86:87] offset:2048
	global_load_dwordx4 v[96:99], v1, s[30:31] offset:3072
	global_load_dwordx4 v[160:163], v1, s[86:87] offset:3072
	s_add_i32 s11, s10, 0x4000
	s_lshr_b32 s0, s11, 8
	s_mul_i32 s0, s0, 57
	s_lshr_b32 s44, s0, 9
	s_mul_i32 s1, s44, 0x900
	s_sub_i32 s43, s11, s1
	s_lshl_b32 s0, s44, 21
	s_lshl_b32 s1, s43, 13
	s_add_i32 s0, s0, s1
	s_lshl_b32 s2, s44, 24
	s_add_i32 s3, s43, 0xffffff00
	s_lshl_b32 s3, s3, 13
	s_add_i32 s2, s2, s3
	s_cmpk_lt_u32 s43, 0x100
	s_cselect_b32 s0, s0, s2
	s_cselect_b32 s1, s70, s68
	s_cselect_b32 s2, s71, s69
	s_add_u32 s12, s1, s0
	s_addc_u32 s13, s2, 0
	s_add_u32 s14, s12, 0x1000
	s_addc_u32 s15, s13, 0
	global_load_dwordx4 v[4:7], v1, s[12:13]
	global_load_dwordx4 v[8:11], v1, s[12:13] offset:1024
	global_load_dwordx4 v[12:15], v1, s[12:13] offset:2048
	global_load_dwordx4 v[16:19], v1, s[12:13] offset:3072
	global_load_dwordx4 v[20:23], v1, s[14:15]
	global_load_dwordx4 v[24:27], v1, s[14:15] offset:1024
	global_load_dwordx4 v[28:31], v1, s[14:15] offset:2048
	global_load_dwordx4 v[32:35], v1, s[14:15] offset:3072
	s_waitcnt vmcnt(8)
	v_mul_f32_e32 v236, v36, v36
	v_fmac_f32_e32 v236, v37, v37
	v_fmac_f32_e32 v236, v38, v38
	v_fmac_f32_e32 v236, v39, v39
	v_fmac_f32_e32 v236, v40, v40
	v_fmac_f32_e32 v236, v41, v41
	v_fmac_f32_e32 v236, v42, v42
	v_fmac_f32_e32 v236, v43, v43
	v_fmac_f32_e32 v236, v44, v44
	v_fmac_f32_e32 v236, v45, v45
	v_fmac_f32_e32 v236, v46, v46
	v_fmac_f32_e32 v236, v47, v47
	v_fmac_f32_e32 v236, v48, v48
	v_fmac_f32_e32 v236, v49, v49
	v_fmac_f32_e32 v236, v50, v50
	v_fmac_f32_e32 v236, v51, v51
	v_fmac_f32_e32 v236, v52, v52
	v_fmac_f32_e32 v236, v53, v53
	v_fmac_f32_e32 v236, v54, v54
	v_fmac_f32_e32 v236, v55, v55
	v_fmac_f32_e32 v236, v56, v56
	v_fmac_f32_e32 v236, v57, v57
	v_fmac_f32_e32 v236, v58, v58
	v_fmac_f32_e32 v236, v59, v59
	v_fmac_f32_e32 v236, v60, v60
	v_fmac_f32_e32 v236, v61, v61
	v_fmac_f32_e32 v236, v62, v62
	v_fmac_f32_e32 v236, v63, v63
	v_fmac_f32_e32 v236, v64, v64
	v_fmac_f32_e32 v236, v65, v65
	v_fmac_f32_e32 v236, v66, v66
	v_fmac_f32_e32 v236, v67, v67
	v_fma_f32 v100, v100, v132, v100
	v_fma_f32 v101, v101, v133, v101
	v_fma_f32 v102, v102, v134, v102
	v_fma_f32 v103, v103, v135, v103
	v_fma_f32 v104, v104, v136, v104
	v_fma_f32 v105, v105, v137, v105
	v_fma_f32 v106, v106, v138, v106
	v_fma_f32 v107, v107, v139, v107
	v_fma_f32 v108, v108, v140, v108
	v_fma_f32 v109, v109, v141, v109
	v_fma_f32 v110, v110, v142, v110
	v_fma_f32 v111, v111, v143, v111
	v_fma_f32 v112, v112, v144, v112
	v_fma_f32 v113, v113, v145, v113
	v_fma_f32 v114, v114, v146, v114
	v_fma_f32 v115, v115, v147, v115
	v_fma_f32 v116, v116, v148, v116
	v_fma_f32 v117, v117, v149, v117
	v_fma_f32 v118, v118, v150, v118
	v_fma_f32 v119, v119, v151, v119
	v_fma_f32 v120, v120, v152, v120
	v_fma_f32 v121, v121, v153, v121
	v_fma_f32 v122, v122, v154, v122
	v_fma_f32 v123, v123, v155, v123
	v_fma_f32 v124, v124, v156, v124
	v_fma_f32 v125, v125, v157, v125
	v_fma_f32 v126, v126, v158, v126
	v_fma_f32 v127, v127, v159, v127
	v_fma_f32 v128, v128, v160, v128
	v_fma_f32 v129, v129, v161, v129
	v_fma_f32 v130, v130, v162, v130
	v_fma_f32 v131, v131, v163, v131
	s_nop 1
	v_add_f32_dpp v236, v236, v236 quad_perm:[1,0,3,2] row_mask:0xf bank_mask:0xf
	s_nop 1
	v_add_f32_dpp v236, v236, v236 quad_perm:[2,3,0,1] row_mask:0xf bank_mask:0xf
	s_nop 1
	v_add_f32_dpp v236, v236, v236 row_half_mirror row_mask:0xf bank_mask:0xf
	s_nop 1
	v_add_f32_dpp v236, v236, v236 row_mirror row_mask:0xf bank_mask:0xf
	s_nop 1
	v_readlane_b32 s0, v236, 0
	v_readlane_b32 s1, v236, 16
	v_readlane_b32 s2, v236, 32
	v_readlane_b32 s3, v236, 48
	s_nop 3
	v_mov_b32_e32 v237, s0
	v_add_f32_e32 v237, s1, v237
	v_add_f32_e32 v237, s2, v237
	v_add_f32_e32 v237, s3, v237
	v_mul_f32_e32 v237, 0x3a000000, v237
	v_add_f32_e32 v237, 0x358637bd, v237
	v_rsq_f32_e32 v237, v237
	s_nop 0
	v_mul_f32_e32 v100, v100, v237
	v_mul_f32_e32 v101, v101, v237
	v_mul_f32_e32 v102, v102, v237
	v_mul_f32_e32 v103, v103, v237
	v_mul_f32_e32 v104, v104, v237
	v_mul_f32_e32 v105, v105, v237
	v_mul_f32_e32 v106, v106, v237
	v_mul_f32_e32 v107, v107, v237
	v_mul_f32_e32 v108, v108, v237
	v_mul_f32_e32 v109, v109, v237
	v_mul_f32_e32 v110, v110, v237
	v_mul_f32_e32 v111, v111, v237
	v_mul_f32_e32 v112, v112, v237
	v_mul_f32_e32 v113, v113, v237
	v_mul_f32_e32 v114, v114, v237
	v_mul_f32_e32 v115, v115, v237
	v_mul_f32_e32 v116, v116, v237
	v_mul_f32_e32 v117, v117, v237
	v_mul_f32_e32 v118, v118, v237
	v_mul_f32_e32 v119, v119, v237
	v_mul_f32_e32 v120, v120, v237
	v_mul_f32_e32 v121, v121, v237
	v_mul_f32_e32 v122, v122, v237
	v_mul_f32_e32 v123, v123, v237
	v_mul_f32_e32 v124, v124, v237
	v_mul_f32_e32 v125, v125, v237
	v_mul_f32_e32 v126, v126, v237
	v_mul_f32_e32 v127, v127, v237
	v_mul_f32_e32 v128, v128, v237
	v_mul_f32_e32 v129, v129, v237
	v_mul_f32_e32 v130, v130, v237
	v_mul_f32_e32 v131, v131, v237
	v_fma_f32 v36, v36, v100, v68
	v_fma_f32 v37, v37, v101, v69
	v_fma_f32 v38, v38, v102, v70
	v_fma_f32 v39, v39, v103, v71
	v_cvt_pk_bf16_f32 v238, v36, v37
	v_cvt_pk_bf16_f32 v239, v38, v39
	global_store_dwordx2 v2, v[238:239], s[22:23]
	v_fma_f32 v40, v40, v104, v72
	v_fma_f32 v41, v41, v105, v73
	v_fma_f32 v42, v42, v106, v74
	v_fma_f32 v43, v43, v107, v75
	v_cvt_pk_bf16_f32 v240, v40, v41
	v_cvt_pk_bf16_f32 v241, v42, v43
	global_store_dwordx2 v2, v[240:241], s[22:23] offset:512
	v_fma_f32 v44, v44, v108, v76
	v_fma_f32 v45, v45, v109, v77
	v_fma_f32 v46, v46, v110, v78
	v_fma_f32 v47, v47, v111, v79
	v_cvt_pk_bf16_f32 v238, v44, v45
	v_cvt_pk_bf16_f32 v239, v46, v47
	global_store_dwordx2 v2, v[238:239], s[22:23] offset:1024
	v_fma_f32 v48, v48, v112, v80
	v_fma_f32 v49, v49, v113, v81
	v_fma_f32 v50, v50, v114, v82
	v_fma_f32 v51, v51, v115, v83
	v_cvt_pk_bf16_f32 v240, v48, v49
	v_cvt_pk_bf16_f32 v241, v50, v51
	global_store_dwordx2 v2, v[240:241], s[22:23] offset:1536
	v_fma_f32 v52, v52, v116, v84
	v_fma_f32 v53, v53, v117, v85
	v_fma_f32 v54, v54, v118, v86
	v_fma_f32 v55, v55, v119, v87
	v_cvt_pk_bf16_f32 v238, v52, v53
	v_cvt_pk_bf16_f32 v239, v54, v55
	global_store_dwordx2 v2, v[238:239], s[22:23] offset:2048
	v_fma_f32 v56, v56, v120, v88
	v_fma_f32 v57, v57, v121, v89
	v_fma_f32 v58, v58, v122, v90
	v_fma_f32 v59, v59, v123, v91
	v_cvt_pk_bf16_f32 v240, v56, v57
	v_cvt_pk_bf16_f32 v241, v58, v59
	global_store_dwordx2 v2, v[240:241], s[22:23] offset:2560
	v_fma_f32 v60, v60, v124, v92
	v_fma_f32 v61, v61, v125, v93
	v_fma_f32 v62, v62, v126, v94
	v_fma_f32 v63, v63, v127, v95
	v_cvt_pk_bf16_f32 v238, v60, v61
	v_cvt_pk_bf16_f32 v239, v62, v63
	global_store_dwordx2 v2, v[238:239], s[22:23] offset:3072
	v_fma_f32 v64, v64, v128, v96
	v_fma_f32 v65, v65, v129, v97
	v_fma_f32 v66, v66, v130, v98
	v_fma_f32 v67, v67, v131, v99
	v_cvt_pk_bf16_f32 v240, v64, v65
	v_cvt_pk_bf16_f32 v241, v66, v67
	global_store_dwordx2 v2, v[240:241], s[22:23] offset:3584
	s_add_i32 s11, s10, 0x4000
	s_lshr_b32 s0, s11, 8
	s_mul_i32 s0, s0, 57
	s_lshr_b32 s44, s0, 9
	s_mul_i32 s1, s44, 0x900
	s_sub_i32 s43, s11, s1
	s_lshl_b32 s1, s11, 12
	s_add_u32 s22, s50, s1
	s_addc_u32 s23, s51, 0
	s_cmpk_lt_u32 s43, 0x100
	s_cselect_b32 s0, 8, s44
	s_mul_i32 s1, s0, 0xc000
	s_add_u32 s28, s52, s1
	s_addc_u32 s29, s53, 0
	s_add_u32 s30, s28, 0x1000
	s_addc_u32 s31, s29, 0
	global_load_dwordx4 v[100:103], v1, s[56:57]
	global_load_dwordx4 v[104:107], v1, s[56:57] offset:1024
	global_load_dwordx4 v[108:111], v1, s[56:57] offset:2048
	global_load_dwordx4 v[112:115], v1, s[56:57] offset:3072
	global_load_dwordx4 v[116:119], v1, s[58:59]
	global_load_dwordx4 v[120:123], v1, s[58:59] offset:1024
	global_load_dwordx4 v[124:127], v1, s[58:59] offset:2048
	global_load_dwordx4 v[128:131], v1, s[58:59] offset:3072
	s_add_u32 s84, s28, 0x2000
	s_addc_u32 s85, s29, 0
	s_add_u32 s86, s28, 0x3000
	s_addc_u32 s87, s29, 0
	global_load_dwordx4 v[68:71], v1, s[28:29]
	global_load_dwordx4 v[132:135], v1, s[84:85]
	global_load_dwordx4 v[72:75], v1, s[28:29] offset:1024
	global_load_dwordx4 v[136:139], v1, s[84:85] offset:1024
	global_load_dwordx4 v[76:79], v1, s[28:29] offset:2048
	global_load_dwordx4 v[140:143], v1, s[84:85] offset:2048
	global_load_dwordx4 v[80:83], v1, s[28:29] offset:3072
	global_load_dwordx4 v[144:147], v1, s[84:85] offset:3072
	global_load_dwordx4 v[84:87], v1, s[30:31]
	global_load_dwordx4 v[148:151], v1, s[86:87]
	global_load_dwordx4 v[88:91], v1, s[30:31] offset:1024
	global_load_dwordx4 v[152:155], v1, s[86:87] offset:1024
	global_load_dwordx4 v[92:95], v1, s[30:31] offset:2048
	global_load_dwordx4 v[156:159], v1, s[86:87] offset:2048
	global_load_dwordx4 v[96:99], v1, s[30:31] offset:3072
	global_load_dwordx4 v[160:163], v1, s[86:87] offset:3072
	s_waitcnt vmcnt(0)
	v_mul_f32_e32 v236, v4, v4
	v_fmac_f32_e32 v236, v5, v5
	v_fmac_f32_e32 v236, v6, v6
	v_fmac_f32_e32 v236, v7, v7
	v_fmac_f32_e32 v236, v8, v8
	v_fmac_f32_e32 v236, v9, v9
	v_fmac_f32_e32 v236, v10, v10
	v_fmac_f32_e32 v236, v11, v11
	v_fmac_f32_e32 v236, v12, v12
	v_fmac_f32_e32 v236, v13, v13
	v_fmac_f32_e32 v236, v14, v14
	v_fmac_f32_e32 v236, v15, v15
	v_fmac_f32_e32 v236, v16, v16
	v_fmac_f32_e32 v236, v17, v17
	v_fmac_f32_e32 v236, v18, v18
	v_fmac_f32_e32 v236, v19, v19
	v_fmac_f32_e32 v236, v20, v20
	v_fmac_f32_e32 v236, v21, v21
	v_fmac_f32_e32 v236, v22, v22
	v_fmac_f32_e32 v236, v23, v23
	v_fmac_f32_e32 v236, v24, v24
	v_fmac_f32_e32 v236, v25, v25
	v_fmac_f32_e32 v236, v26, v26
	v_fmac_f32_e32 v236, v27, v27
	v_fmac_f32_e32 v236, v28, v28
	v_fmac_f32_e32 v236, v29, v29
	v_fmac_f32_e32 v236, v30, v30
	v_fmac_f32_e32 v236, v31, v31
	v_fmac_f32_e32 v236, v32, v32
	v_fmac_f32_e32 v236, v33, v33
	v_fmac_f32_e32 v236, v34, v34
	v_fmac_f32_e32 v236, v35, v35
	v_fma_f32 v100, v100, v132, v100
	v_fma_f32 v101, v101, v133, v101
	v_fma_f32 v102, v102, v134, v102
	v_fma_f32 v103, v103, v135, v103
	v_fma_f32 v104, v104, v136, v104
	v_fma_f32 v105, v105, v137, v105
	v_fma_f32 v106, v106, v138, v106
	v_fma_f32 v107, v107, v139, v107
	v_fma_f32 v108, v108, v140, v108
	v_fma_f32 v109, v109, v141, v109
	v_fma_f32 v110, v110, v142, v110
	v_fma_f32 v111, v111, v143, v111
	v_fma_f32 v112, v112, v144, v112
	v_fma_f32 v113, v113, v145, v113
	v_fma_f32 v114, v114, v146, v114
	v_fma_f32 v115, v115, v147, v115
	v_fma_f32 v116, v116, v148, v116
	v_fma_f32 v117, v117, v149, v117
	v_fma_f32 v118, v118, v150, v118
	v_fma_f32 v119, v119, v151, v119
	v_fma_f32 v120, v120, v152, v120
	v_fma_f32 v121, v121, v153, v121
	v_fma_f32 v122, v122, v154, v122
	v_fma_f32 v123, v123, v155, v123
	v_fma_f32 v124, v124, v156, v124
	v_fma_f32 v125, v125, v157, v125
	v_fma_f32 v126, v126, v158, v126
	v_fma_f32 v127, v127, v159, v127
	v_fma_f32 v128, v128, v160, v128
	v_fma_f32 v129, v129, v161, v129
	v_fma_f32 v130, v130, v162, v130
	v_fma_f32 v131, v131, v163, v131
	s_nop 1
	v_add_f32_dpp v236, v236, v236 quad_perm:[1,0,3,2] row_mask:0xf bank_mask:0xf
	s_nop 1
	v_add_f32_dpp v236, v236, v236 quad_perm:[2,3,0,1] row_mask:0xf bank_mask:0xf
	s_nop 1
	v_add_f32_dpp v236, v236, v236 row_half_mirror row_mask:0xf bank_mask:0xf
	s_nop 1
	v_add_f32_dpp v236, v236, v236 row_mirror row_mask:0xf bank_mask:0xf
	s_nop 1
	v_readlane_b32 s0, v236, 0
	v_readlane_b32 s1, v236, 16
	v_readlane_b32 s2, v236, 32
	v_readlane_b32 s3, v236, 48
	s_nop 3
	v_mov_b32_e32 v237, s0
	v_add_f32_e32 v237, s1, v237
	v_add_f32_e32 v237, s2, v237
	v_add_f32_e32 v237, s3, v237
	v_mul_f32_e32 v237, 0x3a000000, v237
	v_add_f32_e32 v237, 0x358637bd, v237
	v_rsq_f32_e32 v237, v237
	s_nop 0
	v_mul_f32_e32 v100, v100, v237
	v_mul_f32_e32 v101, v101, v237
	v_mul_f32_e32 v102, v102, v237
	v_mul_f32_e32 v103, v103, v237
	v_mul_f32_e32 v104, v104, v237
	v_mul_f32_e32 v105, v105, v237
	v_mul_f32_e32 v106, v106, v237
	v_mul_f32_e32 v107, v107, v237
	v_mul_f32_e32 v108, v108, v237
	v_mul_f32_e32 v109, v109, v237
	v_mul_f32_e32 v110, v110, v237
	v_mul_f32_e32 v111, v111, v237
	v_mul_f32_e32 v112, v112, v237
	v_mul_f32_e32 v113, v113, v237
	v_mul_f32_e32 v114, v114, v237
	v_mul_f32_e32 v115, v115, v237
	v_mul_f32_e32 v116, v116, v237
	v_mul_f32_e32 v117, v117, v237
	v_mul_f32_e32 v118, v118, v237
	v_mul_f32_e32 v119, v119, v237
	v_mul_f32_e32 v120, v120, v237
	v_mul_f32_e32 v121, v121, v237
	v_mul_f32_e32 v122, v122, v237
	v_mul_f32_e32 v123, v123, v237
	v_mul_f32_e32 v124, v124, v237
	v_mul_f32_e32 v125, v125, v237
	v_mul_f32_e32 v126, v126, v237
	v_mul_f32_e32 v127, v127, v237
	v_mul_f32_e32 v128, v128, v237
	v_mul_f32_e32 v129, v129, v237
	v_mul_f32_e32 v130, v130, v237
	v_mul_f32_e32 v131, v131, v237
	v_fma_f32 v4, v4, v100, v68
	v_fma_f32 v5, v5, v101, v69
	v_fma_f32 v6, v6, v102, v70
	v_fma_f32 v7, v7, v103, v71
	v_cvt_pk_bf16_f32 v238, v4, v5
	v_cvt_pk_bf16_f32 v239, v6, v7
	global_store_dwordx2 v2, v[238:239], s[22:23]
	v_fma_f32 v8, v8, v104, v72
	v_fma_f32 v9, v9, v105, v73
	v_fma_f32 v10, v10, v106, v74
	v_fma_f32 v11, v11, v107, v75
	v_cvt_pk_bf16_f32 v240, v8, v9
	v_cvt_pk_bf16_f32 v241, v10, v11
	global_store_dwordx2 v2, v[240:241], s[22:23] offset:512
	v_fma_f32 v12, v12, v108, v76
	v_fma_f32 v13, v13, v109, v77
	v_fma_f32 v14, v14, v110, v78
	v_fma_f32 v15, v15, v111, v79
	v_cvt_pk_bf16_f32 v238, v12, v13
	v_cvt_pk_bf16_f32 v239, v14, v15
	global_store_dwordx2 v2, v[238:239], s[22:23] offset:1024
	v_fma_f32 v16, v16, v112, v80
	v_fma_f32 v17, v17, v113, v81
	v_fma_f32 v18, v18, v114, v82
	v_fma_f32 v19, v19, v115, v83
	v_cvt_pk_bf16_f32 v240, v16, v17
	v_cvt_pk_bf16_f32 v241, v18, v19
	global_store_dwordx2 v2, v[240:241], s[22:23] offset:1536
	v_fma_f32 v20, v20, v116, v84
	v_fma_f32 v21, v21, v117, v85
	v_fma_f32 v22, v22, v118, v86
	v_fma_f32 v23, v23, v119, v87
	v_cvt_pk_bf16_f32 v238, v20, v21
	v_cvt_pk_bf16_f32 v239, v22, v23
	global_store_dwordx2 v2, v[238:239], s[22:23] offset:2048
	v_fma_f32 v24, v24, v120, v88
	v_fma_f32 v25, v25, v121, v89
	v_fma_f32 v26, v26, v122, v90
	v_fma_f32 v27, v27, v123, v91
	v_cvt_pk_bf16_f32 v240, v24, v25
	v_cvt_pk_bf16_f32 v241, v26, v27
	global_store_dwordx2 v2, v[240:241], s[22:23] offset:2560
	v_fma_f32 v28, v28, v124, v92
	v_fma_f32 v29, v29, v125, v93
	v_fma_f32 v30, v30, v126, v94
	v_fma_f32 v31, v31, v127, v95
	v_cvt_pk_bf16_f32 v238, v28, v29
	v_cvt_pk_bf16_f32 v239, v30, v31
	global_store_dwordx2 v2, v[238:239], s[22:23] offset:3072
	v_fma_f32 v32, v32, v128, v96
	v_fma_f32 v33, v33, v129, v97
	v_fma_f32 v34, v34, v130, v98
	v_fma_f32 v35, v35, v131, v99
	v_cvt_pk_bf16_f32 v240, v32, v33
	v_cvt_pk_bf16_f32 v241, v34, v35
	global_store_dwordx2 v2, v[240:241], s[22:23] offset:3584

.LBB0_10910:
	v_readlane_b32 s2, v251, 39
	v_readlane_b32 s3, v251, 40
	s_cmp_lt_i32 s2, 28
	s_cselect_b64 s[0:1], -1, 0
	s_cmp_gt_i32 s3, 27
	s_cselect_b64 s[2:3], -1, 0
	s_and_b64 s[0:1], s[0:1], s[2:3]
	v_readlane_b32 s16, v251, 57
	s_and_b64 vcc, exec, s[0:1]
	v_readlane_b32 s17, v251, 58
	v_readlane_b32 s18, v251, 59
	v_readlane_b32 s19, v251, 60
	s_cbranch_vccz .LBB0_10944
	v_readlane_b32 s4, v251, 59
	v_readlane_b32 s5, v251, 60
	v_readlane_b32 s10, v251, 61
	v_readfirstlane_b32 s0, v0
	v_readlane_b32 s66, v251, 57
	v_readlane_b32 s67, v251, 58
	s_nop 3
	s_mov_b32 s8, 1
	s_lshr_b32 s0, s0, 6
	s_add_i32 s10, s10, s0
	s_mul_i32 s1, s8, 0x6c000
	s_add_i32 s1, s1, 0x10000
	s_add_u32 s52, s4, s1
	s_addc_u32 s53, s5, 0
	s_add_u32 s48, s4, 0x33c90000
	s_addc_u32 s49, s5, 0
	s_add_u32 s62, s4, 0x4f0000
	s_addc_u32 s63, s5, 0
	s_add_u32 s64, s4, 0x57c90000
	s_addc_u32 s65, s5, 0
	v_and_b32_e32 v238, 63, v0
	v_lshlrev_b32_e32 v1, 4, v238
	v_lshlrev_b32_e32 v2, 3, v238
	v_lshlrev_b32_e32 v246, 2, v238
	s_add_i32 s11, s10, 0x0
	s_lshr_b32 s0, s11, 8
	s_mul_i32 s0, s0, 57
	s_lshr_b32 s44, s0, 9
	s_mul_i32 s1, s44, 0x900
	s_sub_i32 s43, s11, s1
	s_lshl_b32 s1, s11, 6
	s_add_u32 s78, s62, s1
	s_addc_u32 s79, s63, 0
	global_load_dword v234, v246, s[78:79]
	s_lshl_b32 s1, s11, 13
	s_add_u32 s12, s48, s1
	s_addc_u32 s13, s49, 0
	s_add_u32 s14, s12, 0x1000
	s_addc_u32 s15, s13, 0
	global_load_dwordx4 v[4:7], v1, s[12:13]
	global_load_dwordx4 v[8:11], v1, s[12:13] offset:1024
	global_load_dwordx4 v[12:15], v1, s[12:13] offset:2048
	global_load_dwordx4 v[16:19], v1, s[12:13] offset:3072
	global_load_dwordx4 v[20:23], v1, s[14:15]
	global_load_dwordx4 v[24:27], v1, s[14:15] offset:1024
	global_load_dwordx4 v[28:31], v1, s[14:15] offset:2048
	global_load_dwordx4 v[32:35], v1, s[14:15] offset:3072
	s_add_i32 s11, s10, 0x0
	s_lshr_b32 s0, s11, 8
	s_mul_i32 s0, s0, 57
	s_lshr_b32 s44, s0, 9
	s_mul_i32 s1, s44, 0x900
	s_sub_i32 s43, s11, s1
	s_lshl_b32 s0, s44, 11
	s_add_i32 s0, s0, s43
	s_add_i32 s0, s0, 0xffffff00
	s_lshl_b32 s0, s0, 13
	s_lshl_b32 s1, s11, 13
	s_cmpk_lt_u32 s43, 0x100
	s_cselect_b32 s0, s1, s0
	s_cselect_b32 s1, s48, s66
	s_cselect_b32 s2, s49, s67
	s_add_u32 s16, s1, s0
	s_addc_u32 s17, s2, 0
	s_add_u32 s18, s16, 0x1000
	s_addc_u32 s19, s17, 0
	s_cmpk_lt_u32 s43, 0x100
	s_cselect_b32 s0, 8, s44
	s_mul_i32 s1, s0, 0xc000
	s_add_u32 s72, s52, s1
	s_addc_u32 s73, s53, 0
	s_add_u32 s72, s72, 0xa000
	s_addc_u32 s73, s73, 0
	s_add_u32 s74, s72, 0x1000
	s_addc_u32 s75, s73, 0
	global_load_dwordx4 v[68:71], v1, s[72:73]
	global_load_dwordx4 v[72:75], v1, s[72:73] offset:1024
	global_load_dwordx4 v[76:79], v1, s[72:73] offset:2048
	global_load_dwordx4 v[80:83], v1, s[72:73] offset:3072
	global_load_dwordx4 v[84:87], v1, s[74:75]
	global_load_dwordx4 v[88:91], v1, s[74:75] offset:1024
	global_load_dwordx4 v[92:95], v1, s[74:75] offset:2048
	global_load_dwordx4 v[96:99], v1, s[74:75] offset:3072
	s_waitcnt vmcnt(16)
	v_cmp_le_i32_e64 s[0:1], 0, v234
	s_nop 1
	s_and_b32 s45, s0, 0xffff
	s_cmpk_lt_u32 s43, 0x100
	s_cselect_b32 s45, 0, s45
	s_mov_b32 s47, 0
	s_mov_b32 s61, 0
	s_cmp_eq_u32 s45, 0
	s_cbranch_scc1 .Ln2_y0_0
	s_mov_b32 s47, 1
	s_ff1_i32_b32 s0, s45
	s_add_i32 s1, s45, -1
	s_and_b32 s45, s45, s1
	s_nop 0
	v_readlane_b32 s0, v234, s0
	s_nop 3
	s_lshl_b32 s0, s0, 12
	s_add_u32 s76, s64, s0
	s_addc_u32 s77, s65, 0
	global_load_dwordx2 v[196:197], v2, s[76:77]
	global_load_dwordx2 v[198:199], v2, s[76:77] offset:512
	global_load_dwordx2 v[200:201], v2, s[76:77] offset:1024
	global_load_dwordx2 v[202:203], v2, s[76:77] offset:1536
	global_load_dwordx2 v[204:205], v2, s[76:77] offset:2048
	global_load_dwordx2 v[206:207], v2, s[76:77] offset:2560
	global_load_dwordx2 v[208:209], v2, s[76:77] offset:3072
	global_load_dwordx2 v[210:211], v2, s[76:77] offset:3584
	s_cmp_eq_u32 s45, 0
	s_cbranch_scc1 .Ln2_y0_0
	s_mov_b32 s61, 1
	s_ff1_i32_b32 s0, s45
	s_add_i32 s1, s45, -1
	s_and_b32 s45, s45, s1
	s_nop 0
	v_readlane_b32 s0, v234, s0
	s_nop 3
	s_lshl_b32 s0, s0, 12
	s_add_u32 s76, s64, s0
	s_addc_u32 s77, s65, 0
	global_load_dwordx2 v[212:213], v2, s[76:77]
	global_load_dwordx2 v[214:215], v2, s[76:77] offset:512
	global_load_dwordx2 v[216:217], v2, s[76:77] offset:1024
	global_load_dwordx2 v[218:219], v2, s[76:77] offset:1536
	global_load_dwordx2 v[226:227], v2, s[76:77] offset:2048
	global_load_dwordx2 v[228:229], v2, s[76:77] offset:2560
	global_load_dwordx2 v[230:231], v2, s[76:77] offset:3072
	global_load_dwordx2 v[232:233], v2, s[76:77] offset:3584

.Ln2_gd_0:
	global_store_dwordx4 v1, v[4:7], s[16:17]
	global_store_dwordx4 v1, v[8:11], s[16:17] offset:1024
	global_store_dwordx4 v1, v[12:15], s[16:17] offset:2048
	global_store_dwordx4 v1, v[16:19], s[16:17] offset:3072
	global_store_dwordx4 v1, v[20:23], s[18:19]
	global_store_dwordx4 v1, v[24:27], s[18:19] offset:1024
	global_store_dwordx4 v1, v[28:31], s[18:19] offset:2048
	global_store_dwordx4 v1, v[32:35], s[18:19] offset:3072
	s_add_i32 s11, s10, 0x800
	s_lshr_b32 s0, s11, 8
	s_mul_i32 s0, s0, 57
	s_lshr_b32 s44, s0, 9
	s_mul_i32 s1, s44, 0x900
	s_sub_i32 s43, s11, s1
	s_lshl_b32 s0, s44, 11
	s_add_i32 s0, s0, s43
	s_add_i32 s0, s0, 0xffffff00
	s_lshl_b32 s0, s0, 13
	s_lshl_b32 s1, s11, 13
	s_cmpk_lt_u32 s43, 0x100
	s_cselect_b32 s0, s1, s0
	s_cselect_b32 s1, s48, s66
	s_cselect_b32 s2, s49, s67
	s_add_u32 s16, s1, s0
	s_addc_u32 s17, s2, 0
	s_add_u32 s18, s16, 0x1000
	s_addc_u32 s19, s17, 0
	s_cmpk_lt_u32 s43, 0x100
	s_cselect_b32 s0, 8, s44
	s_mul_i32 s1, s0, 0xc000
	s_add_u32 s72, s52, s1
	s_addc_u32 s73, s53, 0
	s_add_u32 s72, s72, 0xa000
	s_addc_u32 s73, s73, 0
	s_add_u32 s74, s72, 0x1000
	s_addc_u32 s75, s73, 0
	global_load_dwordx4 v[68:71], v1, s[72:73]
	global_load_dwordx4 v[72:75], v1, s[72:73] offset:1024
	global_load_dwordx4 v[76:79], v1, s[72:73] offset:2048
	global_load_dwordx4 v[80:83], v1, s[72:73] offset:3072
	global_load_dwordx4 v[84:87], v1, s[74:75]
	global_load_dwordx4 v[88:91], v1, s[74:75] offset:1024
	global_load_dwordx4 v[92:95], v1, s[74:75] offset:2048
	global_load_dwordx4 v[96:99], v1, s[74:75] offset:3072
	s_waitcnt vmcnt(24)
	v_cmp_le_i32_e64 s[0:1], 0, v235
	s_nop 1
	s_and_b32 s45, s0, 0xffff
	s_cmpk_lt_u32 s43, 0x100
	s_cselect_b32 s45, 0, s45
	s_mov_b32 s47, 0
	s_mov_b32 s61, 0
	s_cmp_eq_u32 s45, 0
	s_cbranch_scc1 .Ln2_y0_1
	s_mov_b32 s47, 1
	s_ff1_i32_b32 s0, s45
	s_add_i32 s1, s45, -1
	s_and_b32 s45, s45, s1
	s_nop 0
	v_readlane_b32 s0, v235, s0
	s_nop 3
	s_lshl_b32 s0, s0, 12
	s_add_u32 s76, s64, s0
	s_addc_u32 s77, s65, 0
	global_load_dwordx2 v[196:197], v2, s[76:77]
	global_load_dwordx2 v[198:199], v2, s[76:77] offset:512
	global_load_dwordx2 v[200:201], v2, s[76:77] offset:1024
	global_load_dwordx2 v[202:203], v2, s[76:77] offset:1536
	global_load_dwordx2 v[204:205], v2, s[76:77] offset:2048
	global_load_dwordx2 v[206:207], v2, s[76:77] offset:2560
	global_load_dwordx2 v[208:209], v2, s[76:77] offset:3072
	global_load_dwordx2 v[210:211], v2, s[76:77] offset:3584
	s_cmp_eq_u32 s45, 0
	s_cbranch_scc1 .Ln2_y0_1
	s_mov_b32 s61, 1
	s_ff1_i32_b32 s0, s45
	s_add_i32 s1, s45, -1
	s_and_b32 s45, s45, s1
	s_nop 0
	v_readlane_b32 s0, v235, s0
	s_nop 3
	s_lshl_b32 s0, s0, 12
	s_add_u32 s76, s64, s0
	s_addc_u32 s77, s65, 0
	global_load_dwordx2 v[212:213], v2, s[76:77]
	global_load_dwordx2 v[214:215], v2, s[76:77] offset:512
	global_load_dwordx2 v[216:217], v2, s[76:77] offset:1024
	global_load_dwordx2 v[218:219], v2, s[76:77] offset:1536
	global_load_dwordx2 v[226:227], v2, s[76:77] offset:2048
	global_load_dwordx2 v[228:229], v2, s[76:77] offset:2560
	global_load_dwordx2 v[230:231], v2, s[76:77] offset:3072
	global_load_dwordx2 v[232:233], v2, s[76:77] offset:3584

.Ln2_gd_1:
	global_store_dwordx4 v1, v[36:39], s[16:17]
	global_store_dwordx4 v1, v[40:43], s[16:17] offset:1024
	global_store_dwordx4 v1, v[44:47], s[16:17] offset:2048
	global_store_dwordx4 v1, v[48:51], s[16:17] offset:3072
	global_store_dwordx4 v1, v[52:55], s[18:19]
	global_store_dwordx4 v1, v[56:59], s[18:19] offset:1024
	global_store_dwordx4 v1, v[60:63], s[18:19] offset:2048
	global_store_dwordx4 v1, v[64:67], s[18:19] offset:3072
	s_add_i32 s11, s10, 0x1000
	s_lshr_b32 s0, s11, 8
	s_mul_i32 s0, s0, 57
	s_lshr_b32 s44, s0, 9
	s_mul_i32 s1, s44, 0x900
	s_sub_i32 s43, s11, s1
	s_lshl_b32 s0, s44, 11
	s_add_i32 s0, s0, s43
	s_add_i32 s0, s0, 0xffffff00
	s_lshl_b32 s0, s0, 13
	s_lshl_b32 s1, s11, 13
	s_cmpk_lt_u32 s43, 0x100
	s_cselect_b32 s0, s1, s0
	s_cselect_b32 s1, s48, s66
	s_cselect_b32 s2, s49, s67
	s_add_u32 s16, s1, s0
	s_addc_u32 s17, s2, 0
	s_add_u32 s18, s16, 0x1000
	s_addc_u32 s19, s17, 0
	s_cmpk_lt_u32 s43, 0x100
	s_cselect_b32 s0, 8, s44
	s_mul_i32 s1, s0, 0xc000
	s_add_u32 s72, s52, s1
	s_addc_u32 s73, s53, 0
	s_add_u32 s72, s72, 0xa000
	s_addc_u32 s73, s73, 0
	s_add_u32 s74, s72, 0x1000
	s_addc_u32 s75, s73, 0
	global_load_dwordx4 v[68:71], v1, s[72:73]
	global_load_dwordx4 v[72:75], v1, s[72:73] offset:1024
	global_load_dwordx4 v[76:79], v1, s[72:73] offset:2048
	global_load_dwordx4 v[80:83], v1, s[72:73] offset:3072
	global_load_dwordx4 v[84:87], v1, s[74:75]
	global_load_dwordx4 v[88:91], v1, s[74:75] offset:1024
	global_load_dwordx4 v[92:95], v1, s[74:75] offset:2048
	global_load_dwordx4 v[96:99], v1, s[74:75] offset:3072
	s_waitcnt vmcnt(24)
	v_cmp_le_i32_e64 s[0:1], 0, v234
	s_nop 1
	s_and_b32 s45, s0, 0xffff
	s_cmpk_lt_u32 s43, 0x100
	s_cselect_b32 s45, 0, s45
	s_mov_b32 s47, 0
	s_mov_b32 s61, 0
	s_cmp_eq_u32 s45, 0
	s_cbranch_scc1 .Ln2_y0_2
	s_mov_b32 s47, 1
	s_ff1_i32_b32 s0, s45
	s_add_i32 s1, s45, -1
	s_and_b32 s45, s45, s1
	s_nop 0
	v_readlane_b32 s0, v234, s0
	s_nop 3
	s_lshl_b32 s0, s0, 12
	s_add_u32 s76, s64, s0
	s_addc_u32 s77, s65, 0
	global_load_dwordx2 v[196:197], v2, s[76:77]
	global_load_dwordx2 v[198:199], v2, s[76:77] offset:512
	global_load_dwordx2 v[200:201], v2, s[76:77] offset:1024
	global_load_dwordx2 v[202:203], v2, s[76:77] offset:1536
	global_load_dwordx2 v[204:205], v2, s[76:77] offset:2048
	global_load_dwordx2 v[206:207], v2, s[76:77] offset:2560
	global_load_dwordx2 v[208:209], v2, s[76:77] offset:3072
	global_load_dwordx2 v[210:211], v2, s[76:77] offset:3584
	s_cmp_eq_u32 s45, 0
	s_cbranch_scc1 .Ln2_y0_2
	s_mov_b32 s61, 1
	s_ff1_i32_b32 s0, s45
	s_add_i32 s1, s45, -1
	s_and_b32 s45, s45, s1
	s_nop 0
	v_readlane_b32 s0, v234, s0
	s_nop 3
	s_lshl_b32 s0, s0, 12
	s_add_u32 s76, s64, s0
	s_addc_u32 s77, s65, 0
	global_load_dwordx2 v[212:213], v2, s[76:77]
	global_load_dwordx2 v[214:215], v2, s[76:77] offset:512
	global_load_dwordx2 v[216:217], v2, s[76:77] offset:1024
	global_load_dwordx2 v[218:219], v2, s[76:77] offset:1536
	global_load_dwordx2 v[226:227], v2, s[76:77] offset:2048
	global_load_dwordx2 v[228:229], v2, s[76:77] offset:2560
	global_load_dwordx2 v[230:231], v2, s[76:77] offset:3072
	global_load_dwordx2 v[232:233], v2, s[76:77] offset:3584

.Ln2_gd_2:
	global_store_dwordx4 v1, v[4:7], s[16:17]
	global_store_dwordx4 v1, v[8:11], s[16:17] offset:1024
	global_store_dwordx4 v1, v[12:15], s[16:17] offset:2048
	global_store_dwordx4 v1, v[16:19], s[16:17] offset:3072
	global_store_dwordx4 v1, v[20:23], s[18:19]
	global_store_dwordx4 v1, v[24:27], s[18:19] offset:1024
	global_store_dwordx4 v1, v[28:31], s[18:19] offset:2048
	global_store_dwordx4 v1, v[32:35], s[18:19] offset:3072
	s_add_i32 s11, s10, 0x1800
	s_lshr_b32 s0, s11, 8
	s_mul_i32 s0, s0, 57
	s_lshr_b32 s44, s0, 9
	s_mul_i32 s1, s44, 0x900
	s_sub_i32 s43, s11, s1
	s_lshl_b32 s0, s44, 11
	s_add_i32 s0, s0, s43
	s_add_i32 s0, s0, 0xffffff00
	s_lshl_b32 s0, s0, 13
	s_lshl_b32 s1, s11, 13
	s_cmpk_lt_u32 s43, 0x100
	s_cselect_b32 s0, s1, s0
	s_cselect_b32 s1, s48, s66
	s_cselect_b32 s2, s49, s67
	s_add_u32 s16, s1, s0
	s_addc_u32 s17, s2, 0
	s_add_u32 s18, s16, 0x1000
	s_addc_u32 s19, s17, 0
	s_cmpk_lt_u32 s43, 0x100
	s_cselect_b32 s0, 8, s44
	s_mul_i32 s1, s0, 0xc000
	s_add_u32 s72, s52, s1
	s_addc_u32 s73, s53, 0
	s_add_u32 s72, s72, 0xa000
	s_addc_u32 s73, s73, 0
	s_add_u32 s74, s72, 0x1000
	s_addc_u32 s75, s73, 0
	global_load_dwordx4 v[68:71], v1, s[72:73]
	global_load_dwordx4 v[72:75], v1, s[72:73] offset:1024
	global_load_dwordx4 v[76:79], v1, s[72:73] offset:2048
	global_load_dwordx4 v[80:83], v1, s[72:73] offset:3072
	global_load_dwordx4 v[84:87], v1, s[74:75]
	global_load_dwordx4 v[88:91], v1, s[74:75] offset:1024
	global_load_dwordx4 v[92:95], v1, s[74:75] offset:2048
	global_load_dwordx4 v[96:99], v1, s[74:75] offset:3072
	s_waitcnt vmcnt(24)
	v_cmp_le_i32_e64 s[0:1], 0, v235
	s_nop 1
	s_and_b32 s45, s0, 0xffff
	s_cmpk_lt_u32 s43, 0x100
	s_cselect_b32 s45, 0, s45
	s_mov_b32 s47, 0
	s_mov_b32 s61, 0
	s_cmp_eq_u32 s45, 0
	s_cbranch_scc1 .Ln2_y0_3
	s_mov_b32 s47, 1
	s_ff1_i32_b32 s0, s45
	s_add_i32 s1, s45, -1
	s_and_b32 s45, s45, s1
	s_nop 0
	v_readlane_b32 s0, v235, s0
	s_nop 3
	s_lshl_b32 s0, s0, 12
	s_add_u32 s76, s64, s0
	s_addc_u32 s77, s65, 0
	global_load_dwordx2 v[196:197], v2, s[76:77]
	global_load_dwordx2 v[198:199], v2, s[76:77] offset:512
	global_load_dwordx2 v[200:201], v2, s[76:77] offset:1024
	global_load_dwordx2 v[202:203], v2, s[76:77] offset:1536
	global_load_dwordx2 v[204:205], v2, s[76:77] offset:2048
	global_load_dwordx2 v[206:207], v2, s[76:77] offset:2560
	global_load_dwordx2 v[208:209], v2, s[76:77] offset:3072
	global_load_dwordx2 v[210:211], v2, s[76:77] offset:3584
	s_cmp_eq_u32 s45, 0
	s_cbranch_scc1 .Ln2_y0_3
	s_mov_b32 s61, 1
	s_ff1_i32_b32 s0, s45
	s_add_i32 s1, s45, -1
	s_and_b32 s45, s45, s1
	s_nop 0
	v_readlane_b32 s0, v235, s0
	s_nop 3
	s_lshl_b32 s0, s0, 12
	s_add_u32 s76, s64, s0
	s_addc_u32 s77, s65, 0
	global_load_dwordx2 v[212:213], v2, s[76:77]
	global_load_dwordx2 v[214:215], v2, s[76:77] offset:512
	global_load_dwordx2 v[216:217], v2, s[76:77] offset:1024
	global_load_dwordx2 v[218:219], v2, s[76:77] offset:1536
	global_load_dwordx2 v[226:227], v2, s[76:77] offset:2048
	global_load_dwordx2 v[228:229], v2, s[76:77] offset:2560
	global_load_dwordx2 v[230:231], v2, s[76:77] offset:3072
	global_load_dwordx2 v[232:233], v2, s[76:77] offset:3584

.Ln2_gd_3:
	global_store_dwordx4 v1, v[36:39], s[16:17]
	global_store_dwordx4 v1, v[40:43], s[16:17] offset:1024
	global_store_dwordx4 v1, v[44:47], s[16:17] offset:2048
	global_store_dwordx4 v1, v[48:51], s[16:17] offset:3072
	global_store_dwordx4 v1, v[52:55], s[18:19]
	global_store_dwordx4 v1, v[56:59], s[18:19] offset:1024
	global_store_dwordx4 v1, v[60:63], s[18:19] offset:2048
	global_store_dwordx4 v1, v[64:67], s[18:19] offset:3072
	s_add_i32 s11, s10, 0x2000
	s_lshr_b32 s0, s11, 8
	s_mul_i32 s0, s0, 57
	s_lshr_b32 s44, s0, 9
	s_mul_i32 s1, s44, 0x900
	s_sub_i32 s43, s11, s1
	s_lshl_b32 s0, s44, 11
	s_add_i32 s0, s0, s43
	s_add_i32 s0, s0, 0xffffff00
	s_lshl_b32 s0, s0, 13
	s_lshl_b32 s1, s11, 13
	s_cmpk_lt_u32 s43, 0x100
	s_cselect_b32 s0, s1, s0
	s_cselect_b32 s1, s48, s66
	s_cselect_b32 s2, s49, s67
	s_add_u32 s16, s1, s0
	s_addc_u32 s17, s2, 0
	s_add_u32 s18, s16, 0x1000
	s_addc_u32 s19, s17, 0
	s_cmpk_lt_u32 s43, 0x100
	s_cselect_b32 s0, 8, s44
	s_mul_i32 s1, s0, 0xc000
	s_add_u32 s72, s52, s1
	s_addc_u32 s73, s53, 0
	s_add_u32 s72, s72, 0xa000
	s_addc_u32 s73, s73, 0
	s_add_u32 s74, s72, 0x1000
	s_addc_u32 s75, s73, 0
	global_load_dwordx4 v[68:71], v1, s[72:73]
	global_load_dwordx4 v[72:75], v1, s[72:73] offset:1024
	global_load_dwordx4 v[76:79], v1, s[72:73] offset:2048
	global_load_dwordx4 v[80:83], v1, s[72:73] offset:3072
	global_load_dwordx4 v[84:87], v1, s[74:75]
	global_load_dwordx4 v[88:91], v1, s[74:75] offset:1024
	global_load_dwordx4 v[92:95], v1, s[74:75] offset:2048
	global_load_dwordx4 v[96:99], v1, s[74:75] offset:3072
	s_waitcnt vmcnt(24)
	v_cmp_le_i32_e64 s[0:1], 0, v234
	s_nop 1
	s_and_b32 s45, s0, 0xffff
	s_cmpk_lt_u32 s43, 0x100
	s_cselect_b32 s45, 0, s45
	s_mov_b32 s47, 0
	s_mov_b32 s61, 0
	s_cmp_eq_u32 s45, 0
	s_cbranch_scc1 .Ln2_y0_4
	s_mov_b32 s47, 1
	s_ff1_i32_b32 s0, s45
	s_add_i32 s1, s45, -1
	s_and_b32 s45, s45, s1
	s_nop 0
	v_readlane_b32 s0, v234, s0
	s_nop 3
	s_lshl_b32 s0, s0, 12
	s_add_u32 s76, s64, s0
	s_addc_u32 s77, s65, 0
	global_load_dwordx2 v[196:197], v2, s[76:77]
	global_load_dwordx2 v[198:199], v2, s[76:77] offset:512
	global_load_dwordx2 v[200:201], v2, s[76:77] offset:1024
	global_load_dwordx2 v[202:203], v2, s[76:77] offset:1536
	global_load_dwordx2 v[204:205], v2, s[76:77] offset:2048
	global_load_dwordx2 v[206:207], v2, s[76:77] offset:2560
	global_load_dwordx2 v[208:209], v2, s[76:77] offset:3072
	global_load_dwordx2 v[210:211], v2, s[76:77] offset:3584
	s_cmp_eq_u32 s45, 0
	s_cbranch_scc1 .Ln2_y0_4
	s_mov_b32 s61, 1
	s_ff1_i32_b32 s0, s45
	s_add_i32 s1, s45, -1
	s_and_b32 s45, s45, s1
	s_nop 0
	v_readlane_b32 s0, v234, s0
	s_nop 3
	s_lshl_b32 s0, s0, 12
	s_add_u32 s76, s64, s0
	s_addc_u32 s77, s65, 0
	global_load_dwordx2 v[212:213], v2, s[76:77]
	global_load_dwordx2 v[214:215], v2, s[76:77] offset:512
	global_load_dwordx2 v[216:217], v2, s[76:77] offset:1024
	global_load_dwordx2 v[218:219], v2, s[76:77] offset:1536
	global_load_dwordx2 v[226:227], v2, s[76:77] offset:2048
	global_load_dwordx2 v[228:229], v2, s[76:77] offset:2560
	global_load_dwordx2 v[230:231], v2, s[76:77] offset:3072
	global_load_dwordx2 v[232:233], v2, s[76:77] offset:3584

.Ln2_gd_4:
	global_store_dwordx4 v1, v[4:7], s[16:17]
	global_store_dwordx4 v1, v[8:11], s[16:17] offset:1024
	global_store_dwordx4 v1, v[12:15], s[16:17] offset:2048
	global_store_dwordx4 v1, v[16:19], s[16:17] offset:3072
	global_store_dwordx4 v1, v[20:23], s[18:19]
	global_store_dwordx4 v1, v[24:27], s[18:19] offset:1024
	global_store_dwordx4 v1, v[28:31], s[18:19] offset:2048
	global_store_dwordx4 v1, v[32:35], s[18:19] offset:3072
	s_add_i32 s11, s10, 0x2800
	s_lshr_b32 s0, s11, 8
	s_mul_i32 s0, s0, 57
	s_lshr_b32 s44, s0, 9
	s_mul_i32 s1, s44, 0x900
	s_sub_i32 s43, s11, s1
	s_lshl_b32 s0, s44, 11
	s_add_i32 s0, s0, s43
	s_add_i32 s0, s0, 0xffffff00
	s_lshl_b32 s0, s0, 13
	s_lshl_b32 s1, s11, 13
	s_cmpk_lt_u32 s43, 0x100
	s_cselect_b32 s0, s1, s0
	s_cselect_b32 s1, s48, s66
	s_cselect_b32 s2, s49, s67
	s_add_u32 s16, s1, s0
	s_addc_u32 s17, s2, 0
	s_add_u32 s18, s16, 0x1000
	s_addc_u32 s19, s17, 0
	s_cmpk_lt_u32 s43, 0x100
	s_cselect_b32 s0, 8, s44
	s_mul_i32 s1, s0, 0xc000
	s_add_u32 s72, s52, s1
	s_addc_u32 s73, s53, 0
	s_add_u32 s72, s72, 0xa000
	s_addc_u32 s73, s73, 0
	s_add_u32 s74, s72, 0x1000
	s_addc_u32 s75, s73, 0
	global_load_dwordx4 v[68:71], v1, s[72:73]
	global_load_dwordx4 v[72:75], v1, s[72:73] offset:1024
	global_load_dwordx4 v[76:79], v1, s[72:73] offset:2048
	global_load_dwordx4 v[80:83], v1, s[72:73] offset:3072
	global_load_dwordx4 v[84:87], v1, s[74:75]
	global_load_dwordx4 v[88:91], v1, s[74:75] offset:1024
	global_load_dwordx4 v[92:95], v1, s[74:75] offset:2048
	global_load_dwordx4 v[96:99], v1, s[74:75] offset:3072
	s_waitcnt vmcnt(24)
	v_cmp_le_i32_e64 s[0:1], 0, v235
	s_nop 1
	s_and_b32 s45, s0, 0xffff
	s_cmpk_lt_u32 s43, 0x100
	s_cselect_b32 s45, 0, s45
	s_mov_b32 s47, 0
	s_mov_b32 s61, 0
	s_cmp_eq_u32 s45, 0
	s_cbranch_scc1 .Ln2_y0_5
	s_mov_b32 s47, 1
	s_ff1_i32_b32 s0, s45
	s_add_i32 s1, s45, -1
	s_and_b32 s45, s45, s1
	s_nop 0
	v_readlane_b32 s0, v235, s0
	s_nop 3
	s_lshl_b32 s0, s0, 12
	s_add_u32 s76, s64, s0
	s_addc_u32 s77, s65, 0
	global_load_dwordx2 v[196:197], v2, s[76:77]
	global_load_dwordx2 v[198:199], v2, s[76:77] offset:512
	global_load_dwordx2 v[200:201], v2, s[76:77] offset:1024
	global_load_dwordx2 v[202:203], v2, s[76:77] offset:1536
	global_load_dwordx2 v[204:205], v2, s[76:77] offset:2048
	global_load_dwordx2 v[206:207], v2, s[76:77] offset:2560
	global_load_dwordx2 v[208:209], v2, s[76:77] offset:3072
	global_load_dwordx2 v[210:211], v2, s[76:77] offset:3584
	s_cmp_eq_u32 s45, 0
	s_cbranch_scc1 .Ln2_y0_5
	s_mov_b32 s61, 1
	s_ff1_i32_b32 s0, s45
	s_add_i32 s1, s45, -1
	s_and_b32 s45, s45, s1
	s_nop 0
	v_readlane_b32 s0, v235, s0
	s_nop 3
	s_lshl_b32 s0, s0, 12
	s_add_u32 s76, s64, s0
	s_addc_u32 s77, s65, 0
	global_load_dwordx2 v[212:213], v2, s[76:77]
	global_load_dwordx2 v[214:215], v2, s[76:77] offset:512
	global_load_dwordx2 v[216:217], v2, s[76:77] offset:1024
	global_load_dwordx2 v[218:219], v2, s[76:77] offset:1536
	global_load_dwordx2 v[226:227], v2, s[76:77] offset:2048
	global_load_dwordx2 v[228:229], v2, s[76:77] offset:2560
	global_load_dwordx2 v[230:231], v2, s[76:77] offset:3072
	global_load_dwordx2 v[232:233], v2, s[76:77] offset:3584

.Ln2_gd_5:
	global_store_dwordx4 v1, v[36:39], s[16:17]
	global_store_dwordx4 v1, v[40:43], s[16:17] offset:1024
	global_store_dwordx4 v1, v[44:47], s[16:17] offset:2048
	global_store_dwordx4 v1, v[48:51], s[16:17] offset:3072
	global_store_dwordx4 v1, v[52:55], s[18:19]
	global_store_dwordx4 v1, v[56:59], s[18:19] offset:1024
	global_store_dwordx4 v1, v[60:63], s[18:19] offset:2048
	global_store_dwordx4 v1, v[64:67], s[18:19] offset:3072
	s_add_i32 s11, s10, 0x3000
	s_lshr_b32 s0, s11, 8
	s_mul_i32 s0, s0, 57
	s_lshr_b32 s44, s0, 9
	s_mul_i32 s1, s44, 0x900
	s_sub_i32 s43, s11, s1
	s_lshl_b32 s0, s44, 11
	s_add_i32 s0, s0, s43
	s_add_i32 s0, s0, 0xffffff00
	s_lshl_b32 s0, s0, 13
	s_lshl_b32 s1, s11, 13
	s_cmpk_lt_u32 s43, 0x100
	s_cselect_b32 s0, s1, s0
	s_cselect_b32 s1, s48, s66
	s_cselect_b32 s2, s49, s67
	s_add_u32 s16, s1, s0
	s_addc_u32 s17, s2, 0
	s_add_u32 s18, s16, 0x1000
	s_addc_u32 s19, s17, 0
	s_cmpk_lt_u32 s43, 0x100
	s_cselect_b32 s0, 8, s44
	s_mul_i32 s1, s0, 0xc000
	s_add_u32 s72, s52, s1
	s_addc_u32 s73, s53, 0
	s_add_u32 s72, s72, 0xa000
	s_addc_u32 s73, s73, 0
	s_add_u32 s74, s72, 0x1000
	s_addc_u32 s75, s73, 0
	global_load_dwordx4 v[68:71], v1, s[72:73]
	global_load_dwordx4 v[72:75], v1, s[72:73] offset:1024
	global_load_dwordx4 v[76:79], v1, s[72:73] offset:2048
	global_load_dwordx4 v[80:83], v1, s[72:73] offset:3072
	global_load_dwordx4 v[84:87], v1, s[74:75]
	global_load_dwordx4 v[88:91], v1, s[74:75] offset:1024
	global_load_dwordx4 v[92:95], v1, s[74:75] offset:2048
	global_load_dwordx4 v[96:99], v1, s[74:75] offset:3072
	s_waitcnt vmcnt(24)
	v_cmp_le_i32_e64 s[0:1], 0, v234
	s_nop 1
	s_and_b32 s45, s0, 0xffff
	s_cmpk_lt_u32 s43, 0x100
	s_cselect_b32 s45, 0, s45
	s_mov_b32 s47, 0
	s_mov_b32 s61, 0
	s_cmp_eq_u32 s45, 0
	s_cbranch_scc1 .Ln2_y0_6
	s_mov_b32 s47, 1
	s_ff1_i32_b32 s0, s45
	s_add_i32 s1, s45, -1
	s_and_b32 s45, s45, s1
	s_nop 0
	v_readlane_b32 s0, v234, s0
	s_nop 3
	s_lshl_b32 s0, s0, 12
	s_add_u32 s76, s64, s0
	s_addc_u32 s77, s65, 0
	global_load_dwordx2 v[196:197], v2, s[76:77]
	global_load_dwordx2 v[198:199], v2, s[76:77] offset:512
	global_load_dwordx2 v[200:201], v2, s[76:77] offset:1024
	global_load_dwordx2 v[202:203], v2, s[76:77] offset:1536
	global_load_dwordx2 v[204:205], v2, s[76:77] offset:2048
	global_load_dwordx2 v[206:207], v2, s[76:77] offset:2560
	global_load_dwordx2 v[208:209], v2, s[76:77] offset:3072
	global_load_dwordx2 v[210:211], v2, s[76:77] offset:3584
	s_cmp_eq_u32 s45, 0
	s_cbranch_scc1 .Ln2_y0_6
	s_mov_b32 s61, 1
	s_ff1_i32_b32 s0, s45
	s_add_i32 s1, s45, -1
	s_and_b32 s45, s45, s1
	s_nop 0
	v_readlane_b32 s0, v234, s0
	s_nop 3
	s_lshl_b32 s0, s0, 12
	s_add_u32 s76, s64, s0
	s_addc_u32 s77, s65, 0
	global_load_dwordx2 v[212:213], v2, s[76:77]
	global_load_dwordx2 v[214:215], v2, s[76:77] offset:512
	global_load_dwordx2 v[216:217], v2, s[76:77] offset:1024
	global_load_dwordx2 v[218:219], v2, s[76:77] offset:1536
	global_load_dwordx2 v[226:227], v2, s[76:77] offset:2048
	global_load_dwordx2 v[228:229], v2, s[76:77] offset:2560
	global_load_dwordx2 v[230:231], v2, s[76:77] offset:3072
	global_load_dwordx2 v[232:233], v2, s[76:77] offset:3584

.Ln2_gd_6:
	global_store_dwordx4 v1, v[4:7], s[16:17]
	global_store_dwordx4 v1, v[8:11], s[16:17] offset:1024
	global_store_dwordx4 v1, v[12:15], s[16:17] offset:2048
	global_store_dwordx4 v1, v[16:19], s[16:17] offset:3072
	global_store_dwordx4 v1, v[20:23], s[18:19]
	global_store_dwordx4 v1, v[24:27], s[18:19] offset:1024
	global_store_dwordx4 v1, v[28:31], s[18:19] offset:2048
	global_store_dwordx4 v1, v[32:35], s[18:19] offset:3072
	s_add_i32 s11, s10, 0x3800
	s_lshr_b32 s0, s11, 8
	s_mul_i32 s0, s0, 57
	s_lshr_b32 s44, s0, 9
	s_mul_i32 s1, s44, 0x900
	s_sub_i32 s43, s11, s1
	s_lshl_b32 s0, s44, 11
	s_add_i32 s0, s0, s43
	s_add_i32 s0, s0, 0xffffff00
	s_lshl_b32 s0, s0, 13
	s_lshl_b32 s1, s11, 13
	s_cmpk_lt_u32 s43, 0x100
	s_cselect_b32 s0, s1, s0
	s_cselect_b32 s1, s48, s66
	s_cselect_b32 s2, s49, s67
	s_add_u32 s16, s1, s0
	s_addc_u32 s17, s2, 0
	s_add_u32 s18, s16, 0x1000
	s_addc_u32 s19, s17, 0
	s_cmpk_lt_u32 s43, 0x100
	s_cselect_b32 s0, 8, s44
	s_mul_i32 s1, s0, 0xc000
	s_add_u32 s72, s52, s1
	s_addc_u32 s73, s53, 0
	s_add_u32 s72, s72, 0xa000
	s_addc_u32 s73, s73, 0
	s_add_u32 s74, s72, 0x1000
	s_addc_u32 s75, s73, 0
	global_load_dwordx4 v[68:71], v1, s[72:73]
	global_load_dwordx4 v[72:75], v1, s[72:73] offset:1024
	global_load_dwordx4 v[76:79], v1, s[72:73] offset:2048
	global_load_dwordx4 v[80:83], v1, s[72:73] offset:3072
	global_load_dwordx4 v[84:87], v1, s[74:75]
	global_load_dwordx4 v[88:91], v1, s[74:75] offset:1024
	global_load_dwordx4 v[92:95], v1, s[74:75] offset:2048
	global_load_dwordx4 v[96:99], v1, s[74:75] offset:3072
	s_waitcnt vmcnt(24)
	v_cmp_le_i32_e64 s[0:1], 0, v235
	s_nop 1
	s_and_b32 s45, s0, 0xffff
	s_cmpk_lt_u32 s43, 0x100
	s_cselect_b32 s45, 0, s45
	s_mov_b32 s47, 0
	s_mov_b32 s61, 0
	s_cmp_eq_u32 s45, 0
	s_cbranch_scc1 .Ln2_y0_7
	s_mov_b32 s47, 1
	s_ff1_i32_b32 s0, s45
	s_add_i32 s1, s45, -1
	s_and_b32 s45, s45, s1
	s_nop 0
	v_readlane_b32 s0, v235, s0
	s_nop 3
	s_lshl_b32 s0, s0, 12
	s_add_u32 s76, s64, s0
	s_addc_u32 s77, s65, 0
	global_load_dwordx2 v[196:197], v2, s[76:77]
	global_load_dwordx2 v[198:199], v2, s[76:77] offset:512
	global_load_dwordx2 v[200:201], v2, s[76:77] offset:1024
	global_load_dwordx2 v[202:203], v2, s[76:77] offset:1536
	global_load_dwordx2 v[204:205], v2, s[76:77] offset:2048
	global_load_dwordx2 v[206:207], v2, s[76:77] offset:2560
	global_load_dwordx2 v[208:209], v2, s[76:77] offset:3072
	global_load_dwordx2 v[210:211], v2, s[76:77] offset:3584
	s_cmp_eq_u32 s45, 0
	s_cbranch_scc1 .Ln2_y0_7
	s_mov_b32 s61, 1
	s_ff1_i32_b32 s0, s45
	s_add_i32 s1, s45, -1
	s_and_b32 s45, s45, s1
	s_nop 0
	v_readlane_b32 s0, v235, s0
	s_nop 3
	s_lshl_b32 s0, s0, 12
	s_add_u32 s76, s64, s0
	s_addc_u32 s77, s65, 0
	global_load_dwordx2 v[212:213], v2, s[76:77]
	global_load_dwordx2 v[214:215], v2, s[76:77] offset:512
	global_load_dwordx2 v[216:217], v2, s[76:77] offset:1024
	global_load_dwordx2 v[218:219], v2, s[76:77] offset:1536
	global_load_dwordx2 v[226:227], v2, s[76:77] offset:2048
	global_load_dwordx2 v[228:229], v2, s[76:77] offset:2560
	global_load_dwordx2 v[230:231], v2, s[76:77] offset:3072
	global_load_dwordx2 v[232:233], v2, s[76:77] offset:3584

.Ln2_gd_7:
	global_store_dwordx4 v1, v[36:39], s[16:17]
	global_store_dwordx4 v1, v[40:43], s[16:17] offset:1024
	global_store_dwordx4 v1, v[44:47], s[16:17] offset:2048
	global_store_dwordx4 v1, v[48:51], s[16:17] offset:3072
	global_store_dwordx4 v1, v[52:55], s[18:19]
	global_store_dwordx4 v1, v[56:59], s[18:19] offset:1024
	global_store_dwordx4 v1, v[60:63], s[18:19] offset:2048
	global_store_dwordx4 v1, v[64:67], s[18:19] offset:3072
	s_add_i32 s11, s10, 0x4000
	s_lshr_b32 s0, s11, 8
	s_mul_i32 s0, s0, 57
	s_lshr_b32 s44, s0, 9
	s_mul_i32 s1, s44, 0x900
	s_sub_i32 s43, s11, s1
	s_lshl_b32 s0, s44, 11
	s_add_i32 s0, s0, s43
	s_add_i32 s0, s0, 0xffffff00
	s_lshl_b32 s0, s0, 13
	s_lshl_b32 s1, s11, 13
	s_cmpk_lt_u32 s43, 0x100
	s_cselect_b32 s0, s1, s0
	s_cselect_b32 s1, s48, s66
	s_cselect_b32 s2, s49, s67
	s_add_u32 s16, s1, s0
	s_addc_u32 s17, s2, 0
	s_add_u32 s18, s16, 0x1000
	s_addc_u32 s19, s17, 0
	s_cmpk_lt_u32 s43, 0x100
	s_cselect_b32 s0, 8, s44
	s_mul_i32 s1, s0, 0xc000
	s_add_u32 s72, s52, s1
	s_addc_u32 s73, s53, 0
	s_add_u32 s72, s72, 0xa000
	s_addc_u32 s73, s73, 0
	s_add_u32 s74, s72, 0x1000
	s_addc_u32 s75, s73, 0
	global_load_dwordx4 v[68:71], v1, s[72:73]
	global_load_dwordx4 v[72:75], v1, s[72:73] offset:1024
	global_load_dwordx4 v[76:79], v1, s[72:73] offset:2048
	global_load_dwordx4 v[80:83], v1, s[72:73] offset:3072
	global_load_dwordx4 v[84:87], v1, s[74:75]
	global_load_dwordx4 v[88:91], v1, s[74:75] offset:1024
	global_load_dwordx4 v[92:95], v1, s[74:75] offset:2048
	global_load_dwordx4 v[96:99], v1, s[74:75] offset:3072
	s_waitcnt vmcnt(24)
	v_cmp_le_i32_e64 s[0:1], 0, v234
	s_nop 1
	s_and_b32 s45, s0, 0xffff
	s_cmpk_lt_u32 s43, 0x100
	s_cselect_b32 s45, 0, s45
	s_mov_b32 s47, 0
	s_mov_b32 s61, 0
	s_cmp_eq_u32 s45, 0
	s_cbranch_scc1 .Ln2_y0_8
	s_mov_b32 s47, 1
	s_ff1_i32_b32 s0, s45
	s_add_i32 s1, s45, -1
	s_and_b32 s45, s45, s1
	s_nop 0
	v_readlane_b32 s0, v234, s0
	s_nop 3
	s_lshl_b32 s0, s0, 12
	s_add_u32 s76, s64, s0
	s_addc_u32 s77, s65, 0
	global_load_dwordx2 v[196:197], v2, s[76:77]
	global_load_dwordx2 v[198:199], v2, s[76:77] offset:512
	global_load_dwordx2 v[200:201], v2, s[76:77] offset:1024
	global_load_dwordx2 v[202:203], v2, s[76:77] offset:1536
	global_load_dwordx2 v[204:205], v2, s[76:77] offset:2048
	global_load_dwordx2 v[206:207], v2, s[76:77] offset:2560
	global_load_dwordx2 v[208:209], v2, s[76:77] offset:3072
	global_load_dwordx2 v[210:211], v2, s[76:77] offset:3584
	s_cmp_eq_u32 s45, 0
	s_cbranch_scc1 .Ln2_y0_8
	s_mov_b32 s61, 1
	s_ff1_i32_b32 s0, s45
	s_add_i32 s1, s45, -1
	s_and_b32 s45, s45, s1
	s_nop 0
	v_readlane_b32 s0, v234, s0
	s_nop 3
	s_lshl_b32 s0, s0, 12
	s_add_u32 s76, s64, s0
	s_addc_u32 s77, s65, 0
	global_load_dwordx2 v[212:213], v2, s[76:77]
	global_load_dwordx2 v[214:215], v2, s[76:77] offset:512
	global_load_dwordx2 v[216:217], v2, s[76:77] offset:1024
	global_load_dwordx2 v[218:219], v2, s[76:77] offset:1536
	global_load_dwordx2 v[226:227], v2, s[76:77] offset:2048
	global_load_dwordx2 v[228:229], v2, s[76:77] offset:2560
	global_load_dwordx2 v[230:231], v2, s[76:77] offset:3072
	global_load_dwordx2 v[232:233], v2, s[76:77] offset:3584

.Ln2_gd_8:
	global_store_dwordx4 v1, v[4:7], s[16:17]
	global_store_dwordx4 v1, v[8:11], s[16:17] offset:1024
	global_store_dwordx4 v1, v[12:15], s[16:17] offset:2048
	global_store_dwordx4 v1, v[16:19], s[16:17] offset:3072
	global_store_dwordx4 v1, v[20:23], s[18:19]
	global_store_dwordx4 v1, v[24:27], s[18:19] offset:1024
	global_store_dwordx4 v1, v[28:31], s[18:19] offset:2048
	global_store_dwordx4 v1, v[32:35], s[18:19] offset:3072
